# GEMM phases: the store-drain wait before each tile's K-loop removed and the first iteration's two staging waits skipped after an epilogue, so the previous tile's stores drain under the first MFMA bloc
# baseline (speedup 1.0000x reference)
_Z10fwd_kernel4Args:
	s_mov_b64 s[100:101], 0
	v_lshl_add_u32 v1, v0, 2, 0
	v_add_u32_e32 v1, 0x20000, v1
	v_mov_b32_e32 v2, 0
	s_mov_b32 s96, s2
	ds_write2st64_b32 v1, v2, v2 offset1:8
	ds_write2st64_b32 v1, v2, v2 offset0:16 offset1:24
	v_or_b32_e32 v1, 0x800, v0
	s_mov_b64 s[4:5], -1
	s_and_saveexec_b64 s[6:7], s[4:5]
	v_lshl_add_u32 v3, v1, 2, 0
	v_add_u32_e32 v3, 0x20000, v3
	ds_write_b32 v3, v2
	s_or_b64 exec, exec, s[6:7]
	s_and_saveexec_b64 s[6:7], s[4:5]
	s_add_i32 s2, 0, 0x20000
	v_lshl_add_u32 v1, v1, 2, s2
	v_mov_b32_e32 v2, 0
	ds_write_b32 v1, v2 offset:2048
	s_or_b64 exec, exec, s[6:7]
	v_or_b32_e32 v1, 0xc00, v0
	v_cmp_gt_u32_e64 s[4:5], 7, 6
	v_cmp_gt_u32_e64 s[2:3], 7, 5
	s_and_saveexec_b64 s[6:7], s[2:3]
	v_lshl_add_u32 v2, v1, 2, 0
	v_add_u32_e32 v2, 0x20000, v2
	v_mov_b32_e32 v3, 0
	ds_write_b32 v2, v3
	s_or_b64 exec, exec, s[6:7]
	s_load_dwordx2 s[92:93], s[0:1], 0xf8
	s_load_dwordx4 s[52:55], s[0:1], 0xe8
	s_and_saveexec_b64 s[6:7], s[4:5]
	s_add_i32 s2, 0, 0x20000
	v_lshl_add_u32 v1, v1, 2, s2
	v_mov_b32_e32 v2, 0
	ds_write_b32 v1, v2 offset:2048
	s_or_b64 exec, exec, s[6:7]
	s_waitcnt lgkmcnt(0)
	s_barrier
	s_add_u32 s8, s54, 0x4000
	s_getreg_b32 s2, hwreg(HW_REG_XCC_ID, 0, 4)
	s_addc_u32 s9, s55, 0
	s_and_b32 s2, s2, 15
	v_cmp_eq_u32_e64 s[6:7], 0, v0
	s_mov_b64 s[4:5], exec
	s_nop 0
	v_writelane_b32 v251, s6, 0
	s_nop 1
	v_writelane_b32 v251, s7, 1
	s_and_b64 s[6:7], s[4:5], s[6:7]
	s_mov_b64 exec, s[6:7]
	s_cbranch_execz .LBB0_11
	s_mov_b64 s[6:7], exec
	v_mbcnt_lo_u32_b32 v1, s6, 0
	v_mbcnt_hi_u32_b32 v1, s7, v1
	v_cmp_eq_u32_e32 vcc, 0, v1
	s_and_b64 s[10:11], exec, vcc
	s_mov_b64 exec, s[10:11]
	s_cbranch_execz .LBB0_11
	s_lshl_b32 s3, s2, 8
	s_bcnt1_i32_b64 s6, s[6:7]
	v_mov_b32_e32 v1, s3
	v_mov_b32_e32 v2, s6
	global_atomic_add v1, v2, s[8:9] offset:1024

.LBB0_214:
	s_mov_b64 s[100:101], 0
	s_cmp_le_i32 s92, s2
	s_cselect_b64 s[4:5], -1, 0
	s_cmp_lt_i32 s2, s93
	s_cselect_b64 s[6:7], -1, 0
	s_and_b64 s[6:7], s[4:5], s[6:7]
	s_mov_b64 s[4:5], -1
	s_and_b64 vcc, exec, s[6:7]
	s_cbranch_vccnz .LBB0_216
	v_readlane_b32 s2, v255, 4
	s_add_i32 s2, s2, 4
	s_mov_b64 s[4:5], 0

.LBB0_225:
	s_ashr_i32 s43, s42, 31
	s_lshl_b64 s[44:45], s[42:43], 19
	s_add_u32 s44, s12, s44
	s_addc_u32 s45, s13, s45
	s_and_b64 s[46:47], s[40:41], exec
	v_lshl_add_u32 v2, s56, 19, v239
	s_cselect_b32 s43, s45, s11
	s_cselect_b32 s59, s44, s10
	v_add_u32_e32 v245, v2, v238
	v_add_u32_e32 v246, v2, v240
	v_add_u32_e32 v212, v2, v241
	v_add_u32_e32 v214, v2, v242
	s_add_u32 s60, s10, 0x100
	v_mov_b32_e32 v2, 0
	v_mov_b32_e32 v213, v99
	v_mov_b32_e32 v215, v99
	s_addc_u32 s61, s11, 0
	s_mov_b32 s65, -2
	s_mov_b64 s[10:11], 0
	v_mov_b32_e32 v3, v2
	v_mov_b32_e32 v4, v2
	v_mov_b32_e32 v5, v2
	v_mov_b32_e32 v6, v2
	v_mov_b32_e32 v7, v2
	v_mov_b32_e32 v8, v2
	v_mov_b32_e32 v9, v2
	v_mov_b32_e32 v18, v2
	v_mov_b32_e32 v19, v2
	v_mov_b32_e32 v20, v2
	v_mov_b32_e32 v21, v2
	v_mov_b32_e32 v22, v2
	v_mov_b32_e32 v23, v2
	v_mov_b32_e32 v24, v2
	v_mov_b32_e32 v25, v2
	v_mov_b32_e32 v34, v2
	v_mov_b32_e32 v35, v2
	v_mov_b32_e32 v36, v2
	v_mov_b32_e32 v37, v2
	v_mov_b32_e32 v38, v2
	v_mov_b32_e32 v39, v2
	v_mov_b32_e32 v40, v2
	v_mov_b32_e32 v41, v2
	v_mov_b32_e32 v50, v2
	v_mov_b32_e32 v51, v2
	v_mov_b32_e32 v52, v2
	v_mov_b32_e32 v53, v2
	v_mov_b32_e32 v54, v2
	v_mov_b32_e32 v55, v2
	v_mov_b32_e32 v56, v2
	v_mov_b32_e32 v57, v2
	v_mov_b32_e32 v10, v2
	v_mov_b32_e32 v11, v2
	v_mov_b32_e32 v12, v2
	v_mov_b32_e32 v13, v2
	v_mov_b32_e32 v14, v2
	v_mov_b32_e32 v15, v2
	v_mov_b32_e32 v16, v2
	v_mov_b32_e32 v17, v2
	v_mov_b32_e32 v26, v2
	v_mov_b32_e32 v27, v2
	v_mov_b32_e32 v28, v2
	v_mov_b32_e32 v29, v2
	v_mov_b32_e32 v30, v2
	v_mov_b32_e32 v31, v2
	v_mov_b32_e32 v32, v2
	v_mov_b32_e32 v33, v2
	v_mov_b32_e32 v42, v2
	v_mov_b32_e32 v43, v2
	v_mov_b32_e32 v44, v2
	v_mov_b32_e32 v45, v2
	v_mov_b32_e32 v46, v2
	v_mov_b32_e32 v47, v2
	v_mov_b32_e32 v48, v2
	v_mov_b32_e32 v49, v2
	v_mov_b32_e32 v58, v2
	v_mov_b32_e32 v59, v2
	v_mov_b32_e32 v60, v2
	v_mov_b32_e32 v61, v2
	v_mov_b32_e32 v62, v2
	v_mov_b32_e32 v63, v2
	v_mov_b32_e32 v64, v2
	v_mov_b32_e32 v65, v2
	v_mov_b32_e32 v66, v2
	v_mov_b32_e32 v67, v2
	v_mov_b32_e32 v68, v2
	v_mov_b32_e32 v69, v2
	v_mov_b32_e32 v70, v2
	v_mov_b32_e32 v71, v2
	v_mov_b32_e32 v72, v2
	v_mov_b32_e32 v73, v2
	v_mov_b32_e32 v90, v2
	v_mov_b32_e32 v91, v2
	v_mov_b32_e32 v92, v2
	v_mov_b32_e32 v93, v2
	v_mov_b32_e32 v100, v2
	v_mov_b32_e32 v101, v2
	v_mov_b32_e32 v102, v2
	v_mov_b32_e32 v103, v2
	v_mov_b32_e32 v116, v2
	v_mov_b32_e32 v117, v2
	v_mov_b32_e32 v118, v2
	v_mov_b32_e32 v119, v2
	v_mov_b32_e32 v120, v2
	v_mov_b32_e32 v121, v2
	v_mov_b32_e32 v122, v2
	v_mov_b32_e32 v123, v2
	v_mov_b32_e32 v132, v2
	v_mov_b32_e32 v133, v2
	v_mov_b32_e32 v134, v2
	v_mov_b32_e32 v135, v2
	v_mov_b32_e32 v136, v2
	v_mov_b32_e32 v137, v2
	v_mov_b32_e32 v138, v2
	v_mov_b32_e32 v139, v2
	v_mov_b32_e32 v78, v2
	v_mov_b32_e32 v79, v2
	v_mov_b32_e32 v80, v2
	v_mov_b32_e32 v81, v2
	v_mov_b32_e32 v86, v2
	v_mov_b32_e32 v87, v2
	v_mov_b32_e32 v88, v2
	v_mov_b32_e32 v89, v2
	v_mov_b32_e32 v108, v2
	v_mov_b32_e32 v109, v2
	v_mov_b32_e32 v110, v2
	v_mov_b32_e32 v111, v2
	v_mov_b32_e32 v112, v2
	v_mov_b32_e32 v113, v2
	v_mov_b32_e32 v114, v2
	v_mov_b32_e32 v115, v2
	v_mov_b32_e32 v124, v2
	v_mov_b32_e32 v125, v2
	v_mov_b32_e32 v126, v2
	v_mov_b32_e32 v127, v2
	v_mov_b32_e32 v128, v2
	v_mov_b32_e32 v129, v2
	v_mov_b32_e32 v130, v2
	v_mov_b32_e32 v131, v2
	v_mov_b32_e32 v140, v2
	v_mov_b32_e32 v141, v2
	v_mov_b32_e32 v142, v2
	v_mov_b32_e32 v143, v2
	v_mov_b32_e32 v144, v2
	v_mov_b32_e32 v145, v2
	v_mov_b32_e32 v146, v2
	v_mov_b32_e32 v147, v2
.LBB0_226:
	ds_read_b128 v[148:151], v243
	ds_read_b128 v[152:155], v243 offset:1024
	ds_read_b128 v[156:159], v243 offset:2048
	ds_read_b128 v[160:163], v243 offset:3072
	ds_read_b128 v[74:77], v243 offset:16384
	ds_read_b128 v[82:85], v243 offset:17408
	ds_read_b128 v[94:97], v243 offset:18432
	ds_read_b128 v[104:107], v243 offset:19456
	s_cmp_eq_u32 s65, 12
	s_cselect_b64 s[48:49], -1, 0
	s_add_i32 m0, s17, 0xc000
	s_add_u32 s46, s34, s10
	s_addc_u32 s47, s35, s11
	ds_read_b128 v[188:191], v244
	ds_read_b128 v[192:195], v244 offset:1024
	ds_read_b128 v[180:183], v244 offset:2048
	ds_read_b128 v[184:187], v244 offset:3072
	ds_read_b128 v[172:175], v244 offset:4096
	ds_read_b128 v[176:179], v244 offset:5120
	ds_read_b128 v[164:167], v244 offset:6144
	ds_read_b128 v[168:171], v244 offset:7168
	global_load_lds_dwordx4 v208, s[46:47]
	s_add_i32 m0, s17, 0xe000
	s_nop 0
	global_load_lds_dwordx4 v210, s[46:47]
	s_and_b64 s[46:47], s[40:41], s[48:49]
	s_andn2_b64 vcc, exec, s[46:47]
	s_cbranch_vccnz .LBB0_228
	v_mov_b64_e32 v[216:217], v[214:215]
	v_mov_b64_e32 v[218:219], v[212:213]
	v_mov_b32_e32 v206, v246
	v_mov_b32_e32 v98, v245
	v_mov_b32_e32 v210, v214
	v_mov_b32_e32 v208, v212
	s_branch .LBB0_229

.LBB0_229:
	s_add_u32 s46, s10, 0x100
	s_addc_u32 s47, s11, 0
	s_add_u32 s31, s60, s10
	s_addc_u32 s66, s61, s11
	s_mov_b64 vcc, s[100:101]
	s_cbranch_vccnz .Lepw2
	s_waitcnt vmcnt(8)
.Lepw2:
	s_and_b64 s[10:11], s[48:49], exec
	s_waitcnt lgkmcnt(0)
	s_cselect_b32 s48, 0, s46
	s_cselect_b32 s11, s43, s66
	s_cselect_b32 s10, s59, s31
	s_cselect_b32 s31, 0, s47
	s_add_u32 s48, s76, s48
	s_addc_u32 s49, s77, s31
	s_barrier
	s_setprio 1
	s_waitcnt lgkmcnt(0)
	v_mfma_i32_16x16x64_i8 v[144:147], v[148:151], v[188:191], v[144:147]
	v_mfma_i32_16x16x64_i8 v[140:143], v[156:159], v[188:191], v[140:143]
	v_mfma_i32_16x16x64_i8 v[128:131], v[148:151], v[180:183], v[128:131]
	v_mfma_i32_16x16x64_i8 v[124:127], v[156:159], v[180:183], v[124:127]
	v_mfma_i32_16x16x64_i8 v[112:115], v[148:151], v[172:175], v[112:115]
	v_mfma_i32_16x16x64_i8 v[108:111], v[156:159], v[172:175], v[108:111]
	v_mfma_i32_16x16x64_i8 v[86:89], v[148:151], v[164:167], v[86:89]
	v_mfma_i32_16x16x64_i8 v[78:81], v[156:159], v[164:167], v[78:81]
	v_mfma_i32_16x16x64_i8 v[144:147], v[152:155], v[192:195], v[144:147]
	v_mfma_i32_16x16x64_i8 v[140:143], v[160:163], v[192:195], v[140:143]
	v_mfma_i32_16x16x64_i8 v[128:131], v[152:155], v[184:187], v[128:131]
	v_mfma_i32_16x16x64_i8 v[124:127], v[160:163], v[184:187], v[124:127]
	v_mfma_i32_16x16x64_i8 v[112:115], v[152:155], v[176:179], v[112:115]
	v_mfma_i32_16x16x64_i8 v[108:111], v[160:163], v[176:179], v[108:111]
	v_mfma_i32_16x16x64_i8 v[86:89], v[152:155], v[168:171], v[86:89]
	v_mfma_i32_16x16x64_i8 v[78:81], v[160:163], v[168:171], v[78:81]
	s_setprio 0
	s_setprio 1
	v_mfma_i32_16x16x64_i8 v[136:139], v[74:77], v[188:191], v[136:139]
	v_mfma_i32_16x16x64_i8 v[132:135], v[94:97], v[188:191], v[132:135]
	v_mfma_i32_16x16x64_i8 v[120:123], v[74:77], v[180:183], v[120:123]
	v_mfma_i32_16x16x64_i8 v[116:119], v[94:97], v[180:183], v[116:119]
	v_mfma_i32_16x16x64_i8 v[100:103], v[74:77], v[172:175], v[100:103]
	v_mfma_i32_16x16x64_i8 v[90:93], v[94:97], v[172:175], v[90:93]
	v_mfma_i32_16x16x64_i8 v[70:73], v[74:77], v[164:167], v[70:73]
	v_mfma_i32_16x16x64_i8 v[66:69], v[94:97], v[164:167], v[66:69]
	v_mfma_i32_16x16x64_i8 v[136:139], v[82:85], v[192:195], v[136:139]
	v_mfma_i32_16x16x64_i8 v[132:135], v[104:107], v[192:195], v[132:135]
	v_mfma_i32_16x16x64_i8 v[120:123], v[82:85], v[184:187], v[120:123]
	v_mfma_i32_16x16x64_i8 v[116:119], v[104:107], v[184:187], v[116:119]
	v_mfma_i32_16x16x64_i8 v[100:103], v[82:85], v[176:179], v[100:103]
	v_mfma_i32_16x16x64_i8 v[90:93], v[104:107], v[176:179], v[90:93]
	v_mfma_i32_16x16x64_i8 v[70:73], v[82:85], v[168:171], v[70:73]
	v_mfma_i32_16x16x64_i8 v[66:69], v[104:107], v[168:171], v[66:69]
	s_setprio 0
	s_barrier
	s_mov_b32 m0, s18
	v_lshl_add_u64 v[248:249], s[10:11], 0, v[204:205]
	s_add_u32 s90, s10, 0x40000
	ds_read_b128 v[164:167], v244 offset:16384
	ds_read_b128 v[168:171], v244 offset:17408
	ds_read_b128 v[172:175], v244 offset:18432
	ds_read_b128 v[176:179], v244 offset:19456
	ds_read_b128 v[180:183], v244 offset:20480
	ds_read_b128 v[184:187], v244 offset:21504
	ds_read_b128 v[188:191], v244 offset:22528
	ds_read_b128 v[192:195], v244 offset:23552
	global_load_lds_dwordx4 v[248:249], off
	v_lshl_add_u64 v[228:229], s[10:11], 0, v[202:203]
	s_mov_b32 m0, s19
	s_addc_u32 s91, s11, 0
	global_load_lds_dwordx4 v[228:229], off
	v_lshl_add_u64 v[226:227], s[90:91], 0, v[204:205]
	s_mov_b32 m0, s20
	v_mov_b32_e32 v207, v99
	global_load_lds_dwordx4 v[226:227], off
	v_lshl_add_u64 v[226:227], s[90:91], 0, v[202:203]
	s_mov_b32 m0, s21
	v_lshl_add_u64 v[196:197], s[48:49], 0, v[206:207]
	global_load_lds_dwordx4 v[226:227], off
	s_mov_b32 m0, s17
	v_lshl_add_u64 v[226:227], s[48:49], 0, v[98:99]
	global_load_lds_dwordx4 v98, s[48:49]
	s_mov_b32 m0, s24
	s_nop 0
	global_load_lds_dwordx4 v206, s[48:49]
	s_mov_b64 vcc, s[100:101]
	s_cbranch_vccnz .Lepw1
	s_waitcnt vmcnt(8)
.Lepw1:
	s_waitcnt lgkmcnt(0)
	s_barrier
	s_setprio 1
	s_waitcnt lgkmcnt(0)
	v_mfma_i32_16x16x64_i8 v[62:65], v[148:151], v[164:167], v[62:65]
	v_mfma_i32_16x16x64_i8 v[58:61], v[156:159], v[164:167], v[58:61]
	v_mfma_i32_16x16x64_i8 v[46:49], v[148:151], v[172:175], v[46:49]
	v_mfma_i32_16x16x64_i8 v[42:45], v[156:159], v[172:175], v[42:45]
	v_mfma_i32_16x16x64_i8 v[30:33], v[148:151], v[180:183], v[30:33]
	v_mfma_i32_16x16x64_i8 v[26:29], v[156:159], v[180:183], v[26:29]
	v_mfma_i32_16x16x64_i8 v[14:17], v[148:151], v[188:191], v[14:17]
	v_mfma_i32_16x16x64_i8 v[10:13], v[156:159], v[188:191], v[10:13]
	v_mfma_i32_16x16x64_i8 v[62:65], v[152:155], v[168:171], v[62:65]
	v_mfma_i32_16x16x64_i8 v[58:61], v[160:163], v[168:171], v[58:61]
	v_mfma_i32_16x16x64_i8 v[46:49], v[152:155], v[176:179], v[46:49]
	v_mfma_i32_16x16x64_i8 v[42:45], v[160:163], v[176:179], v[42:45]
	v_mfma_i32_16x16x64_i8 v[30:33], v[152:155], v[184:187], v[30:33]
	v_mfma_i32_16x16x64_i8 v[26:29], v[160:163], v[184:187], v[26:29]
	v_mfma_i32_16x16x64_i8 v[14:17], v[152:155], v[192:195], v[14:17]
	v_mfma_i32_16x16x64_i8 v[10:13], v[160:163], v[192:195], v[10:13]
	s_setprio 0
	s_setprio 1
	v_mfma_i32_16x16x64_i8 v[54:57], v[74:77], v[164:167], v[54:57]
	v_mfma_i32_16x16x64_i8 v[50:53], v[94:97], v[164:167], v[50:53]
	v_mfma_i32_16x16x64_i8 v[38:41], v[74:77], v[172:175], v[38:41]
	v_mfma_i32_16x16x64_i8 v[34:37], v[94:97], v[172:175], v[34:37]
	v_mfma_i32_16x16x64_i8 v[22:25], v[74:77], v[180:183], v[22:25]
	v_mfma_i32_16x16x64_i8 v[18:21], v[94:97], v[180:183], v[18:21]
	v_mfma_i32_16x16x64_i8 v[6:9], v[74:77], v[188:191], v[6:9]
	v_mfma_i32_16x16x64_i8 v[2:5], v[94:97], v[188:191], v[2:5]
	v_mfma_i32_16x16x64_i8 v[54:57], v[82:85], v[168:171], v[54:57]
	v_mfma_i32_16x16x64_i8 v[50:53], v[104:107], v[168:171], v[50:53]
	v_mfma_i32_16x16x64_i8 v[38:41], v[82:85], v[176:179], v[38:41]
	v_mfma_i32_16x16x64_i8 v[34:37], v[104:107], v[176:179], v[34:37]
	v_mfma_i32_16x16x64_i8 v[22:25], v[82:85], v[184:187], v[22:25]
	v_mfma_i32_16x16x64_i8 v[18:21], v[104:107], v[184:187], v[18:21]
	v_mfma_i32_16x16x64_i8 v[6:9], v[82:85], v[192:195], v[6:9]
	v_mfma_i32_16x16x64_i8 v[2:5], v[104:107], v[192:195], v[2:5]
	s_setprio 0
	s_barrier
	ds_read_b128 v[74:77], v243 offset:32768
	ds_read_b128 v[82:85], v243 offset:33792
	ds_read_b128 v[94:97], v243 offset:34816
	ds_read_b128 v[104:107], v243 offset:35840
	ds_read_b128 v[148:151], v243 offset:49152
	ds_read_b128 v[152:155], v243 offset:50176
	ds_read_b128 v[156:159], v243 offset:51200
	ds_read_b128 v[160:163], v243 offset:52224
	s_mov_b32 m0, s27
	v_lshl_add_u64 v[218:219], s[48:49], 0, v[218:219]
	ds_read_b128 v[164:167], v244 offset:32768
	ds_read_b128 v[168:171], v244 offset:33792
	ds_read_b128 v[172:175], v244 offset:34816
	ds_read_b128 v[176:179], v244 offset:35840
	ds_read_b128 v[180:183], v244 offset:36864
	ds_read_b128 v[184:187], v244 offset:37888
	ds_read_b128 v[188:191], v244 offset:38912
	ds_read_b128 v[192:195], v244 offset:39936
	global_load_lds_dwordx4 v[218:219], off
	v_lshl_add_u64 v[216:217], s[48:49], 0, v[216:217]
	s_mov_b32 m0, s28
	s_nop 0
	global_load_lds_dwordx4 v[216:217], off
	s_waitcnt vmcnt(8)
	s_mov_b64 s[100:101], 0
	s_waitcnt lgkmcnt(0)
	s_barrier
	s_setprio 1
	s_waitcnt lgkmcnt(0)
	v_mfma_i32_16x16x64_i8 v[144:147], v[74:77], v[164:167], v[144:147]
	v_mfma_i32_16x16x64_i8 v[140:143], v[94:97], v[164:167], v[140:143]
	v_mfma_i32_16x16x64_i8 v[128:131], v[74:77], v[172:175], v[128:131]
	v_mfma_i32_16x16x64_i8 v[124:127], v[94:97], v[172:175], v[124:127]
	v_mfma_i32_16x16x64_i8 v[112:115], v[74:77], v[180:183], v[112:115]
	v_mfma_i32_16x16x64_i8 v[108:111], v[94:97], v[180:183], v[108:111]
	v_mfma_i32_16x16x64_i8 v[86:89], v[74:77], v[188:191], v[86:89]
	v_mfma_i32_16x16x64_i8 v[78:81], v[94:97], v[188:191], v[78:81]
	v_mfma_i32_16x16x64_i8 v[144:147], v[82:85], v[168:171], v[144:147]
	v_mfma_i32_16x16x64_i8 v[140:143], v[104:107], v[168:171], v[140:143]
	v_mfma_i32_16x16x64_i8 v[128:131], v[82:85], v[176:179], v[128:131]
	v_mfma_i32_16x16x64_i8 v[124:127], v[104:107], v[176:179], v[124:127]
	v_mfma_i32_16x16x64_i8 v[112:115], v[82:85], v[184:187], v[112:115]
	v_mfma_i32_16x16x64_i8 v[108:111], v[104:107], v[184:187], v[108:111]
	v_mfma_i32_16x16x64_i8 v[86:89], v[82:85], v[192:195], v[86:89]
	v_mfma_i32_16x16x64_i8 v[78:81], v[104:107], v[192:195], v[78:81]
	s_setprio 0
	s_setprio 1
	v_mfma_i32_16x16x64_i8 v[136:139], v[148:151], v[164:167], v[136:139]
	v_mfma_i32_16x16x64_i8 v[132:135], v[156:159], v[164:167], v[132:135]
	v_mfma_i32_16x16x64_i8 v[120:123], v[148:151], v[172:175], v[120:123]
	v_mfma_i32_16x16x64_i8 v[116:119], v[156:159], v[172:175], v[116:119]
	v_mfma_i32_16x16x64_i8 v[100:103], v[148:151], v[180:183], v[100:103]
	v_mfma_i32_16x16x64_i8 v[90:93], v[156:159], v[180:183], v[90:93]
	v_mfma_i32_16x16x64_i8 v[70:73], v[148:151], v[188:191], v[70:73]
	v_mfma_i32_16x16x64_i8 v[66:69], v[156:159], v[188:191], v[66:69]
	v_mfma_i32_16x16x64_i8 v[136:139], v[152:155], v[168:171], v[136:139]
	v_mfma_i32_16x16x64_i8 v[132:135], v[160:163], v[168:171], v[132:135]
	v_mfma_i32_16x16x64_i8 v[120:123], v[152:155], v[176:179], v[120:123]
	v_mfma_i32_16x16x64_i8 v[116:119], v[160:163], v[176:179], v[116:119]
	v_mfma_i32_16x16x64_i8 v[100:103], v[152:155], v[184:187], v[100:103]
	v_mfma_i32_16x16x64_i8 v[90:93], v[160:163], v[184:187], v[90:93]
	v_mfma_i32_16x16x64_i8 v[70:73], v[152:155], v[192:195], v[70:73]
	v_mfma_i32_16x16x64_i8 v[66:69], v[160:163], v[192:195], v[66:69]
	s_setprio 0
	s_barrier
	s_mov_b32 m0, s50
	v_lshl_add_u64 v[216:217], v[248:249], 0, s[62:63]
	s_add_u32 s10, s10, 0x40080
	ds_read_b128 v[164:167], v244 offset:49152
	ds_read_b128 v[168:171], v244 offset:50176
	ds_read_b128 v[172:175], v244 offset:51200
	ds_read_b128 v[176:179], v244 offset:52224
	ds_read_b128 v[180:183], v244 offset:53248
	ds_read_b128 v[184:187], v244 offset:54272
	ds_read_b128 v[188:191], v244 offset:55296
	ds_read_b128 v[192:195], v244 offset:56320
	global_load_lds_dwordx4 v[216:217], off
	v_lshl_add_u64 v[216:217], v[228:229], 0, s[62:63]
	s_mov_b32 m0, s51
	s_addc_u32 s11, s11, 0
	global_load_lds_dwordx4 v[216:217], off
	v_lshl_add_u64 v[216:217], s[10:11], 0, v[204:205]
	s_mov_b32 m0, s54
	v_lshl_add_u64 v[196:197], v[196:197], 0, s[62:63]
	global_load_lds_dwordx4 v[216:217], off
	v_lshl_add_u64 v[216:217], s[10:11], 0, v[202:203]
	s_mov_b32 m0, s55
	s_nop 0
	global_load_lds_dwordx4 v[216:217], off
	v_lshl_add_u64 v[216:217], v[226:227], 0, s[62:63]
	s_mov_b32 m0, s52
	s_nop 0
	global_load_lds_dwordx4 v[216:217], off
	s_mov_b32 m0, s53
	s_nop 0
	global_load_lds_dwordx4 v[196:197], off
	s_waitcnt vmcnt(8)
	s_waitcnt lgkmcnt(0)
	s_barrier
	s_setprio 1
	s_waitcnt lgkmcnt(0)
	v_mfma_i32_16x16x64_i8 v[62:65], v[74:77], v[164:167], v[62:65]
	v_mfma_i32_16x16x64_i8 v[58:61], v[94:97], v[164:167], v[58:61]
	v_mfma_i32_16x16x64_i8 v[46:49], v[74:77], v[172:175], v[46:49]
	v_mfma_i32_16x16x64_i8 v[42:45], v[94:97], v[172:175], v[42:45]
	v_mfma_i32_16x16x64_i8 v[30:33], v[74:77], v[180:183], v[30:33]
	v_mfma_i32_16x16x64_i8 v[26:29], v[94:97], v[180:183], v[26:29]
	v_mfma_i32_16x16x64_i8 v[14:17], v[74:77], v[188:191], v[14:17]
	v_mfma_i32_16x16x64_i8 v[10:13], v[94:97], v[188:191], v[10:13]
	v_mfma_i32_16x16x64_i8 v[62:65], v[82:85], v[168:171], v[62:65]
	v_mfma_i32_16x16x64_i8 v[58:61], v[104:107], v[168:171], v[58:61]
	v_mfma_i32_16x16x64_i8 v[46:49], v[82:85], v[176:179], v[46:49]
	v_mfma_i32_16x16x64_i8 v[42:45], v[104:107], v[176:179], v[42:45]
	v_mfma_i32_16x16x64_i8 v[30:33], v[82:85], v[184:187], v[30:33]
	v_mfma_i32_16x16x64_i8 v[26:29], v[104:107], v[184:187], v[26:29]
	v_mfma_i32_16x16x64_i8 v[14:17], v[82:85], v[192:195], v[14:17]
	v_mfma_i32_16x16x64_i8 v[10:13], v[104:107], v[192:195], v[10:13]
	s_setprio 0
	s_setprio 1
	v_mfma_i32_16x16x64_i8 v[54:57], v[148:151], v[164:167], v[54:57]
	v_mfma_i32_16x16x64_i8 v[50:53], v[156:159], v[164:167], v[50:53]
	v_mfma_i32_16x16x64_i8 v[38:41], v[148:151], v[172:175], v[38:41]
	v_mfma_i32_16x16x64_i8 v[34:37], v[156:159], v[172:175], v[34:37]
	v_mfma_i32_16x16x64_i8 v[22:25], v[148:151], v[180:183], v[22:25]
	v_mfma_i32_16x16x64_i8 v[18:21], v[156:159], v[180:183], v[18:21]
	v_mfma_i32_16x16x64_i8 v[6:9], v[148:151], v[188:191], v[6:9]
	v_mfma_i32_16x16x64_i8 v[2:5], v[156:159], v[188:191], v[2:5]
	v_mfma_i32_16x16x64_i8 v[54:57], v[152:155], v[168:171], v[54:57]
	v_mfma_i32_16x16x64_i8 v[50:53], v[160:163], v[168:171], v[50:53]
	v_mfma_i32_16x16x64_i8 v[38:41], v[152:155], v[176:179], v[38:41]
	v_mfma_i32_16x16x64_i8 v[34:37], v[160:163], v[176:179], v[34:37]
	v_mfma_i32_16x16x64_i8 v[22:25], v[152:155], v[184:187], v[22:25]
	v_mfma_i32_16x16x64_i8 v[18:21], v[160:163], v[184:187], v[18:21]
	v_mfma_i32_16x16x64_i8 v[6:9], v[152:155], v[192:195], v[6:9]
	v_mfma_i32_16x16x64_i8 v[2:5], v[160:163], v[192:195], v[2:5]
	s_setprio 0
	s_barrier
	s_add_i32 s65, s65, 2
	s_cmp_gt_u32 s65, 13
	s_cbranch_scc1 .LBB0_231
	s_mov_b64 s[10:11], s[46:47]
	s_branch .LBB0_226

.LBB0_233:
	s_lshl_b32 s10, s58, 8
	s_lshl_b32 s11, s57, 8
	v_mov_b32_e32 v74, v201
	v_mov_b32_e32 v148, v237
	s_add_i32 s10, s10, s29
	s_or_b32 s11, s11, s2
	v_cvt_f32_i32_e32 v145, v145
	v_lshl_add_u32 v154, v74, 3, s11
	v_add_u32_e32 v166, s10, v148
	v_ashrrev_i32_e32 v155, 31, v154
	v_ashrrev_i32_e32 v167, 31, v166
	v_lshl_add_u64 v[82:83], v[154:155], 2, s[6:7]
	v_lshl_add_u64 v[152:153], v[166:167], 2, s[78:79]
	global_load_dwordx4 v[94:97], v[82:83], off offset:16
	global_load_dwordx4 v[104:107], v[82:83], off
	global_load_dwordx4 v[74:77], v[82:83], off offset:528
	s_nop 0
	global_load_dwordx4 v[82:85], v[82:83], off offset:512
	s_nop 0
	global_load_dword v148, v[152:153], off offset:704
	global_load_dword v150, v[152:153], off offset:640
	global_load_dword v156, v[152:153], off offset:576
	global_load_dword v158, v[152:153], off offset:512
	global_load_dword v160, v[152:153], off offset:192
	global_load_dword v162, v[152:153], off offset:128
	global_load_dword v164, v[152:153], off offset:64
	global_load_dword v168, v[152:153], off
	v_cvt_f32_i32_e32 v144, v144
	v_cvt_f32_i32_e32 v147, v147
	v_cvt_f32_i32_e32 v146, v146
	v_cvt_f32_i32_e32 v141, v141
	v_cvt_f32_i32_e32 v140, v140
	v_cvt_f32_i32_e32 v143, v143
	v_cvt_f32_i32_e32 v142, v142
	v_cvt_f32_i32_e32 v137, v137
	v_cvt_f32_i32_e32 v136, v136
	v_cvt_f32_i32_e32 v139, v139
	v_cvt_f32_i32_e32 v138, v138
	v_cvt_f32_i32_e32 v133, v133
	v_cvt_f32_i32_e32 v132, v132
	v_cvt_f32_i32_e32 v135, v135
	v_cvt_f32_i32_e32 v134, v134
	v_mov_b64_e32 v[152:153], s[94:95]
	v_cvt_f32_i32_e32 v129, v129
	v_cvt_f32_i32_e32 v128, v128
	v_cvt_f32_i32_e32 v131, v131
	v_cvt_f32_i32_e32 v130, v130
	v_cvt_f32_i32_e32 v125, v125
	v_cvt_f32_i32_e32 v124, v124
	v_cvt_f32_i32_e32 v127, v127
	v_cvt_f32_i32_e32 v126, v126
	v_add_u32_e32 v165, 16, v166
	v_add_u32_e32 v163, 32, v166
	v_add_u32_e32 v161, 48, v166
	v_add_u32_e32 v159, 0x80, v166
	v_add_u32_e32 v157, 0x90, v166
	v_add_u32_e32 v151, 0xa0, v166
	v_add_u32_e32 v149, 0xb0, v166
	v_mad_i64_i32 v[166:167], s[10:11], v166, s30, v[152:153]
	v_lshlrev_b64 v[154:155], 1, v[154:155]
	v_cvt_f32_i32_e32 v121, v121
	v_cvt_f32_i32_e32 v120, v120
	v_cvt_f32_i32_e32 v123, v123
	v_cvt_f32_i32_e32 v122, v122
	v_cvt_f32_i32_e32 v117, v117
	v_cvt_f32_i32_e32 v116, v116
	v_cvt_f32_i32_e32 v119, v119
	v_cvt_f32_i32_e32 v118, v118
	v_lshl_add_u64 v[166:167], v[166:167], 0, v[154:155]
	v_cvt_f32_i32_e32 v113, v113
	v_cvt_f32_i32_e32 v112, v112
	v_cvt_f32_i32_e32 v115, v115
	v_cvt_f32_i32_e32 v114, v114
	v_cvt_f32_i32_e32 v109, v109
	v_cvt_f32_i32_e32 v108, v108
	v_cvt_f32_i32_e32 v111, v111
	v_cvt_f32_i32_e32 v110, v110
	v_cvt_f32_i32_e32 v101, v101
	v_cvt_f32_i32_e32 v100, v100
	v_cvt_f32_i32_e32 v103, v103
	v_cvt_f32_i32_e32 v102, v102
	v_cvt_f32_i32_e32 v91, v91
	v_cvt_f32_i32_e32 v90, v90
	v_cvt_f32_i32_e32 v93, v93
	v_cvt_f32_i32_e32 v92, v92
	v_cvt_f32_i32_e32 v87, v87
	v_cvt_f32_i32_e32 v86, v86
	v_cvt_f32_i32_e32 v89, v89
	v_cvt_f32_i32_e32 v88, v88
	v_cvt_f32_i32_e32 v79, v79
	v_cvt_f32_i32_e32 v78, v78
	v_cvt_f32_i32_e32 v81, v81
	v_cvt_f32_i32_e32 v80, v80
	v_cvt_f32_i32_e32 v71, v71
	v_cvt_f32_i32_e32 v70, v70
	s_waitcnt vmcnt(0)
	v_pk_mul_f32 v[146:147], v[106:107], v[146:147]
	v_pk_mul_f32 v[144:145], v[104:105], v[144:145]
	v_pk_mul_f32 v[142:143], v[96:97], v[142:143]
	v_pk_mul_f32 v[140:141], v[94:95], v[140:141]
	v_pk_mul_f32 v[146:147], v[146:147], v[168:169] op_sel_hi:[1,0]
	v_pk_mul_f32 v[144:145], v[144:145], v[168:169] op_sel_hi:[1,0]
	v_pk_mul_f32 v[170:171], v[142:143], v[168:169] op_sel_hi:[1,0]
	v_pk_mul_f32 v[142:143], v[140:141], v[168:169] op_sel_hi:[1,0]
	v_cvt_pk_bf16_f32 v140, v144, v145
	v_cvt_pk_bf16_f32 v141, v146, v147
	v_pk_mul_f32 v[138:139], v[84:85], v[138:139]
	v_pk_mul_f32 v[136:137], v[82:83], v[136:137]
	v_pk_mul_f32 v[134:135], v[76:77], v[134:135]
	v_pk_mul_f32 v[132:133], v[74:75], v[132:133]
	v_cvt_pk_bf16_f32 v142, v142, v143
	v_cvt_pk_bf16_f32 v143, v170, v171
	global_store_dwordx4 v[166:167], v[140:143], off
	v_pk_mul_f32 v[138:139], v[138:139], v[168:169] op_sel_hi:[1,0]
	v_pk_mul_f32 v[136:137], v[136:137], v[168:169] op_sel_hi:[1,0]
	v_pk_mul_f32 v[140:141], v[134:135], v[168:169] op_sel_hi:[1,0]
	v_pk_mul_f32 v[134:135], v[132:133], v[168:169] op_sel_hi:[1,0]
	v_cvt_pk_bf16_f32 v132, v136, v137
	v_cvt_pk_bf16_f32 v133, v138, v139
	v_pk_mul_f32 v[130:131], v[106:107], v[130:131]
	v_cvt_pk_bf16_f32 v134, v134, v135
	v_cvt_pk_bf16_f32 v135, v140, v141
	global_store_dwordx4 v[166:167], v[132:135], off offset:256
	v_pk_mul_f32 v[128:129], v[104:105], v[128:129]
	v_pk_mul_f32 v[126:127], v[96:97], v[126:127]
	v_mad_i64_i32 v[132:133], s[10:11], v165, s30, v[152:153]
	v_pk_mul_f32 v[124:125], v[94:95], v[124:125]
	v_lshl_add_u64 v[132:133], v[132:133], 0, v[154:155]
	v_pk_mul_f32 v[130:131], v[130:131], v[164:165] op_sel_hi:[1,0]
	v_pk_mul_f32 v[128:129], v[128:129], v[164:165] op_sel_hi:[1,0]
	v_pk_mul_f32 v[134:135], v[126:127], v[164:165] op_sel_hi:[1,0]
	v_pk_mul_f32 v[126:127], v[124:125], v[164:165] op_sel_hi:[1,0]
	v_cvt_pk_bf16_f32 v124, v128, v129
	v_cvt_pk_bf16_f32 v125, v130, v131
	v_pk_mul_f32 v[122:123], v[84:85], v[122:123]
	v_pk_mul_f32 v[120:121], v[82:83], v[120:121]
	v_pk_mul_f32 v[118:119], v[76:77], v[118:119]
	v_pk_mul_f32 v[116:117], v[74:75], v[116:117]
	v_cvt_pk_bf16_f32 v126, v126, v127
	v_cvt_pk_bf16_f32 v127, v134, v135
	global_store_dwordx4 v[132:133], v[124:127], off
	v_pk_mul_f32 v[122:123], v[122:123], v[164:165] op_sel_hi:[1,0]
	v_pk_mul_f32 v[120:121], v[120:121], v[164:165] op_sel_hi:[1,0]
	v_pk_mul_f32 v[124:125], v[118:119], v[164:165] op_sel_hi:[1,0]
	v_pk_mul_f32 v[118:119], v[116:117], v[164:165] op_sel_hi:[1,0]
	v_cvt_pk_bf16_f32 v116, v120, v121
	v_cvt_pk_bf16_f32 v117, v122, v123
	v_pk_mul_f32 v[114:115], v[106:107], v[114:115]
	v_cvt_pk_bf16_f32 v118, v118, v119
	v_cvt_pk_bf16_f32 v119, v124, v125
	global_store_dwordx4 v[132:133], v[116:119], off offset:256
	v_pk_mul_f32 v[112:113], v[104:105], v[112:113]
	v_pk_mul_f32 v[110:111], v[96:97], v[110:111]
	v_mad_i64_i32 v[116:117], s[10:11], v163, s30, v[152:153]
	v_pk_mul_f32 v[108:109], v[94:95], v[108:109]
	v_cvt_f32_i32_e32 v73, v73
	v_cvt_f32_i32_e32 v72, v72
	v_cvt_f32_i32_e32 v67, v67
	v_cvt_f32_i32_e32 v66, v66
	v_cvt_f32_i32_e32 v69, v69
	v_cvt_f32_i32_e32 v68, v68
	v_lshl_add_u64 v[116:117], v[116:117], 0, v[154:155]
	v_pk_mul_f32 v[114:115], v[114:115], v[162:163] op_sel_hi:[1,0]
	v_pk_mul_f32 v[112:113], v[112:113], v[162:163] op_sel_hi:[1,0]
	v_pk_mul_f32 v[118:119], v[110:111], v[162:163] op_sel_hi:[1,0]
	v_pk_mul_f32 v[110:111], v[108:109], v[162:163] op_sel_hi:[1,0]
	v_cvt_pk_bf16_f32 v108, v112, v113
	v_cvt_pk_bf16_f32 v109, v114, v115
	v_pk_mul_f32 v[102:103], v[84:85], v[102:103]
	v_pk_mul_f32 v[100:101], v[82:83], v[100:101]
	v_pk_mul_f32 v[92:93], v[76:77], v[92:93]
	v_pk_mul_f32 v[90:91], v[74:75], v[90:91]
	v_cvt_pk_bf16_f32 v110, v110, v111
	v_cvt_pk_bf16_f32 v111, v118, v119
	global_store_dwordx4 v[116:117], v[108:111], off
	v_pk_mul_f32 v[102:103], v[102:103], v[162:163] op_sel_hi:[1,0]
	v_pk_mul_f32 v[100:101], v[100:101], v[162:163] op_sel_hi:[1,0]
	v_pk_mul_f32 v[108:109], v[92:93], v[162:163] op_sel_hi:[1,0]
	v_pk_mul_f32 v[92:93], v[90:91], v[162:163] op_sel_hi:[1,0]
	v_cvt_pk_bf16_f32 v90, v100, v101
	v_cvt_pk_bf16_f32 v91, v102, v103
	v_cvt_f32_i32_e32 v63, v63
	v_cvt_f32_i32_e32 v62, v62
	v_cvt_f32_i32_e32 v65, v65
	v_cvt_f32_i32_e32 v64, v64
	v_cvt_f32_i32_e32 v59, v59
	v_cvt_f32_i32_e32 v58, v58
	v_cvt_f32_i32_e32 v61, v61
	v_cvt_f32_i32_e32 v60, v60
	v_cvt_pk_bf16_f32 v92, v92, v93
	v_cvt_pk_bf16_f32 v93, v108, v109
	global_store_dwordx4 v[116:117], v[90:93], off offset:256
	v_pk_mul_f32 v[88:89], v[106:107], v[88:89]
	v_pk_mul_f32 v[86:87], v[104:105], v[86:87]
	v_mad_i64_i32 v[90:91], s[10:11], v161, s30, v[152:153]
	v_pk_mul_f32 v[80:81], v[96:97], v[80:81]
	v_pk_mul_f32 v[78:79], v[94:95], v[78:79]
	v_cvt_f32_i32_e32 v55, v55
	v_cvt_f32_i32_e32 v54, v54
	v_cvt_f32_i32_e32 v57, v57
	v_cvt_f32_i32_e32 v56, v56
	v_cvt_f32_i32_e32 v51, v51
	v_cvt_f32_i32_e32 v50, v50
	v_cvt_f32_i32_e32 v53, v53
	v_cvt_f32_i32_e32 v52, v52
	v_lshl_add_u64 v[90:91], v[90:91], 0, v[154:155]
	v_pk_mul_f32 v[88:89], v[88:89], v[160:161] op_sel_hi:[1,0]
	v_pk_mul_f32 v[86:87], v[86:87], v[160:161] op_sel_hi:[1,0]
	v_pk_mul_f32 v[92:93], v[80:81], v[160:161] op_sel_hi:[1,0]
	v_pk_mul_f32 v[80:81], v[78:79], v[160:161] op_sel_hi:[1,0]
	v_cvt_pk_bf16_f32 v78, v86, v87
	v_cvt_pk_bf16_f32 v79, v88, v89
	v_pk_mul_f32 v[72:73], v[84:85], v[72:73]
	v_pk_mul_f32 v[70:71], v[82:83], v[70:71]
	v_pk_mul_f32 v[68:69], v[76:77], v[68:69]
	v_pk_mul_f32 v[66:67], v[74:75], v[66:67]
	v_cvt_pk_bf16_f32 v80, v80, v81
	v_cvt_pk_bf16_f32 v81, v92, v93
	global_store_dwordx4 v[90:91], v[78:81], off
	v_pk_mul_f32 v[72:73], v[72:73], v[160:161] op_sel_hi:[1,0]
	v_pk_mul_f32 v[70:71], v[70:71], v[160:161] op_sel_hi:[1,0]
	v_pk_mul_f32 v[78:79], v[68:69], v[160:161] op_sel_hi:[1,0]
	v_pk_mul_f32 v[68:69], v[66:67], v[160:161] op_sel_hi:[1,0]
	v_cvt_pk_bf16_f32 v66, v70, v71
	v_cvt_pk_bf16_f32 v67, v72, v73
	v_cvt_f32_i32_e32 v47, v47
	v_cvt_f32_i32_e32 v46, v46
	v_cvt_f32_i32_e32 v49, v49
	v_cvt_f32_i32_e32 v48, v48
	v_cvt_f32_i32_e32 v43, v43
	v_cvt_f32_i32_e32 v42, v42
	v_cvt_f32_i32_e32 v45, v45
	v_cvt_f32_i32_e32 v44, v44
	v_cvt_pk_bf16_f32 v68, v68, v69
	v_cvt_pk_bf16_f32 v69, v78, v79
	global_store_dwordx4 v[90:91], v[66:69], off offset:256
	v_pk_mul_f32 v[64:65], v[106:107], v[64:65]
	v_pk_mul_f32 v[62:63], v[104:105], v[62:63]
	v_mad_i64_i32 v[66:67], s[10:11], v159, s30, v[152:153]
	v_pk_mul_f32 v[60:61], v[96:97], v[60:61]
	v_pk_mul_f32 v[58:59], v[94:95], v[58:59]
	v_cvt_f32_i32_e32 v39, v39
	v_cvt_f32_i32_e32 v38, v38
	v_cvt_f32_i32_e32 v41, v41
	v_cvt_f32_i32_e32 v40, v40
	v_cvt_f32_i32_e32 v35, v35
	v_cvt_f32_i32_e32 v34, v34
	v_cvt_f32_i32_e32 v37, v37
	v_cvt_f32_i32_e32 v36, v36
	v_lshl_add_u64 v[66:67], v[66:67], 0, v[154:155]
	v_pk_mul_f32 v[64:65], v[64:65], v[158:159] op_sel_hi:[1,0]
	v_pk_mul_f32 v[62:63], v[62:63], v[158:159] op_sel_hi:[1,0]
	v_pk_mul_f32 v[68:69], v[60:61], v[158:159] op_sel_hi:[1,0]
	v_pk_mul_f32 v[60:61], v[58:59], v[158:159] op_sel_hi:[1,0]
	v_cvt_pk_bf16_f32 v58, v62, v63
	v_cvt_pk_bf16_f32 v59, v64, v65
	v_pk_mul_f32 v[56:57], v[84:85], v[56:57]
	v_pk_mul_f32 v[54:55], v[82:83], v[54:55]
	v_pk_mul_f32 v[52:53], v[76:77], v[52:53]
	v_pk_mul_f32 v[50:51], v[74:75], v[50:51]
	v_cvt_pk_bf16_f32 v60, v60, v61
	v_cvt_pk_bf16_f32 v61, v68, v69
	global_store_dwordx4 v[66:67], v[58:61], off
	v_pk_mul_f32 v[56:57], v[56:57], v[158:159] op_sel_hi:[1,0]
	v_pk_mul_f32 v[54:55], v[54:55], v[158:159] op_sel_hi:[1,0]
	v_pk_mul_f32 v[58:59], v[52:53], v[158:159] op_sel_hi:[1,0]
	v_pk_mul_f32 v[52:53], v[50:51], v[158:159] op_sel_hi:[1,0]
	v_cvt_pk_bf16_f32 v50, v54, v55
	v_cvt_pk_bf16_f32 v51, v56, v57
	v_cvt_f32_i32_e32 v31, v31
	v_cvt_f32_i32_e32 v30, v30
	v_cvt_f32_i32_e32 v33, v33
	v_cvt_f32_i32_e32 v32, v32
	v_cvt_f32_i32_e32 v27, v27
	v_cvt_f32_i32_e32 v26, v26
	v_cvt_f32_i32_e32 v29, v29
	v_cvt_f32_i32_e32 v28, v28
	v_cvt_pk_bf16_f32 v52, v52, v53
	v_cvt_pk_bf16_f32 v53, v58, v59
	global_store_dwordx4 v[66:67], v[50:53], off offset:256
	v_pk_mul_f32 v[48:49], v[106:107], v[48:49]
	v_pk_mul_f32 v[46:47], v[104:105], v[46:47]
	v_mad_i64_i32 v[50:51], s[10:11], v157, s30, v[152:153]
	v_pk_mul_f32 v[44:45], v[96:97], v[44:45]
	v_pk_mul_f32 v[42:43], v[94:95], v[42:43]
	v_cvt_f32_i32_e32 v23, v23
	v_cvt_f32_i32_e32 v22, v22
	v_cvt_f32_i32_e32 v25, v25
	v_cvt_f32_i32_e32 v24, v24
	v_cvt_f32_i32_e32 v19, v19
	v_cvt_f32_i32_e32 v18, v18
	v_cvt_f32_i32_e32 v21, v21
	v_cvt_f32_i32_e32 v20, v20
	v_lshl_add_u64 v[50:51], v[50:51], 0, v[154:155]
	v_pk_mul_f32 v[48:49], v[48:49], v[156:157] op_sel_hi:[1,0]
	v_pk_mul_f32 v[46:47], v[46:47], v[156:157] op_sel_hi:[1,0]
	v_pk_mul_f32 v[52:53], v[44:45], v[156:157] op_sel_hi:[1,0]
	v_pk_mul_f32 v[44:45], v[42:43], v[156:157] op_sel_hi:[1,0]
	v_cvt_pk_bf16_f32 v42, v46, v47
	v_cvt_pk_bf16_f32 v43, v48, v49
	v_pk_mul_f32 v[40:41], v[84:85], v[40:41]
	v_pk_mul_f32 v[38:39], v[82:83], v[38:39]
	v_pk_mul_f32 v[36:37], v[76:77], v[36:37]
	v_pk_mul_f32 v[34:35], v[74:75], v[34:35]
	v_cvt_pk_bf16_f32 v44, v44, v45
	v_cvt_pk_bf16_f32 v45, v52, v53
	global_store_dwordx4 v[50:51], v[42:45], off
	v_pk_mul_f32 v[40:41], v[40:41], v[156:157] op_sel_hi:[1,0]
	v_pk_mul_f32 v[38:39], v[38:39], v[156:157] op_sel_hi:[1,0]
	v_pk_mul_f32 v[42:43], v[36:37], v[156:157] op_sel_hi:[1,0]
	v_pk_mul_f32 v[36:37], v[34:35], v[156:157] op_sel_hi:[1,0]
	v_cvt_pk_bf16_f32 v34, v38, v39
	v_cvt_pk_bf16_f32 v35, v40, v41
	v_cvt_f32_i32_e32 v15, v15
	v_cvt_f32_i32_e32 v14, v14
	v_cvt_f32_i32_e32 v17, v17
	v_cvt_f32_i32_e32 v16, v16
	v_cvt_f32_i32_e32 v11, v11
	v_cvt_f32_i32_e32 v10, v10
	v_cvt_f32_i32_e32 v13, v13
	v_cvt_f32_i32_e32 v12, v12
	v_cvt_pk_bf16_f32 v36, v36, v37
	v_cvt_pk_bf16_f32 v37, v42, v43
	global_store_dwordx4 v[50:51], v[34:37], off offset:256
	v_pk_mul_f32 v[32:33], v[106:107], v[32:33]
	v_pk_mul_f32 v[30:31], v[104:105], v[30:31]
	v_mad_i64_i32 v[34:35], s[10:11], v151, s30, v[152:153]
	v_pk_mul_f32 v[28:29], v[96:97], v[28:29]
	v_pk_mul_f32 v[26:27], v[94:95], v[26:27]
	v_cvt_f32_i32_e32 v3, v3
	v_cvt_f32_i32_e32 v2, v2
	v_cvt_f32_i32_e32 v5, v5
	v_cvt_f32_i32_e32 v4, v4
	v_lshl_add_u64 v[34:35], v[34:35], 0, v[154:155]
	v_pk_mul_f32 v[32:33], v[32:33], v[150:151] op_sel_hi:[1,0]
	v_pk_mul_f32 v[30:31], v[30:31], v[150:151] op_sel_hi:[1,0]
	v_pk_mul_f32 v[36:37], v[28:29], v[150:151] op_sel_hi:[1,0]
	v_pk_mul_f32 v[28:29], v[26:27], v[150:151] op_sel_hi:[1,0]
	v_cvt_pk_bf16_f32 v26, v30, v31
	v_cvt_pk_bf16_f32 v27, v32, v33
	v_pk_mul_f32 v[24:25], v[84:85], v[24:25]
	v_pk_mul_f32 v[22:23], v[82:83], v[22:23]
	v_pk_mul_f32 v[20:21], v[76:77], v[20:21]
	v_pk_mul_f32 v[18:19], v[74:75], v[18:19]
	v_cvt_f32_i32_e32 v7, v7
	v_cvt_f32_i32_e32 v6, v6
	v_cvt_f32_i32_e32 v9, v9
	v_cvt_f32_i32_e32 v8, v8
	v_cvt_pk_bf16_f32 v28, v28, v29
	v_cvt_pk_bf16_f32 v29, v36, v37
	global_store_dwordx4 v[34:35], v[26:29], off
	v_pk_mul_f32 v[24:25], v[24:25], v[150:151] op_sel_hi:[1,0]
	v_pk_mul_f32 v[22:23], v[22:23], v[150:151] op_sel_hi:[1,0]
	v_pk_mul_f32 v[26:27], v[20:21], v[150:151] op_sel_hi:[1,0]
	v_pk_mul_f32 v[20:21], v[18:19], v[150:151] op_sel_hi:[1,0]
	v_cvt_pk_bf16_f32 v18, v22, v23
	v_cvt_pk_bf16_f32 v19, v24, v25
	v_pk_mul_f32 v[16:17], v[106:107], v[16:17]
	v_cvt_pk_bf16_f32 v20, v20, v21
	v_cvt_pk_bf16_f32 v21, v26, v27
	global_store_dwordx4 v[34:35], v[18:21], off offset:256
	v_pk_mul_f32 v[14:15], v[104:105], v[14:15]
	v_pk_mul_f32 v[12:13], v[96:97], v[12:13]
	v_mad_i64_i32 v[18:19], s[10:11], v149, s30, v[152:153]
	v_pk_mul_f32 v[10:11], v[94:95], v[10:11]
	v_lshl_add_u64 v[18:19], v[18:19], 0, v[154:155]
	v_pk_mul_f32 v[16:17], v[16:17], v[148:149] op_sel_hi:[1,0]
	v_pk_mul_f32 v[14:15], v[14:15], v[148:149] op_sel_hi:[1,0]
	v_pk_mul_f32 v[20:21], v[12:13], v[148:149] op_sel_hi:[1,0]
	v_pk_mul_f32 v[12:13], v[10:11], v[148:149] op_sel_hi:[1,0]
	v_cvt_pk_bf16_f32 v10, v14, v15
	v_cvt_pk_bf16_f32 v11, v16, v17
	v_pk_mul_f32 v[4:5], v[76:77], v[4:5]
	v_pk_mul_f32 v[2:3], v[74:75], v[2:3]
	v_cvt_pk_bf16_f32 v12, v12, v13
	v_cvt_pk_bf16_f32 v13, v20, v21
	global_store_dwordx4 v[18:19], v[10:13], off
	v_pk_mul_f32 v[8:9], v[84:85], v[8:9]
	v_pk_mul_f32 v[6:7], v[82:83], v[6:7]
	v_pk_mul_f32 v[10:11], v[4:5], v[148:149] op_sel_hi:[1,0]
	v_pk_mul_f32 v[4:5], v[2:3], v[148:149] op_sel_hi:[1,0]
	s_mov_b64 s[10:11], -1
	s_andn2_b64 vcc, exec, s[40:41]
	v_readlane_b32 s60, v254, 61
	v_readlane_b32 s59, v254, 62
	s_mov_b64 s[46:47], s[36:37]
	v_readlane_b32 s65, v255, 3
	v_pk_mul_f32 v[8:9], v[8:9], v[148:149] op_sel_hi:[1,0]
	v_pk_mul_f32 v[6:7], v[6:7], v[148:149] op_sel_hi:[1,0]
	s_nop 0
	v_cvt_pk_bf16_f32 v2, v6, v7
	v_cvt_pk_bf16_f32 v3, v8, v9
	v_cvt_pk_bf16_f32 v4, v4, v5
	v_cvt_pk_bf16_f32 v5, v10, v11
	global_store_dwordx4 v[18:19], v[2:5], off offset:256
	s_mov_b64 s[100:101], -1
	s_cbranch_vccnz .LBB0_222
	s_andn2_b64 vcc, exec, s[4:5]
	s_cbranch_vccnz .LBB0_221
	s_barrier
	s_branch .LBB0_221

.LBB0_1035:
	s_mov_b64 s[100:101], 0
	s_cmp_le_i32 s92, s2
	s_cselect_b64 s[4:5], -1, 0
	s_cmp_lt_i32 s2, s93
	s_cselect_b64 s[6:7], -1, 0
	s_and_b64 s[6:7], s[4:5], s[6:7]
	s_mov_b64 s[4:5], -1
	s_and_b64 vcc, exec, s[6:7]
	s_cbranch_vccnz .LBB0_1037
	v_readlane_b32 s2, v255, 4
	s_add_i32 s2, s2, 8
	s_mov_b64 s[4:5], 0

.LBB0_1048:
	ds_read_b128 v[42:45], v174
	ds_read_b128 v[46:49], v174 offset:1024
	ds_read_b128 v[58:61], v174 offset:2048
	ds_read_b128 v[62:65], v174 offset:3072
	ds_read_b128 v[148:151], v174 offset:16384
	ds_read_b128 v[152:155], v174 offset:17408
	ds_read_b128 v[166:169], v174 offset:18432
	ds_read_b128 v[176:179], v174 offset:19456
	s_add_u32 s31, s10, 0xfff80080
	s_addc_u32 s50, s11, -1
	s_cmp_eq_u32 s93, 28
	s_cselect_b32 s53, s45, s50
	s_cselect_b32 s52, s88, s31
	s_cselect_b32 s51, s9, s92
	s_cselect_b32 s50, s90, s91
	v_lshl_add_u64 v[170:171], s[10:11], 0, v[162:163]
	s_add_i32 m0, s17, 0xc000
	ds_read_b128 v[180:183], v175
	ds_read_b128 v[184:187], v175 offset:1024
	ds_read_b128 v[188:191], v175 offset:2048
	ds_read_b128 v[192:195], v175 offset:3072
	ds_read_b128 v[202:205], v175 offset:4096
	ds_read_b128 v[206:209], v175 offset:5120
	ds_read_b128 v[210:213], v175 offset:6144
	ds_read_b128 v[214:217], v175 offset:7168
	global_load_lds_dwordx4 v[170:171], off
	v_lshl_add_u64 v[170:171], s[10:11], 0, v[164:165]
	s_add_i32 m0, s17, 0xe000
	s_nop 0
	global_load_lds_dwordx4 v[170:171], off
	s_mov_b64 vcc, s[100:101]
	s_cbranch_vccnz .Lepw4
	s_waitcnt vmcnt(8)
.Lepw4:
	s_waitcnt lgkmcnt(0)
	s_barrier
	s_setprio 1
	s_waitcnt lgkmcnt(0)
	v_mfma_f32_16x16x32_bf16 v[144:147], v[42:45], v[180:183], v[144:147]
	v_mfma_f32_16x16x32_bf16 v[140:143], v[58:61], v[180:183], v[140:143]
	v_mfma_f32_16x16x32_bf16 v[128:131], v[42:45], v[188:191], v[128:131]
	v_mfma_f32_16x16x32_bf16 v[124:127], v[58:61], v[188:191], v[124:127]
	v_mfma_f32_16x16x32_bf16 v[112:115], v[42:45], v[202:205], v[112:115]
	v_mfma_f32_16x16x32_bf16 v[108:111], v[58:61], v[202:205], v[108:111]
	v_mfma_f32_16x16x32_bf16 v[94:97], v[42:45], v[210:213], v[94:97]
	v_mfma_f32_16x16x32_bf16 v[90:93], v[58:61], v[210:213], v[90:93]
	v_mfma_f32_16x16x32_bf16 v[144:147], v[46:49], v[184:187], v[144:147]
	v_mfma_f32_16x16x32_bf16 v[140:143], v[62:65], v[184:187], v[140:143]
	v_mfma_f32_16x16x32_bf16 v[128:131], v[46:49], v[192:195], v[128:131]
	v_mfma_f32_16x16x32_bf16 v[124:127], v[62:65], v[192:195], v[124:127]
	v_mfma_f32_16x16x32_bf16 v[112:115], v[46:49], v[206:209], v[112:115]
	v_mfma_f32_16x16x32_bf16 v[108:111], v[62:65], v[206:209], v[108:111]
	v_mfma_f32_16x16x32_bf16 v[94:97], v[46:49], v[214:217], v[94:97]
	v_mfma_f32_16x16x32_bf16 v[90:93], v[62:65], v[214:217], v[90:93]
	s_setprio 0
	s_setprio 1
	v_mfma_f32_16x16x32_bf16 v[136:139], v[148:151], v[180:183], v[136:139]
	v_mfma_f32_16x16x32_bf16 v[132:135], v[166:169], v[180:183], v[132:135]
	v_mfma_f32_16x16x32_bf16 v[120:123], v[148:151], v[188:191], v[120:123]
	v_mfma_f32_16x16x32_bf16 v[116:119], v[166:169], v[188:191], v[116:119]
	v_mfma_f32_16x16x32_bf16 v[104:107], v[148:151], v[202:205], v[104:107]
	v_mfma_f32_16x16x32_bf16 v[100:103], v[166:169], v[202:205], v[100:103]
	v_mfma_f32_16x16x32_bf16 v[86:89], v[148:151], v[210:213], v[86:89]
	v_mfma_f32_16x16x32_bf16 v[82:85], v[166:169], v[210:213], v[82:85]
	v_mfma_f32_16x16x32_bf16 v[136:139], v[152:155], v[184:187], v[136:139]
	v_mfma_f32_16x16x32_bf16 v[132:135], v[176:179], v[184:187], v[132:135]
	v_mfma_f32_16x16x32_bf16 v[120:123], v[152:155], v[192:195], v[120:123]
	v_mfma_f32_16x16x32_bf16 v[116:119], v[176:179], v[192:195], v[116:119]
	v_mfma_f32_16x16x32_bf16 v[104:107], v[152:155], v[206:209], v[104:107]
	v_mfma_f32_16x16x32_bf16 v[100:103], v[176:179], v[206:209], v[100:103]
	v_mfma_f32_16x16x32_bf16 v[86:89], v[152:155], v[214:217], v[86:89]
	v_mfma_f32_16x16x32_bf16 v[82:85], v[176:179], v[214:217], v[82:85]
	s_setprio 0
	s_barrier
	s_mov_b32 m0, s18
	v_lshl_add_u64 v[170:171], s[50:51], 0, v[98:99]
	s_add_u32 s94, s50, 0x80000
	ds_read_b128 v[180:183], v175 offset:16384
	ds_read_b128 v[184:187], v175 offset:17408
	ds_read_b128 v[188:191], v175 offset:18432
	ds_read_b128 v[192:195], v175 offset:19456
	ds_read_b128 v[202:205], v175 offset:20480
	ds_read_b128 v[206:209], v175 offset:21504
	ds_read_b128 v[210:213], v175 offset:22528
	ds_read_b128 v[214:217], v175 offset:23552
	global_load_lds_dwordx4 v[170:171], off
	v_lshl_add_u64 v[196:197], s[50:51], 0, v[156:157]
	s_mov_b32 m0, s19
	s_addc_u32 s95, s51, 0
	global_load_lds_dwordx4 v[196:197], off
	v_lshl_add_u64 v[218:219], s[94:95], 0, v[98:99]
	s_mov_b32 m0, s20
	v_lshl_add_u64 v[226:227], s[52:53], 0, v[158:159]
	global_load_lds_dwordx4 v[218:219], off
	v_lshl_add_u64 v[218:219], s[94:95], 0, v[156:157]
	s_mov_b32 m0, s24
	s_nop 0
	global_load_lds_dwordx4 v[218:219], off
	v_lshl_add_u64 v[218:219], s[52:53], 0, v[160:161]
	s_mov_b32 m0, s17
	s_nop 0
	global_load_lds_dwordx4 v[218:219], off
	s_mov_b32 m0, s27
	s_nop 0
	global_load_lds_dwordx4 v[226:227], off
	s_mov_b64 vcc, s[100:101]
	s_cbranch_vccnz .Lepw3
	s_waitcnt vmcnt(8)
.Lepw3:
	s_waitcnt lgkmcnt(0)
	s_barrier
	s_setprio 1
	s_waitcnt lgkmcnt(0)
	v_mfma_f32_16x16x32_bf16 v[78:81], v[42:45], v[180:183], v[78:81]
	v_mfma_f32_16x16x32_bf16 v[74:77], v[58:61], v[180:183], v[74:77]
	v_mfma_f32_16x16x32_bf16 v[54:57], v[42:45], v[188:191], v[54:57]
	v_mfma_f32_16x16x32_bf16 v[50:53], v[58:61], v[188:191], v[50:53]
	v_mfma_f32_16x16x32_bf16 v[30:33], v[42:45], v[202:205], v[30:33]
	v_mfma_f32_16x16x32_bf16 v[26:29], v[58:61], v[202:205], v[26:29]
	v_mfma_f32_16x16x32_bf16 v[14:17], v[42:45], v[210:213], v[14:17]
	v_mfma_f32_16x16x32_bf16 v[10:13], v[58:61], v[210:213], v[10:13]
	v_mfma_f32_16x16x32_bf16 v[78:81], v[46:49], v[184:187], v[78:81]
	v_mfma_f32_16x16x32_bf16 v[74:77], v[62:65], v[184:187], v[74:77]
	v_mfma_f32_16x16x32_bf16 v[54:57], v[46:49], v[192:195], v[54:57]
	v_mfma_f32_16x16x32_bf16 v[50:53], v[62:65], v[192:195], v[50:53]
	v_mfma_f32_16x16x32_bf16 v[30:33], v[46:49], v[206:209], v[30:33]
	v_mfma_f32_16x16x32_bf16 v[26:29], v[62:65], v[206:209], v[26:29]
	v_mfma_f32_16x16x32_bf16 v[14:17], v[46:49], v[214:217], v[14:17]
	v_mfma_f32_16x16x32_bf16 v[10:13], v[62:65], v[214:217], v[10:13]
	s_setprio 0
	s_setprio 1
	v_mfma_f32_16x16x32_bf16 v[38:41], v[148:151], v[188:191], v[38:41]
	v_mfma_f32_16x16x32_bf16 v[34:37], v[166:169], v[188:191], v[34:37]
	v_mfma_f32_16x16x32_bf16 v[22:25], v[148:151], v[202:205], v[22:25]
	v_mfma_f32_16x16x32_bf16 v[18:21], v[166:169], v[202:205], v[18:21]
	v_mfma_f32_16x16x32_bf16 v[6:9], v[148:151], v[210:213], v[6:9]
	v_mfma_f32_16x16x32_bf16 v[2:5], v[166:169], v[210:213], v[2:5]
	v_mfma_f32_16x16x32_bf16 v[42:45], v[148:151], v[180:183], v[70:73]
	v_mfma_f32_16x16x32_bf16 v[46:49], v[166:169], v[180:183], v[66:69]
	v_mfma_f32_16x16x32_bf16 v[38:41], v[152:155], v[192:195], v[38:41]
	v_mfma_f32_16x16x32_bf16 v[34:37], v[176:179], v[192:195], v[34:37]
	v_mfma_f32_16x16x32_bf16 v[22:25], v[152:155], v[206:209], v[22:25]
	v_mfma_f32_16x16x32_bf16 v[18:21], v[176:179], v[206:209], v[18:21]
	v_mfma_f32_16x16x32_bf16 v[6:9], v[152:155], v[214:217], v[6:9]
	v_mfma_f32_16x16x32_bf16 v[2:5], v[176:179], v[214:217], v[2:5]
	v_mfma_f32_16x16x32_bf16 v[42:45], v[152:155], v[184:187], v[42:45]
	v_mfma_f32_16x16x32_bf16 v[46:49], v[176:179], v[184:187], v[46:49]
	s_setprio 0
	s_barrier
	ds_read_b128 v[58:61], v174 offset:32768
	ds_read_b128 v[62:65], v174 offset:33792
	ds_read_b128 v[66:69], v174 offset:34816
	ds_read_b128 v[70:73], v174 offset:35840
	ds_read_b128 v[148:151], v174 offset:49152
	ds_read_b128 v[152:155], v174 offset:50176
	ds_read_b128 v[166:169], v174 offset:51200
	ds_read_b128 v[176:179], v174 offset:52224
	s_add_u32 s52, s52, 0x80000
	s_addc_u32 s53, s53, 0
	s_mov_b32 m0, s28
	v_lshl_add_u64 v[228:229], s[52:53], 0, v[160:161]
	ds_read_b128 v[180:183], v175 offset:32768
	ds_read_b128 v[184:187], v175 offset:33792
	ds_read_b128 v[188:191], v175 offset:34816
	ds_read_b128 v[192:195], v175 offset:35840
	ds_read_b128 v[202:205], v175 offset:36864
	ds_read_b128 v[206:209], v175 offset:37888
	ds_read_b128 v[210:213], v175 offset:38912
	ds_read_b128 v[214:217], v175 offset:39936
	global_load_lds_dwordx4 v[228:229], off
	v_lshl_add_u64 v[228:229], s[52:53], 0, v[158:159]
	s_mov_b32 m0, s29
	s_nop 0
	global_load_lds_dwordx4 v[228:229], off
	s_waitcnt vmcnt(8)
	s_mov_b64 s[100:101], 0
	s_waitcnt lgkmcnt(0)
	s_barrier
	s_setprio 1
	s_waitcnt lgkmcnt(0)
	v_mfma_f32_16x16x32_bf16 v[144:147], v[58:61], v[180:183], v[144:147]
	v_mfma_f32_16x16x32_bf16 v[140:143], v[66:69], v[180:183], v[140:143]
	v_mfma_f32_16x16x32_bf16 v[128:131], v[58:61], v[188:191], v[128:131]
	v_mfma_f32_16x16x32_bf16 v[124:127], v[66:69], v[188:191], v[124:127]
	v_mfma_f32_16x16x32_bf16 v[112:115], v[58:61], v[202:205], v[112:115]
	v_mfma_f32_16x16x32_bf16 v[108:111], v[66:69], v[202:205], v[108:111]
	v_mfma_f32_16x16x32_bf16 v[94:97], v[58:61], v[210:213], v[94:97]
	v_mfma_f32_16x16x32_bf16 v[90:93], v[66:69], v[210:213], v[90:93]
	v_mfma_f32_16x16x32_bf16 v[144:147], v[62:65], v[184:187], v[144:147]
	v_mfma_f32_16x16x32_bf16 v[140:143], v[70:73], v[184:187], v[140:143]
	v_mfma_f32_16x16x32_bf16 v[128:131], v[62:65], v[192:195], v[128:131]
	v_mfma_f32_16x16x32_bf16 v[124:127], v[70:73], v[192:195], v[124:127]
	v_mfma_f32_16x16x32_bf16 v[112:115], v[62:65], v[206:209], v[112:115]
	v_mfma_f32_16x16x32_bf16 v[108:111], v[70:73], v[206:209], v[108:111]
	v_mfma_f32_16x16x32_bf16 v[94:97], v[62:65], v[214:217], v[94:97]
	v_mfma_f32_16x16x32_bf16 v[90:93], v[70:73], v[214:217], v[90:93]
	s_setprio 0
	s_setprio 1
	v_mfma_f32_16x16x32_bf16 v[136:139], v[148:151], v[180:183], v[136:139]
	v_mfma_f32_16x16x32_bf16 v[132:135], v[166:169], v[180:183], v[132:135]
	v_mfma_f32_16x16x32_bf16 v[120:123], v[148:151], v[188:191], v[120:123]
	v_mfma_f32_16x16x32_bf16 v[116:119], v[166:169], v[188:191], v[116:119]
	v_mfma_f32_16x16x32_bf16 v[104:107], v[148:151], v[202:205], v[104:107]
	v_mfma_f32_16x16x32_bf16 v[100:103], v[166:169], v[202:205], v[100:103]
	v_mfma_f32_16x16x32_bf16 v[86:89], v[148:151], v[210:213], v[86:89]
	v_mfma_f32_16x16x32_bf16 v[82:85], v[166:169], v[210:213], v[82:85]
	v_mfma_f32_16x16x32_bf16 v[136:139], v[152:155], v[184:187], v[136:139]
	v_mfma_f32_16x16x32_bf16 v[132:135], v[176:179], v[184:187], v[132:135]
	v_mfma_f32_16x16x32_bf16 v[120:123], v[152:155], v[192:195], v[120:123]
	v_mfma_f32_16x16x32_bf16 v[116:119], v[176:179], v[192:195], v[116:119]
	v_mfma_f32_16x16x32_bf16 v[104:107], v[152:155], v[206:209], v[104:107]
	v_mfma_f32_16x16x32_bf16 v[100:103], v[176:179], v[206:209], v[100:103]
	v_mfma_f32_16x16x32_bf16 v[86:89], v[152:155], v[214:217], v[86:89]
	v_mfma_f32_16x16x32_bf16 v[82:85], v[176:179], v[214:217], v[82:85]
	s_setprio 0
	s_barrier
	s_mov_b32 m0, s55
	v_lshl_add_u64 v[170:171], v[170:171], 0, s[62:63]
	s_add_u32 s50, s50, 0x80080
	ds_read_b128 v[180:183], v175 offset:49152
	ds_read_b128 v[184:187], v175 offset:50176
	ds_read_b128 v[188:191], v175 offset:51200
	ds_read_b128 v[192:195], v175 offset:52224
	ds_read_b128 v[202:205], v175 offset:53248
	ds_read_b128 v[206:209], v175 offset:54272
	ds_read_b128 v[210:213], v175 offset:55296
	ds_read_b128 v[214:217], v175 offset:56320
	global_load_lds_dwordx4 v[170:171], off
	v_lshl_add_u64 v[170:171], v[196:197], 0, s[62:63]
	s_mov_b32 m0, s56
	s_addc_u32 s51, s51, 0
	global_load_lds_dwordx4 v[170:171], off
	v_lshl_add_u64 v[170:171], s[50:51], 0, v[98:99]
	s_mov_b32 m0, s65
	s_nop 0
	global_load_lds_dwordx4 v[170:171], off
	v_lshl_add_u64 v[170:171], s[50:51], 0, v[156:157]
	s_mov_b32 m0, s66
	s_nop 0
	global_load_lds_dwordx4 v[170:171], off
	v_lshl_add_u64 v[170:171], v[218:219], 0, s[62:63]
	s_mov_b32 m0, s57
	s_nop 0
	global_load_lds_dwordx4 v[170:171], off
	v_lshl_add_u64 v[170:171], v[226:227], 0, s[62:63]
	s_mov_b32 m0, s60
	s_nop 0
	global_load_lds_dwordx4 v[170:171], off
	s_waitcnt vmcnt(8)
	s_waitcnt lgkmcnt(0)
	s_barrier
	s_setprio 1
	s_waitcnt lgkmcnt(0)
	v_mfma_f32_16x16x32_bf16 v[78:81], v[58:61], v[180:183], v[78:81]
	v_mfma_f32_16x16x32_bf16 v[74:77], v[66:69], v[180:183], v[74:77]
	v_mfma_f32_16x16x32_bf16 v[54:57], v[58:61], v[188:191], v[54:57]
	v_mfma_f32_16x16x32_bf16 v[50:53], v[66:69], v[188:191], v[50:53]
	v_mfma_f32_16x16x32_bf16 v[30:33], v[58:61], v[202:205], v[30:33]
	v_mfma_f32_16x16x32_bf16 v[26:29], v[66:69], v[202:205], v[26:29]
	v_mfma_f32_16x16x32_bf16 v[14:17], v[58:61], v[210:213], v[14:17]
	v_mfma_f32_16x16x32_bf16 v[10:13], v[66:69], v[210:213], v[10:13]
	v_mfma_f32_16x16x32_bf16 v[78:81], v[62:65], v[184:187], v[78:81]
	v_mfma_f32_16x16x32_bf16 v[74:77], v[70:73], v[184:187], v[74:77]
	v_mfma_f32_16x16x32_bf16 v[54:57], v[62:65], v[192:195], v[54:57]
	v_mfma_f32_16x16x32_bf16 v[50:53], v[70:73], v[192:195], v[50:53]
	v_mfma_f32_16x16x32_bf16 v[30:33], v[62:65], v[206:209], v[30:33]
	v_mfma_f32_16x16x32_bf16 v[26:29], v[70:73], v[206:209], v[26:29]
	v_mfma_f32_16x16x32_bf16 v[14:17], v[62:65], v[214:217], v[14:17]
	v_mfma_f32_16x16x32_bf16 v[10:13], v[70:73], v[214:217], v[10:13]
	s_setprio 0
	s_setprio 1
	v_mfma_f32_16x16x32_bf16 v[42:45], v[148:151], v[180:183], v[42:45]
	v_mfma_f32_16x16x32_bf16 v[70:73], v[152:155], v[184:187], v[42:45]
	v_mfma_f32_16x16x32_bf16 v[42:45], v[166:169], v[180:183], v[46:49]
	v_mfma_f32_16x16x32_bf16 v[38:41], v[148:151], v[188:191], v[38:41]
	v_mfma_f32_16x16x32_bf16 v[34:37], v[166:169], v[188:191], v[34:37]
	v_mfma_f32_16x16x32_bf16 v[22:25], v[148:151], v[202:205], v[22:25]
	v_mfma_f32_16x16x32_bf16 v[18:21], v[166:169], v[202:205], v[18:21]
	v_mfma_f32_16x16x32_bf16 v[6:9], v[148:151], v[210:213], v[6:9]
	v_mfma_f32_16x16x32_bf16 v[2:5], v[166:169], v[210:213], v[2:5]
	v_mfma_f32_16x16x32_bf16 v[66:69], v[176:179], v[184:187], v[42:45]
	v_mfma_f32_16x16x32_bf16 v[38:41], v[152:155], v[192:195], v[38:41]
	v_mfma_f32_16x16x32_bf16 v[34:37], v[176:179], v[192:195], v[34:37]
	v_mfma_f32_16x16x32_bf16 v[22:25], v[152:155], v[206:209], v[22:25]
	v_mfma_f32_16x16x32_bf16 v[18:21], v[176:179], v[206:209], v[18:21]
	v_mfma_f32_16x16x32_bf16 v[6:9], v[152:155], v[214:217], v[6:9]
	v_mfma_f32_16x16x32_bf16 v[2:5], v[176:179], v[214:217], v[2:5]
	s_setprio 0
	s_barrier
	s_add_i32 s93, s93, 2
	s_add_u32 s10, s10, 0x100
	s_addc_u32 s11, s11, 0
	s_add_u32 s91, s91, 0x100
	s_addc_u32 s92, s92, 0
	s_cmp_gt_u32 s93, 29
	s_cbranch_scc0 .LBB0_1048
	s_and_b64 vcc, exec, s[6:7]
	s_cbranch_vccz .LBB0_1051
	s_barrier

.LBB0_1053:
	s_lshl_b32 s9, s83, 8
	s_or_b32 s9, s9, s2
	s_lshl_b64 s[10:11], s[10:11], 2
	s_add_u32 s10, s59, s10
	v_lshl_add_u32 v150, v42, 3, s9
	s_addc_u32 s11, s61, s11
	s_lshl_b32 s9, s21, 8
	s_add_i32 s9, s9, s54
	v_ashrrev_i32_e32 v151, 31, v150
	v_add_u32_e32 v168, s9, v148
	v_lshl_add_u64 v[46:47], v[150:151], 2, s[10:11]
	v_ashrrev_i32_e32 v169, 31, v168
	v_readlane_b32 s10, v251, 4
	v_lshlrev_b64 v[148:149], 12, v[168:169]
	v_readlane_b32 s11, v251, 5
	v_lshlrev_b64 v[166:167], 1, v[150:151]
	global_load_dwordx4 v[58:61], v[46:47], off offset:16
	global_load_dwordx4 v[62:65], v[46:47], off
	global_load_dwordx4 v[42:45], v[46:47], off offset:528
	s_nop 0
	global_load_dwordx4 v[46:49], v[46:47], off offset:512
	v_lshl_add_u64 v[148:149], s[10:11], 0, v[148:149]
	v_lshl_add_u64 v[184:185], v[148:149], 0, v[166:167]
	global_load_dwordx4 v[176:179], v[184:185], off
	global_load_dwordx4 v[180:183], v[184:185], off offset:256
	v_add_u32_e32 v148, 16, v168
	v_ashrrev_i32_e32 v149, 31, v148
	v_lshlrev_b64 v[148:149], 12, v[148:149]
	v_lshl_add_u64 v[148:149], s[10:11], 0, v[148:149]
	v_lshl_add_u64 v[170:171], v[148:149], 0, v[166:167]
	global_load_dwordx4 v[152:155], v[170:171], off
	global_load_dwordx4 v[148:151], v[170:171], off offset:256
	s_andn2_b64 vcc, exec, s[40:41]
	s_waitcnt vmcnt(0)
	v_lshlrev_b32_e32 v186, 16, v176
	v_and_b32_e32 v187, 0xffff0000, v176
	v_lshlrev_b32_e32 v176, 16, v177
	v_and_b32_e32 v177, 0xffff0000, v177
	v_lshlrev_b32_e32 v188, 16, v178
	v_and_b32_e32 v189, 0xffff0000, v178
	v_lshlrev_b32_e32 v178, 16, v179
	v_and_b32_e32 v179, 0xffff0000, v179
	v_pk_fma_f32 v[146:147], v[146:147], v[64:65], v[176:177]
	v_pk_fma_f32 v[144:145], v[144:145], v[62:63], v[186:187]
	v_pk_fma_f32 v[176:177], v[142:143], v[60:61], v[178:179]
	v_pk_fma_f32 v[142:143], v[140:141], v[58:59], v[188:189]
	v_cvt_pk_bf16_f32 v140, v144, v145
	v_cvt_pk_bf16_f32 v141, v146, v147
	v_lshlrev_b32_e32 v144, 16, v182
	v_cvt_pk_bf16_f32 v142, v142, v143
	v_cvt_pk_bf16_f32 v143, v176, v177
	global_store_dwordx4 v[184:185], v[140:143], off
	v_and_b32_e32 v145, 0xffff0000, v182
	v_lshlrev_b32_e32 v146, 16, v183
	v_lshlrev_b32_e32 v140, 16, v180
	v_and_b32_e32 v141, 0xffff0000, v180
	v_and_b32_e32 v147, 0xffff0000, v183
	v_lshlrev_b32_e32 v142, 16, v181
	v_and_b32_e32 v143, 0xffff0000, v181
	v_pk_fma_f32 v[136:137], v[136:137], v[46:47], v[140:141]
	v_pk_fma_f32 v[140:141], v[134:135], v[44:45], v[146:147]
	v_pk_fma_f32 v[134:135], v[132:133], v[42:43], v[144:145]
	v_cvt_pk_bf16_f32 v132, v136, v137
	v_pk_fma_f32 v[138:139], v[138:139], v[48:49], v[142:143]
	v_lshlrev_b32_e32 v142, 16, v152
	v_cvt_pk_bf16_f32 v133, v138, v139
	v_cvt_pk_bf16_f32 v134, v134, v135
	v_cvt_pk_bf16_f32 v135, v140, v141
	global_store_dwordx4 v[184:185], v[132:135], off offset:256
	v_and_b32_e32 v143, 0xffff0000, v152
	v_lshlrev_b32_e32 v144, 16, v153
	v_add_u32_e32 v132, 32, v168
	v_ashrrev_i32_e32 v133, 31, v132
	v_lshlrev_b64 v[132:133], 12, v[132:133]
	v_lshl_add_u64 v[132:133], s[10:11], 0, v[132:133]
	v_lshl_add_u64 v[140:141], v[132:133], 0, v[166:167]
	v_and_b32_e32 v145, 0xffff0000, v153
	v_lshlrev_b32_e32 v146, 16, v154
	v_and_b32_e32 v147, 0xffff0000, v154
	v_lshlrev_b32_e32 v152, 16, v155
	v_and_b32_e32 v153, 0xffff0000, v155
	global_load_dwordx4 v[136:139], v[140:141], off
	global_load_dwordx4 v[132:135], v[140:141], off offset:256
	v_pk_fma_f32 v[130:131], v[130:131], v[64:65], v[144:145]
	v_pk_fma_f32 v[128:129], v[128:129], v[62:63], v[142:143]
	v_pk_fma_f32 v[142:143], v[126:127], v[60:61], v[152:153]
	v_pk_fma_f32 v[126:127], v[124:125], v[58:59], v[146:147]
	v_cvt_pk_bf16_f32 v124, v128, v129
	v_cvt_pk_bf16_f32 v125, v130, v131
	v_lshlrev_b32_e32 v128, 16, v150
	v_cvt_pk_bf16_f32 v126, v126, v127
	v_cvt_pk_bf16_f32 v127, v142, v143
	global_store_dwordx4 v[170:171], v[124:127], off
	v_and_b32_e32 v129, 0xffff0000, v150
	v_lshlrev_b32_e32 v130, 16, v151
	v_lshlrev_b32_e32 v124, 16, v148
	v_and_b32_e32 v125, 0xffff0000, v148
	v_and_b32_e32 v131, 0xffff0000, v151
	v_lshlrev_b32_e32 v126, 16, v149
	v_and_b32_e32 v127, 0xffff0000, v149
	v_pk_fma_f32 v[120:121], v[120:121], v[46:47], v[124:125]
	v_pk_fma_f32 v[124:125], v[118:119], v[44:45], v[130:131]
	v_pk_fma_f32 v[118:119], v[116:117], v[42:43], v[128:129]
	v_cvt_pk_bf16_f32 v116, v120, v121
	v_pk_fma_f32 v[122:123], v[122:123], v[48:49], v[126:127]
	s_waitcnt vmcnt(2)
	v_lshlrev_b32_e32 v126, 16, v136
	v_cvt_pk_bf16_f32 v117, v122, v123
	v_cvt_pk_bf16_f32 v118, v118, v119
	v_cvt_pk_bf16_f32 v119, v124, v125
	global_store_dwordx4 v[170:171], v[116:119], off offset:256
	v_and_b32_e32 v127, 0xffff0000, v136
	v_lshlrev_b32_e32 v128, 16, v137
	v_add_u32_e32 v116, 48, v168
	v_ashrrev_i32_e32 v117, 31, v116
	v_lshlrev_b64 v[116:117], 12, v[116:117]
	v_lshl_add_u64 v[116:117], s[10:11], 0, v[116:117]
	v_lshl_add_u64 v[120:121], v[116:117], 0, v[166:167]
	global_load_dwordx4 v[122:125], v[120:121], off
	global_load_dwordx4 v[116:119], v[120:121], off offset:256
	v_and_b32_e32 v129, 0xffff0000, v137
	v_lshlrev_b32_e32 v130, 16, v138
	v_and_b32_e32 v131, 0xffff0000, v138
	v_lshlrev_b32_e32 v136, 16, v139
	v_and_b32_e32 v137, 0xffff0000, v139
	v_pk_fma_f32 v[114:115], v[114:115], v[64:65], v[128:129]
	v_pk_fma_f32 v[112:113], v[112:113], v[62:63], v[126:127]
	v_pk_fma_f32 v[126:127], v[110:111], v[60:61], v[136:137]
	v_pk_fma_f32 v[110:111], v[108:109], v[58:59], v[130:131]
	v_cvt_pk_bf16_f32 v108, v112, v113
	v_cvt_pk_bf16_f32 v109, v114, v115
	s_waitcnt vmcnt(4)
	v_lshlrev_b32_e32 v112, 16, v134
	v_cvt_pk_bf16_f32 v110, v110, v111
	v_cvt_pk_bf16_f32 v111, v126, v127
	global_store_dwordx4 v[140:141], v[108:111], off
	v_and_b32_e32 v113, 0xffff0000, v134
	v_lshlrev_b32_e32 v114, 16, v135
	v_lshlrev_b32_e32 v108, 16, v132
	v_and_b32_e32 v109, 0xffff0000, v132
	v_and_b32_e32 v115, 0xffff0000, v135
	v_lshlrev_b32_e32 v110, 16, v133
	v_and_b32_e32 v111, 0xffff0000, v133
	v_pk_fma_f32 v[104:105], v[104:105], v[46:47], v[108:109]
	v_pk_fma_f32 v[108:109], v[102:103], v[44:45], v[114:115]
	v_pk_fma_f32 v[102:103], v[100:101], v[42:43], v[112:113]
	v_cvt_pk_bf16_f32 v100, v104, v105
	v_pk_fma_f32 v[106:107], v[106:107], v[48:49], v[110:111]
	s_waitcnt vmcnt(2)
	v_lshlrev_b32_e32 v110, 16, v122
	v_cvt_pk_bf16_f32 v101, v106, v107
	v_cvt_pk_bf16_f32 v102, v102, v103
	v_cvt_pk_bf16_f32 v103, v108, v109
	global_store_dwordx4 v[140:141], v[100:103], off offset:256
	v_and_b32_e32 v111, 0xffff0000, v122
	v_lshlrev_b32_e32 v112, 16, v123
	v_add_u32_e32 v100, 0x80, v168
	v_ashrrev_i32_e32 v101, 31, v100
	v_lshlrev_b64 v[100:101], 12, v[100:101]
	v_lshl_add_u64 v[100:101], s[10:11], 0, v[100:101]
	v_lshl_add_u64 v[108:109], v[100:101], 0, v[166:167]
	v_and_b32_e32 v113, 0xffff0000, v123
	v_lshlrev_b32_e32 v114, 16, v124
	v_and_b32_e32 v115, 0xffff0000, v124
	v_lshlrev_b32_e32 v122, 16, v125
	v_and_b32_e32 v123, 0xffff0000, v125
	global_load_dwordx4 v[104:107], v[108:109], off
	global_load_dwordx4 v[100:103], v[108:109], off offset:256
	v_pk_fma_f32 v[96:97], v[96:97], v[64:65], v[112:113]
	v_pk_fma_f32 v[94:95], v[94:95], v[62:63], v[110:111]
	v_pk_fma_f32 v[110:111], v[92:93], v[60:61], v[122:123]
	v_pk_fma_f32 v[92:93], v[90:91], v[58:59], v[114:115]
	v_cvt_pk_bf16_f32 v90, v94, v95
	v_cvt_pk_bf16_f32 v91, v96, v97
	s_waitcnt vmcnt(4)
	v_lshlrev_b32_e32 v94, 16, v118
	v_cvt_pk_bf16_f32 v92, v92, v93
	v_cvt_pk_bf16_f32 v93, v110, v111
	global_store_dwordx4 v[120:121], v[90:93], off
	v_and_b32_e32 v95, 0xffff0000, v118
	v_lshlrev_b32_e32 v96, 16, v119
	v_lshlrev_b32_e32 v90, 16, v116
	v_and_b32_e32 v91, 0xffff0000, v116
	v_and_b32_e32 v97, 0xffff0000, v119
	v_lshlrev_b32_e32 v92, 16, v117
	v_and_b32_e32 v93, 0xffff0000, v117
	v_pk_fma_f32 v[86:87], v[86:87], v[46:47], v[90:91]
	v_pk_fma_f32 v[90:91], v[84:85], v[44:45], v[96:97]
	v_pk_fma_f32 v[84:85], v[82:83], v[42:43], v[94:95]
	v_cvt_pk_bf16_f32 v82, v86, v87
	v_pk_fma_f32 v[88:89], v[88:89], v[48:49], v[92:93]
	s_waitcnt vmcnt(2)
	v_lshlrev_b32_e32 v92, 16, v104
	v_cvt_pk_bf16_f32 v83, v88, v89
	v_cvt_pk_bf16_f32 v84, v84, v85
	v_cvt_pk_bf16_f32 v85, v90, v91
	global_store_dwordx4 v[120:121], v[82:85], off offset:256
	v_and_b32_e32 v93, 0xffff0000, v104
	v_lshlrev_b32_e32 v94, 16, v105
	v_add_u32_e32 v82, 0x90, v168
	v_ashrrev_i32_e32 v83, 31, v82
	v_lshlrev_b64 v[82:83], 12, v[82:83]
	v_lshl_add_u64 v[82:83], s[10:11], 0, v[82:83]
	v_lshl_add_u64 v[86:87], v[82:83], 0, v[166:167]
	global_load_dwordx4 v[88:91], v[86:87], off
	global_load_dwordx4 v[82:85], v[86:87], off offset:256
	v_and_b32_e32 v95, 0xffff0000, v105
	v_lshlrev_b32_e32 v96, 16, v106
	v_and_b32_e32 v97, 0xffff0000, v106
	v_lshlrev_b32_e32 v104, 16, v107
	v_and_b32_e32 v105, 0xffff0000, v107
	v_pk_fma_f32 v[80:81], v[80:81], v[64:65], v[94:95]
	v_pk_fma_f32 v[78:79], v[78:79], v[62:63], v[92:93]
	v_pk_fma_f32 v[92:93], v[76:77], v[60:61], v[104:105]
	v_pk_fma_f32 v[76:77], v[74:75], v[58:59], v[96:97]
	v_cvt_pk_bf16_f32 v74, v78, v79
	v_cvt_pk_bf16_f32 v75, v80, v81
	s_waitcnt vmcnt(4)
	v_lshlrev_b32_e32 v78, 16, v102
	v_cvt_pk_bf16_f32 v76, v76, v77
	v_cvt_pk_bf16_f32 v77, v92, v93
	global_store_dwordx4 v[108:109], v[74:77], off
	v_and_b32_e32 v79, 0xffff0000, v102
	v_lshlrev_b32_e32 v80, 16, v103
	v_lshlrev_b32_e32 v74, 16, v100
	v_and_b32_e32 v75, 0xffff0000, v100
	v_and_b32_e32 v81, 0xffff0000, v103
	v_lshlrev_b32_e32 v76, 16, v101
	v_and_b32_e32 v77, 0xffff0000, v101
	v_pk_fma_f32 v[70:71], v[70:71], v[46:47], v[74:75]
	v_pk_fma_f32 v[74:75], v[68:69], v[44:45], v[80:81]
	v_pk_fma_f32 v[68:69], v[66:67], v[42:43], v[78:79]
	v_cvt_pk_bf16_f32 v66, v70, v71
	v_pk_fma_f32 v[72:73], v[72:73], v[48:49], v[76:77]
	s_waitcnt vmcnt(2)
	v_lshlrev_b32_e32 v76, 16, v88
	v_cvt_pk_bf16_f32 v67, v72, v73
	v_cvt_pk_bf16_f32 v68, v68, v69
	v_cvt_pk_bf16_f32 v69, v74, v75
	global_store_dwordx4 v[108:109], v[66:69], off offset:256
	v_and_b32_e32 v77, 0xffff0000, v88
	v_lshlrev_b32_e32 v78, 16, v89
	v_add_u32_e32 v66, 0xa0, v168
	v_ashrrev_i32_e32 v67, 31, v66
	v_lshlrev_b64 v[66:67], 12, v[66:67]
	v_lshl_add_u64 v[66:67], s[10:11], 0, v[66:67]
	v_lshl_add_u64 v[74:75], v[66:67], 0, v[166:167]
	v_and_b32_e32 v79, 0xffff0000, v89
	v_lshlrev_b32_e32 v80, 16, v90
	v_and_b32_e32 v81, 0xffff0000, v90
	v_lshlrev_b32_e32 v88, 16, v91
	v_and_b32_e32 v89, 0xffff0000, v91
	global_load_dwordx4 v[70:73], v[74:75], off
	global_load_dwordx4 v[66:69], v[74:75], off offset:256
	v_pk_fma_f32 v[56:57], v[56:57], v[64:65], v[78:79]
	v_pk_fma_f32 v[54:55], v[54:55], v[62:63], v[76:77]
	v_pk_fma_f32 v[76:77], v[52:53], v[60:61], v[88:89]
	v_pk_fma_f32 v[52:53], v[50:51], v[58:59], v[80:81]
	v_cvt_pk_bf16_f32 v50, v54, v55
	v_cvt_pk_bf16_f32 v51, v56, v57
	s_waitcnt vmcnt(4)
	v_lshlrev_b32_e32 v54, 16, v84
	v_cvt_pk_bf16_f32 v52, v52, v53
	v_cvt_pk_bf16_f32 v53, v76, v77
	global_store_dwordx4 v[86:87], v[50:53], off
	v_and_b32_e32 v55, 0xffff0000, v84
	v_lshlrev_b32_e32 v56, 16, v85
	v_lshlrev_b32_e32 v50, 16, v82
	v_and_b32_e32 v51, 0xffff0000, v82
	v_and_b32_e32 v57, 0xffff0000, v85
	v_lshlrev_b32_e32 v52, 16, v83
	v_and_b32_e32 v53, 0xffff0000, v83
	v_pk_fma_f32 v[38:39], v[38:39], v[46:47], v[50:51]
	v_pk_fma_f32 v[50:51], v[36:37], v[44:45], v[56:57]
	v_pk_fma_f32 v[36:37], v[34:35], v[42:43], v[54:55]
	v_cvt_pk_bf16_f32 v34, v38, v39
	v_pk_fma_f32 v[40:41], v[40:41], v[48:49], v[52:53]
	s_waitcnt vmcnt(2)
	v_lshlrev_b32_e32 v54, 16, v71
	v_cvt_pk_bf16_f32 v35, v40, v41
	v_cvt_pk_bf16_f32 v36, v36, v37
	v_cvt_pk_bf16_f32 v37, v50, v51
	global_store_dwordx4 v[86:87], v[34:37], off offset:256
	v_lshlrev_b32_e32 v40, 16, v70
	v_and_b32_e32 v41, 0xffff0000, v70
	v_add_u32_e32 v34, 0xb0, v168
	v_ashrrev_i32_e32 v35, 31, v34
	v_lshlrev_b64 v[34:35], 12, v[34:35]
	v_lshl_add_u64 v[34:35], s[10:11], 0, v[34:35]
	v_lshl_add_u64 v[38:39], v[34:35], 0, v[166:167]
	global_load_dwordx4 v[50:53], v[38:39], off
	global_load_dwordx4 v[34:37], v[38:39], off offset:256
	v_and_b32_e32 v55, 0xffff0000, v71
	v_lshlrev_b32_e32 v56, 16, v72
	v_and_b32_e32 v57, 0xffff0000, v72
	v_lshlrev_b32_e32 v70, 16, v73
	v_and_b32_e32 v71, 0xffff0000, v73
	v_pk_fma_f32 v[32:33], v[32:33], v[64:65], v[54:55]
	v_pk_fma_f32 v[30:31], v[30:31], v[62:63], v[40:41]
	v_pk_fma_f32 v[40:41], v[28:29], v[60:61], v[70:71]
	v_pk_fma_f32 v[28:29], v[26:27], v[58:59], v[56:57]
	v_cvt_pk_bf16_f32 v26, v30, v31
	v_cvt_pk_bf16_f32 v27, v32, v33
	s_waitcnt vmcnt(4)
	v_lshlrev_b32_e32 v30, 16, v68
	v_cvt_pk_bf16_f32 v28, v28, v29
	v_cvt_pk_bf16_f32 v29, v40, v41
	global_store_dwordx4 v[74:75], v[26:29], off
	v_and_b32_e32 v31, 0xffff0000, v68
	v_lshlrev_b32_e32 v32, 16, v69
	v_lshlrev_b32_e32 v26, 16, v66
	v_and_b32_e32 v27, 0xffff0000, v66
	v_and_b32_e32 v33, 0xffff0000, v69
	v_lshlrev_b32_e32 v28, 16, v67
	v_and_b32_e32 v29, 0xffff0000, v67
	v_pk_fma_f32 v[22:23], v[22:23], v[46:47], v[26:27]
	v_pk_fma_f32 v[26:27], v[20:21], v[44:45], v[32:33]
	v_pk_fma_f32 v[20:21], v[18:19], v[42:43], v[30:31]
	v_pk_fma_f32 v[24:25], v[24:25], v[48:49], v[28:29]
	v_cvt_pk_bf16_f32 v18, v22, v23
	s_mov_b64 s[10:11], -1
	v_cvt_pk_bf16_f32 v19, v24, v25
	v_cvt_pk_bf16_f32 v20, v20, v21
	v_cvt_pk_bf16_f32 v21, v26, v27
	global_store_dwordx4 v[74:75], v[18:21], off offset:256
	s_waitcnt vmcnt(3)
	v_lshlrev_b32_e32 v22, 16, v52
	v_lshlrev_b32_e32 v18, 16, v50
	v_and_b32_e32 v19, 0xffff0000, v50
	v_lshlrev_b32_e32 v20, 16, v51
	v_and_b32_e32 v21, 0xffff0000, v51
	v_and_b32_e32 v23, 0xffff0000, v52
	v_lshlrev_b32_e32 v24, 16, v53
	v_and_b32_e32 v25, 0xffff0000, v53
	v_pk_fma_f32 v[16:17], v[16:17], v[64:65], v[20:21]
	v_pk_fma_f32 v[14:15], v[14:15], v[62:63], v[18:19]
	v_pk_fma_f32 v[18:19], v[12:13], v[60:61], v[24:25]
	v_pk_fma_f32 v[12:13], v[10:11], v[58:59], v[22:23]
	v_cvt_pk_bf16_f32 v10, v14, v15
	v_cvt_pk_bf16_f32 v11, v16, v17
	s_waitcnt vmcnt(2)
	v_lshlrev_b32_e32 v14, 16, v36
	v_cvt_pk_bf16_f32 v12, v12, v13
	v_cvt_pk_bf16_f32 v13, v18, v19
	global_store_dwordx4 v[38:39], v[10:13], off
	v_and_b32_e32 v15, 0xffff0000, v36
	v_lshlrev_b32_e32 v16, 16, v37
	v_lshlrev_b32_e32 v10, 16, v34
	v_and_b32_e32 v11, 0xffff0000, v34
	v_and_b32_e32 v17, 0xffff0000, v37
	v_lshlrev_b32_e32 v12, 16, v35
	v_and_b32_e32 v13, 0xffff0000, v35
	v_pk_fma_f32 v[6:7], v[6:7], v[46:47], v[10:11]
	v_pk_fma_f32 v[10:11], v[4:5], v[44:45], v[16:17]
	v_pk_fma_f32 v[4:5], v[2:3], v[42:43], v[14:15]
	v_pk_fma_f32 v[8:9], v[8:9], v[48:49], v[12:13]
	v_cvt_pk_bf16_f32 v2, v6, v7
	s_nop 0
	v_cvt_pk_bf16_f32 v3, v8, v9
	v_cvt_pk_bf16_f32 v4, v4, v5
	v_cvt_pk_bf16_f32 v5, v10, v11
	global_store_dwordx4 v[38:39], v[2:5], off offset:256
	s_mov_b64 s[100:101], -1
	s_cbranch_vccnz .LBB0_1044
	s_andn2_b64 vcc, exec, s[4:5]
	s_cbranch_vccnz .LBB0_1043
	s_barrier
	s_branch .LBB0_1043

.LBB0_1068:
	ds_read_b128 v[42:45], v186
	ds_read_b128 v[46:49], v186 offset:1024
	ds_read_b128 v[66:69], v186 offset:2048
	ds_read_b128 v[70:73], v186 offset:3072
	ds_read_b128 v[148:151], v186 offset:16384
	ds_read_b128 v[152:155], v186 offset:17408
	ds_read_b128 v[156:159], v186 offset:18432
	ds_read_b128 v[160:163], v186 offset:19456
	s_add_u32 s31, s10, 0xfff80080
	s_addc_u32 s54, s11, -1
	s_cmp_eq_u32 s97, 28
	s_cselect_b32 s57, s49, s54
	s_cselect_b32 s56, s93, s31
	s_cselect_b32 s55, s47, s96
	s_cselect_b32 s54, s94, s95
	v_lshl_add_u64 v[182:183], s[10:11], 0, v[170:171]
	s_add_i32 m0, s17, 0xc000
	ds_read_b128 v[174:177], v187
	ds_read_b128 v[178:181], v187 offset:1024
	ds_read_b128 v[188:191], v187 offset:2048
	ds_read_b128 v[192:195], v187 offset:3072
	ds_read_b128 v[202:205], v187 offset:4096
	ds_read_b128 v[206:209], v187 offset:5120
	ds_read_b128 v[210:213], v187 offset:6144
	ds_read_b128 v[214:217], v187 offset:7168
	global_load_lds_dwordx4 v[182:183], off
	v_lshl_add_u64 v[182:183], s[10:11], 0, v[172:173]
	s_add_i32 m0, s17, 0xe000
	s_nop 0
	global_load_lds_dwordx4 v[182:183], off
	s_mov_b64 vcc, s[100:101]
	s_cbranch_vccnz .Lepw6
	s_waitcnt vmcnt(8)
.Lepw6:
	s_waitcnt lgkmcnt(0)
	s_barrier
	s_setprio 1
	s_waitcnt lgkmcnt(0)
	v_mfma_f32_16x16x32_bf16 v[144:147], v[42:45], v[174:177], v[144:147]
	v_mfma_f32_16x16x32_bf16 v[140:143], v[66:69], v[174:177], v[140:143]
	v_mfma_f32_16x16x32_bf16 v[128:131], v[42:45], v[188:191], v[128:131]
	v_mfma_f32_16x16x32_bf16 v[124:127], v[66:69], v[188:191], v[124:127]
	v_mfma_f32_16x16x32_bf16 v[112:115], v[42:45], v[202:205], v[112:115]
	v_mfma_f32_16x16x32_bf16 v[108:111], v[66:69], v[202:205], v[108:111]
	v_mfma_f32_16x16x32_bf16 v[94:97], v[42:45], v[210:213], v[94:97]
	v_mfma_f32_16x16x32_bf16 v[90:93], v[66:69], v[210:213], v[90:93]
	v_mfma_f32_16x16x32_bf16 v[144:147], v[46:49], v[178:181], v[144:147]
	v_mfma_f32_16x16x32_bf16 v[140:143], v[70:73], v[178:181], v[140:143]
	v_mfma_f32_16x16x32_bf16 v[128:131], v[46:49], v[192:195], v[128:131]
	v_mfma_f32_16x16x32_bf16 v[124:127], v[70:73], v[192:195], v[124:127]
	v_mfma_f32_16x16x32_bf16 v[112:115], v[46:49], v[206:209], v[112:115]
	v_mfma_f32_16x16x32_bf16 v[108:111], v[70:73], v[206:209], v[108:111]
	v_mfma_f32_16x16x32_bf16 v[94:97], v[46:49], v[214:217], v[94:97]
	v_mfma_f32_16x16x32_bf16 v[90:93], v[70:73], v[214:217], v[90:93]
	s_setprio 0
	s_setprio 1
	v_mfma_f32_16x16x32_bf16 v[136:139], v[148:151], v[174:177], v[136:139]
	v_mfma_f32_16x16x32_bf16 v[132:135], v[156:159], v[174:177], v[132:135]
	v_mfma_f32_16x16x32_bf16 v[120:123], v[148:151], v[188:191], v[120:123]
	v_mfma_f32_16x16x32_bf16 v[116:119], v[156:159], v[188:191], v[116:119]
	v_mfma_f32_16x16x32_bf16 v[104:107], v[148:151], v[202:205], v[104:107]
	v_mfma_f32_16x16x32_bf16 v[100:103], v[156:159], v[202:205], v[100:103]
	v_mfma_f32_16x16x32_bf16 v[86:89], v[148:151], v[210:213], v[86:89]
	v_mfma_f32_16x16x32_bf16 v[82:85], v[156:159], v[210:213], v[82:85]
	v_mfma_f32_16x16x32_bf16 v[136:139], v[152:155], v[178:181], v[136:139]
	v_mfma_f32_16x16x32_bf16 v[132:135], v[160:163], v[178:181], v[132:135]
	v_mfma_f32_16x16x32_bf16 v[120:123], v[152:155], v[192:195], v[120:123]
	v_mfma_f32_16x16x32_bf16 v[116:119], v[160:163], v[192:195], v[116:119]
	v_mfma_f32_16x16x32_bf16 v[104:107], v[152:155], v[206:209], v[104:107]
	v_mfma_f32_16x16x32_bf16 v[100:103], v[160:163], v[206:209], v[100:103]
	v_mfma_f32_16x16x32_bf16 v[86:89], v[152:155], v[214:217], v[86:89]
	v_mfma_f32_16x16x32_bf16 v[82:85], v[160:163], v[214:217], v[82:85]
	s_setprio 0
	s_barrier
	s_mov_b32 m0, s18
	v_lshl_add_u64 v[182:183], s[54:55], 0, v[98:99]
	s_add_u32 vcc_lo, s54, 0x80000
	ds_read_b128 v[174:177], v187 offset:16384
	ds_read_b128 v[178:181], v187 offset:17408
	ds_read_b128 v[188:191], v187 offset:18432
	ds_read_b128 v[192:195], v187 offset:19456
	ds_read_b128 v[202:205], v187 offset:20480
	ds_read_b128 v[206:209], v187 offset:21504
	ds_read_b128 v[210:213], v187 offset:22528
	ds_read_b128 v[214:217], v187 offset:23552
	global_load_lds_dwordx4 v[182:183], off
	v_lshl_add_u64 v[196:197], s[54:55], 0, v[164:165]
	s_mov_b32 m0, s19
	s_addc_u32 vcc_hi, s55, 0
	global_load_lds_dwordx4 v[196:197], off
	v_lshl_add_u64 v[218:219], vcc, 0, v[98:99]
	s_mov_b32 m0, s20
	v_lshl_add_u64 v[226:227], s[56:57], 0, v[166:167]
	global_load_lds_dwordx4 v[218:219], off
	v_lshl_add_u64 v[218:219], vcc, 0, v[164:165]
	s_mov_b32 m0, s24
	s_nop 0
	global_load_lds_dwordx4 v[218:219], off
	v_lshl_add_u64 v[218:219], s[56:57], 0, v[168:169]
	s_mov_b32 m0, s17
	s_nop 0
	global_load_lds_dwordx4 v[218:219], off
	s_mov_b32 m0, s27
	s_nop 0
	global_load_lds_dwordx4 v[226:227], off
	s_mov_b64 vcc, s[100:101]
	s_cbranch_vccnz .Lepw5
	s_waitcnt vmcnt(8)
.Lepw5:
	s_waitcnt lgkmcnt(0)
	s_barrier
	s_setprio 1
	s_waitcnt lgkmcnt(0)
	v_mfma_f32_16x16x32_bf16 v[78:81], v[42:45], v[174:177], v[78:81]
	v_mfma_f32_16x16x32_bf16 v[74:77], v[66:69], v[174:177], v[74:77]
	v_mfma_f32_16x16x32_bf16 v[54:57], v[42:45], v[188:191], v[54:57]
	v_mfma_f32_16x16x32_bf16 v[50:53], v[66:69], v[188:191], v[50:53]
	v_mfma_f32_16x16x32_bf16 v[30:33], v[42:45], v[202:205], v[30:33]
	v_mfma_f32_16x16x32_bf16 v[26:29], v[66:69], v[202:205], v[26:29]
	v_mfma_f32_16x16x32_bf16 v[14:17], v[42:45], v[210:213], v[14:17]
	v_mfma_f32_16x16x32_bf16 v[10:13], v[66:69], v[210:213], v[10:13]
	v_mfma_f32_16x16x32_bf16 v[78:81], v[46:49], v[178:181], v[78:81]
	v_mfma_f32_16x16x32_bf16 v[74:77], v[70:73], v[178:181], v[74:77]
	v_mfma_f32_16x16x32_bf16 v[54:57], v[46:49], v[192:195], v[54:57]
	v_mfma_f32_16x16x32_bf16 v[50:53], v[70:73], v[192:195], v[50:53]
	v_mfma_f32_16x16x32_bf16 v[30:33], v[46:49], v[206:209], v[30:33]
	v_mfma_f32_16x16x32_bf16 v[26:29], v[70:73], v[206:209], v[26:29]
	v_mfma_f32_16x16x32_bf16 v[14:17], v[46:49], v[214:217], v[14:17]
	v_mfma_f32_16x16x32_bf16 v[10:13], v[70:73], v[214:217], v[10:13]
	s_setprio 0
	s_setprio 1
	v_mfma_f32_16x16x32_bf16 v[38:41], v[148:151], v[188:191], v[38:41]
	v_mfma_f32_16x16x32_bf16 v[34:37], v[156:159], v[188:191], v[34:37]
	v_mfma_f32_16x16x32_bf16 v[22:25], v[148:151], v[202:205], v[22:25]
	v_mfma_f32_16x16x32_bf16 v[18:21], v[156:159], v[202:205], v[18:21]
	v_mfma_f32_16x16x32_bf16 v[6:9], v[148:151], v[210:213], v[6:9]
	v_mfma_f32_16x16x32_bf16 v[2:5], v[156:159], v[210:213], v[2:5]
	v_mfma_f32_16x16x32_bf16 v[42:45], v[148:151], v[174:177], v[62:65]
	v_mfma_f32_16x16x32_bf16 v[46:49], v[156:159], v[174:177], v[58:61]
	v_mfma_f32_16x16x32_bf16 v[38:41], v[152:155], v[192:195], v[38:41]
	v_mfma_f32_16x16x32_bf16 v[34:37], v[160:163], v[192:195], v[34:37]
	v_mfma_f32_16x16x32_bf16 v[22:25], v[152:155], v[206:209], v[22:25]
	v_mfma_f32_16x16x32_bf16 v[18:21], v[160:163], v[206:209], v[18:21]
	v_mfma_f32_16x16x32_bf16 v[6:9], v[152:155], v[214:217], v[6:9]
	v_mfma_f32_16x16x32_bf16 v[2:5], v[160:163], v[214:217], v[2:5]
	v_mfma_f32_16x16x32_bf16 v[42:45], v[152:155], v[178:181], v[42:45]
	v_mfma_f32_16x16x32_bf16 v[46:49], v[160:163], v[178:181], v[46:49]
	s_setprio 0
	s_barrier
	ds_read_b128 v[58:61], v186 offset:32768
	ds_read_b128 v[62:65], v186 offset:33792
	ds_read_b128 v[66:69], v186 offset:34816
	ds_read_b128 v[70:73], v186 offset:35840
	ds_read_b128 v[148:151], v186 offset:49152
	ds_read_b128 v[152:155], v186 offset:50176
	ds_read_b128 v[156:159], v186 offset:51200
	ds_read_b128 v[160:163], v186 offset:52224
	s_add_u32 s56, s56, 0x80000
	s_addc_u32 s57, s57, 0
	s_mov_b32 m0, s28
	v_lshl_add_u64 v[228:229], s[56:57], 0, v[168:169]
	ds_read_b128 v[174:177], v187 offset:32768
	ds_read_b128 v[178:181], v187 offset:33792
	ds_read_b128 v[188:191], v187 offset:34816
	ds_read_b128 v[192:195], v187 offset:35840
	ds_read_b128 v[202:205], v187 offset:36864
	ds_read_b128 v[206:209], v187 offset:37888
	ds_read_b128 v[210:213], v187 offset:38912
	ds_read_b128 v[214:217], v187 offset:39936
	global_load_lds_dwordx4 v[228:229], off
	v_lshl_add_u64 v[228:229], s[56:57], 0, v[166:167]
	s_mov_b32 m0, s29
	s_nop 0
	global_load_lds_dwordx4 v[228:229], off
	s_waitcnt vmcnt(8)
	s_mov_b64 s[100:101], 0
	s_waitcnt lgkmcnt(0)
	s_barrier
	s_setprio 1
	s_waitcnt lgkmcnt(0)
	v_mfma_f32_16x16x32_bf16 v[144:147], v[58:61], v[174:177], v[144:147]
	v_mfma_f32_16x16x32_bf16 v[140:143], v[66:69], v[174:177], v[140:143]
	v_mfma_f32_16x16x32_bf16 v[128:131], v[58:61], v[188:191], v[128:131]
	v_mfma_f32_16x16x32_bf16 v[124:127], v[66:69], v[188:191], v[124:127]
	v_mfma_f32_16x16x32_bf16 v[112:115], v[58:61], v[202:205], v[112:115]
	v_mfma_f32_16x16x32_bf16 v[108:111], v[66:69], v[202:205], v[108:111]
	v_mfma_f32_16x16x32_bf16 v[94:97], v[58:61], v[210:213], v[94:97]
	v_mfma_f32_16x16x32_bf16 v[90:93], v[66:69], v[210:213], v[90:93]
	v_mfma_f32_16x16x32_bf16 v[144:147], v[62:65], v[178:181], v[144:147]
	v_mfma_f32_16x16x32_bf16 v[140:143], v[70:73], v[178:181], v[140:143]
	v_mfma_f32_16x16x32_bf16 v[128:131], v[62:65], v[192:195], v[128:131]
	v_mfma_f32_16x16x32_bf16 v[124:127], v[70:73], v[192:195], v[124:127]
	v_mfma_f32_16x16x32_bf16 v[112:115], v[62:65], v[206:209], v[112:115]
	v_mfma_f32_16x16x32_bf16 v[108:111], v[70:73], v[206:209], v[108:111]
	v_mfma_f32_16x16x32_bf16 v[94:97], v[62:65], v[214:217], v[94:97]
	v_mfma_f32_16x16x32_bf16 v[90:93], v[70:73], v[214:217], v[90:93]
	s_setprio 0
	s_setprio 1
	v_mfma_f32_16x16x32_bf16 v[136:139], v[148:151], v[174:177], v[136:139]
	v_mfma_f32_16x16x32_bf16 v[132:135], v[156:159], v[174:177], v[132:135]
	v_mfma_f32_16x16x32_bf16 v[120:123], v[148:151], v[188:191], v[120:123]
	v_mfma_f32_16x16x32_bf16 v[116:119], v[156:159], v[188:191], v[116:119]
	v_mfma_f32_16x16x32_bf16 v[104:107], v[148:151], v[202:205], v[104:107]
	v_mfma_f32_16x16x32_bf16 v[100:103], v[156:159], v[202:205], v[100:103]
	v_mfma_f32_16x16x32_bf16 v[86:89], v[148:151], v[210:213], v[86:89]
	v_mfma_f32_16x16x32_bf16 v[82:85], v[156:159], v[210:213], v[82:85]
	v_mfma_f32_16x16x32_bf16 v[136:139], v[152:155], v[178:181], v[136:139]
	v_mfma_f32_16x16x32_bf16 v[132:135], v[160:163], v[178:181], v[132:135]
	v_mfma_f32_16x16x32_bf16 v[120:123], v[152:155], v[192:195], v[120:123]
	v_mfma_f32_16x16x32_bf16 v[116:119], v[160:163], v[192:195], v[116:119]
	v_mfma_f32_16x16x32_bf16 v[104:107], v[152:155], v[206:209], v[104:107]
	v_mfma_f32_16x16x32_bf16 v[100:103], v[160:163], v[206:209], v[100:103]
	v_mfma_f32_16x16x32_bf16 v[86:89], v[152:155], v[214:217], v[86:89]
	v_mfma_f32_16x16x32_bf16 v[82:85], v[160:163], v[214:217], v[82:85]
	s_setprio 0
	s_barrier
	s_mov_b32 m0, s65
	v_lshl_add_u64 v[182:183], v[182:183], 0, s[62:63]
	s_add_u32 s54, s54, 0x80080
	ds_read_b128 v[174:177], v187 offset:49152
	ds_read_b128 v[178:181], v187 offset:50176
	ds_read_b128 v[188:191], v187 offset:51200
	ds_read_b128 v[192:195], v187 offset:52224
	ds_read_b128 v[202:205], v187 offset:53248
	ds_read_b128 v[206:209], v187 offset:54272
	ds_read_b128 v[210:213], v187 offset:55296
	ds_read_b128 v[214:217], v187 offset:56320
	global_load_lds_dwordx4 v[182:183], off
	v_lshl_add_u64 v[182:183], v[196:197], 0, s[62:63]
	s_mov_b32 m0, s66
	s_addc_u32 s55, s55, 0
	global_load_lds_dwordx4 v[182:183], off
	v_lshl_add_u64 v[182:183], s[54:55], 0, v[98:99]
	s_mov_b32 m0, s91
	s_nop 0
	global_load_lds_dwordx4 v[182:183], off
	v_lshl_add_u64 v[182:183], s[54:55], 0, v[164:165]
	s_mov_b32 m0, s92
	s_nop 0
	global_load_lds_dwordx4 v[182:183], off
	v_lshl_add_u64 v[182:183], v[218:219], 0, s[62:63]
	s_mov_b32 m0, s83
	s_nop 0
	global_load_lds_dwordx4 v[182:183], off
	v_lshl_add_u64 v[182:183], v[226:227], 0, s[62:63]
	s_mov_b32 m0, s90
	s_nop 0
	global_load_lds_dwordx4 v[182:183], off
	s_waitcnt vmcnt(8)
	s_waitcnt lgkmcnt(0)
	s_barrier
	s_setprio 1
	s_waitcnt lgkmcnt(0)
	v_mfma_f32_16x16x32_bf16 v[78:81], v[58:61], v[174:177], v[78:81]
	v_mfma_f32_16x16x32_bf16 v[74:77], v[66:69], v[174:177], v[74:77]
	v_mfma_f32_16x16x32_bf16 v[54:57], v[58:61], v[188:191], v[54:57]
	v_mfma_f32_16x16x32_bf16 v[50:53], v[66:69], v[188:191], v[50:53]
	v_mfma_f32_16x16x32_bf16 v[30:33], v[58:61], v[202:205], v[30:33]
	v_mfma_f32_16x16x32_bf16 v[26:29], v[66:69], v[202:205], v[26:29]
	v_mfma_f32_16x16x32_bf16 v[14:17], v[58:61], v[210:213], v[14:17]
	v_mfma_f32_16x16x32_bf16 v[10:13], v[66:69], v[210:213], v[10:13]
	v_mfma_f32_16x16x32_bf16 v[78:81], v[62:65], v[178:181], v[78:81]
	v_mfma_f32_16x16x32_bf16 v[74:77], v[70:73], v[178:181], v[74:77]
	v_mfma_f32_16x16x32_bf16 v[54:57], v[62:65], v[192:195], v[54:57]
	v_mfma_f32_16x16x32_bf16 v[50:53], v[70:73], v[192:195], v[50:53]
	v_mfma_f32_16x16x32_bf16 v[30:33], v[62:65], v[206:209], v[30:33]
	v_mfma_f32_16x16x32_bf16 v[26:29], v[70:73], v[206:209], v[26:29]
	v_mfma_f32_16x16x32_bf16 v[14:17], v[62:65], v[214:217], v[14:17]
	v_mfma_f32_16x16x32_bf16 v[10:13], v[70:73], v[214:217], v[10:13]
	s_setprio 0
	s_setprio 1
	v_mfma_f32_16x16x32_bf16 v[42:45], v[148:151], v[174:177], v[42:45]
	v_mfma_f32_16x16x32_bf16 v[62:65], v[152:155], v[178:181], v[42:45]
	v_mfma_f32_16x16x32_bf16 v[42:45], v[156:159], v[174:177], v[46:49]
	v_mfma_f32_16x16x32_bf16 v[38:41], v[148:151], v[188:191], v[38:41]
	v_mfma_f32_16x16x32_bf16 v[34:37], v[156:159], v[188:191], v[34:37]
	v_mfma_f32_16x16x32_bf16 v[22:25], v[148:151], v[202:205], v[22:25]
	v_mfma_f32_16x16x32_bf16 v[18:21], v[156:159], v[202:205], v[18:21]
	v_mfma_f32_16x16x32_bf16 v[6:9], v[148:151], v[210:213], v[6:9]
	v_mfma_f32_16x16x32_bf16 v[2:5], v[156:159], v[210:213], v[2:5]
	v_mfma_f32_16x16x32_bf16 v[58:61], v[160:163], v[178:181], v[42:45]
	v_mfma_f32_16x16x32_bf16 v[38:41], v[152:155], v[192:195], v[38:41]
	v_mfma_f32_16x16x32_bf16 v[34:37], v[160:163], v[192:195], v[34:37]
	v_mfma_f32_16x16x32_bf16 v[22:25], v[152:155], v[206:209], v[22:25]
	v_mfma_f32_16x16x32_bf16 v[18:21], v[160:163], v[206:209], v[18:21]
	v_mfma_f32_16x16x32_bf16 v[6:9], v[152:155], v[214:217], v[6:9]
	v_mfma_f32_16x16x32_bf16 v[2:5], v[160:163], v[214:217], v[2:5]
	s_setprio 0
	s_barrier
	s_add_i32 s97, s97, 2
	s_add_u32 s10, s10, 0x100
	s_addc_u32 s11, s11, 0
	s_add_u32 s95, s95, 0x100
	s_addc_u32 s96, s96, 0
	s_cmp_gt_u32 s97, 29
	s_cbranch_scc0 .LBB0_1068
	s_and_b64 vcc, exec, s[44:45]
	s_cbranch_vccz .LBB0_1071
	s_barrier

.LBB0_1073:
	s_lshl_b32 s31, s88, 8
	s_or_b32 s31, s31, s2
	v_lshl_add_u32 v174, v42, 3, s31
	s_lshl_b64 s[10:11], s[10:11], 2
	s_add_u32 s10, s59, s10
	v_ashrrev_i32_e32 v175, 31, v174
	s_addc_u32 s11, s61, s11
	v_lshlrev_b64 v[176:177], 2, v[174:175]
	v_lshl_add_u64 v[46:47], s[10:11], 0, v[176:177]
	s_lshl_b32 s10, s21, 8
	s_add_i32 s10, s10, s60
	v_add_u32_e32 v178, s10, v148
	s_movk_i32 s21, 0x4000
	v_cmp_gt_i32_e32 vcc, s21, v178
	v_add_u32_e32 v148, 0xffffc000, v178
	v_ashrrev_i32_e32 v179, 31, v178
	v_cndmask_b32_e32 v149, 0, v179, vcc
	v_cndmask_b32_e32 v148, v148, v178, vcc
	v_mov_b32_e32 v188, s7
	v_mov_b32_e32 v189, s5
	v_mov_b32_e32 v190, s6
	v_mov_b32_e32 v191, s4
	v_cndmask_b32_e32 v151, v188, v189, vcc
	v_cndmask_b32_e32 v150, v190, v191, vcc
	v_lshlrev_b64 v[148:149], 13, v[148:149]
	v_lshl_add_u64 v[148:149], v[150:151], 0, v[148:149]
	v_lshl_add_u64 v[148:149], v[148:149], 0, v[176:177]
	global_load_dwordx4 v[66:69], v[46:47], off offset:16
	global_load_dwordx4 v[70:73], v[46:47], off
	global_load_dwordx4 v[42:45], v[46:47], off offset:528
	s_nop 0
	global_load_dwordx4 v[46:49], v[46:47], off offset:512
	s_nop 0
	global_load_dwordx4 v[192:195], v[148:149], off offset:16
	global_load_dwordx4 v[202:205], v[148:149], off
	global_load_dwordx4 v[206:209], v[148:149], off offset:528
	global_load_dwordx4 v[210:213], v[148:149], off offset:512
	v_add_u32_e32 v182, 16, v178
	v_cmp_gt_i32_e32 vcc, s21, v182
	v_add_u32_e32 v148, 0xffffc010, v178
	v_ashrrev_i32_e32 v183, 31, v182
	v_cndmask_b32_e32 v149, 0, v183, vcc
	v_cndmask_b32_e32 v148, v148, v182, vcc
	v_cndmask_b32_e32 v151, v188, v189, vcc
	v_cndmask_b32_e32 v150, v190, v191, vcc
	v_lshlrev_b64 v[148:149], 13, v[148:149]
	v_lshl_add_u64 v[148:149], v[150:151], 0, v[148:149]
	v_lshl_add_u64 v[152:153], v[148:149], 0, v[176:177]
	global_load_dwordx4 v[156:159], v[152:153], off offset:16
	global_load_dwordx4 v[160:163], v[152:153], off
	global_load_dwordx4 v[148:151], v[152:153], off offset:528
	s_nop 0
	global_load_dwordx4 v[152:155], v[152:153], off offset:512
	v_readlane_b32 s10, v251, 4
	v_lshlrev_b64 v[180:181], 12, v[178:179]
	v_readlane_b32 s11, v251, 5
	v_lshlrev_b64 v[174:175], 1, v[174:175]
	v_lshlrev_b64 v[182:183], 12, v[182:183]
	s_waitcnt vmcnt(0)
	v_pk_fma_f32 v[194:195], v[142:143], v[68:69], v[194:195]
	v_pk_fma_f32 v[144:145], v[144:145], v[70:71], v[202:203]
	v_pk_fma_f32 v[142:143], v[140:141], v[66:67], v[192:193]
	v_cvt_pk_bf16_f32 v140, v144, v145
	v_lshl_add_u64 v[144:145], s[10:11], 0, v[180:181]
	v_pk_fma_f32 v[146:147], v[146:147], v[72:73], v[204:205]
	v_lshl_add_u64 v[144:145], v[144:145], 0, v[174:175]
	v_cvt_pk_bf16_f32 v141, v146, v147
	v_cvt_pk_bf16_f32 v142, v142, v143
	v_cvt_pk_bf16_f32 v143, v194, v195
	global_store_dwordx4 v[144:145], v[140:143], off
	v_pk_fma_f32 v[136:137], v[136:137], v[46:47], v[210:211]
	v_add_u32_e32 v180, 32, v178
	v_pk_fma_f32 v[140:141], v[134:135], v[44:45], v[208:209]
	v_pk_fma_f32 v[134:135], v[132:133], v[42:43], v[206:207]
	v_cvt_pk_bf16_f32 v132, v136, v137
	v_pk_fma_f32 v[138:139], v[138:139], v[48:49], v[212:213]
	v_cmp_gt_i32_e32 vcc, s21, v180
	v_cvt_pk_bf16_f32 v133, v138, v139
	v_cvt_pk_bf16_f32 v134, v134, v135
	v_cvt_pk_bf16_f32 v135, v140, v141
	global_store_dwordx4 v[144:145], v[132:135], off offset:256
	v_ashrrev_i32_e32 v181, 31, v180
	v_pk_fma_f32 v[128:129], v[128:129], v[70:71], v[160:161]
	v_add_u32_e32 v132, 0xffffc020, v178
	v_cndmask_b32_e32 v133, 0, v181, vcc
	v_cndmask_b32_e32 v132, v132, v180, vcc
	v_cndmask_b32_e32 v135, v188, v189, vcc
	v_cndmask_b32_e32 v134, v190, v191, vcc
	v_lshlrev_b64 v[132:133], 13, v[132:133]
	v_lshl_add_u64 v[132:133], v[134:135], 0, v[132:133]
	v_lshl_add_u64 v[136:137], v[132:133], 0, v[176:177]
	global_load_dwordx4 v[140:143], v[136:137], off offset:16
	global_load_dwordx4 v[144:147], v[136:137], off
	global_load_dwordx4 v[132:135], v[136:137], off offset:528
	s_nop 0
	global_load_dwordx4 v[136:139], v[136:137], off offset:512
	v_pk_fma_f32 v[158:159], v[126:127], v[68:69], v[158:159]
	v_pk_fma_f32 v[126:127], v[124:125], v[66:67], v[156:157]
	v_cvt_pk_bf16_f32 v124, v128, v129
	v_lshl_add_u64 v[128:129], s[10:11], 0, v[182:183]
	v_pk_fma_f32 v[130:131], v[130:131], v[72:73], v[162:163]
	v_lshl_add_u64 v[128:129], v[128:129], 0, v[174:175]
	v_cvt_pk_bf16_f32 v125, v130, v131
	v_cvt_pk_bf16_f32 v126, v126, v127
	v_cvt_pk_bf16_f32 v127, v158, v159
	global_store_dwordx4 v[128:129], v[124:127], off
	v_pk_fma_f32 v[120:121], v[120:121], v[46:47], v[152:153]
	v_add_u32_e32 v130, 48, v178
	v_pk_fma_f32 v[124:125], v[118:119], v[44:45], v[150:151]
	v_pk_fma_f32 v[118:119], v[116:117], v[42:43], v[148:149]
	v_cvt_pk_bf16_f32 v116, v120, v121
	v_pk_fma_f32 v[122:123], v[122:123], v[48:49], v[154:155]
	v_cmp_gt_i32_e32 vcc, s21, v130
	v_cvt_pk_bf16_f32 v117, v122, v123
	v_cvt_pk_bf16_f32 v118, v118, v119
	v_cvt_pk_bf16_f32 v119, v124, v125
	global_store_dwordx4 v[128:129], v[116:119], off offset:256
	v_ashrrev_i32_e32 v131, 31, v130
	s_waitcnt vmcnt(5)
	v_pk_fma_f32 v[142:143], v[110:111], v[68:69], v[142:143]
	v_add_u32_e32 v116, 0xffffc030, v178
	v_cndmask_b32_e32 v117, 0, v131, vcc
	v_cndmask_b32_e32 v116, v116, v130, vcc
	v_cndmask_b32_e32 v119, v188, v189, vcc
	v_cndmask_b32_e32 v118, v190, v191, vcc
	v_lshlrev_b64 v[116:117], 13, v[116:117]
	v_lshl_add_u64 v[116:117], v[118:119], 0, v[116:117]
	v_lshl_add_u64 v[116:117], v[116:117], 0, v[176:177]
	global_load_dwordx4 v[118:121], v[116:117], off offset:16
	global_load_dwordx4 v[122:125], v[116:117], off
	global_load_dwordx4 v[126:129], v[116:117], off offset:528
	global_load_dwordx4 v[148:151], v[116:117], off offset:512
	v_lshlrev_b64 v[116:117], 12, v[180:181]
	s_waitcnt vmcnt(8)
	v_pk_fma_f32 v[112:113], v[112:113], v[70:71], v[144:145]
	v_pk_fma_f32 v[110:111], v[108:109], v[66:67], v[140:141]
	v_cvt_pk_bf16_f32 v108, v112, v113
	v_lshl_add_u64 v[112:113], s[10:11], 0, v[116:117]
	v_pk_fma_f32 v[114:115], v[114:115], v[72:73], v[146:147]
	v_lshl_add_u64 v[112:113], v[112:113], 0, v[174:175]
	v_cvt_pk_bf16_f32 v109, v114, v115
	v_cvt_pk_bf16_f32 v110, v110, v111
	v_cvt_pk_bf16_f32 v111, v142, v143
	global_store_dwordx4 v[112:113], v[108:111], off
	s_waitcnt vmcnt(7)
	v_pk_fma_f32 v[104:105], v[104:105], v[46:47], v[136:137]
	v_add_u32_e32 v116, 0x80, v178
	v_pk_fma_f32 v[108:109], v[102:103], v[44:45], v[134:135]
	v_pk_fma_f32 v[102:103], v[100:101], v[42:43], v[132:133]
	v_cvt_pk_bf16_f32 v100, v104, v105
	v_pk_fma_f32 v[106:107], v[106:107], v[48:49], v[138:139]
	v_cmp_gt_i32_e32 vcc, s21, v116
	v_cvt_pk_bf16_f32 v101, v106, v107
	v_cvt_pk_bf16_f32 v102, v102, v103
	v_cvt_pk_bf16_f32 v103, v108, v109
	global_store_dwordx4 v[112:113], v[100:103], off offset:256
	v_ashrrev_i32_e32 v117, 31, v116
	v_lshlrev_b64 v[130:131], 12, v[130:131]
	v_add_u32_e32 v100, 0xffffc080, v178
	v_cndmask_b32_e32 v101, 0, v117, vcc
	v_cndmask_b32_e32 v100, v100, v116, vcc
	v_cndmask_b32_e32 v103, v188, v189, vcc
	v_cndmask_b32_e32 v102, v190, v191, vcc
	v_lshlrev_b64 v[100:101], 13, v[100:101]
	v_lshl_add_u64 v[100:101], v[102:103], 0, v[100:101]
	v_lshl_add_u64 v[104:105], v[100:101], 0, v[176:177]
	global_load_dwordx4 v[108:111], v[104:105], off offset:16
	global_load_dwordx4 v[112:115], v[104:105], off
	global_load_dwordx4 v[100:103], v[104:105], off offset:528
	s_nop 0
	global_load_dwordx4 v[104:107], v[104:105], off offset:512
	s_waitcnt vmcnt(9)
	v_pk_fma_f32 v[120:121], v[92:93], v[68:69], v[120:121]
	s_waitcnt vmcnt(8)
	v_pk_fma_f32 v[94:95], v[94:95], v[70:71], v[122:123]
	v_pk_fma_f32 v[92:93], v[90:91], v[66:67], v[118:119]
	v_cvt_pk_bf16_f32 v90, v94, v95
	v_lshl_add_u64 v[94:95], s[10:11], 0, v[130:131]
	v_pk_fma_f32 v[96:97], v[96:97], v[72:73], v[124:125]
	v_lshl_add_u64 v[94:95], v[94:95], 0, v[174:175]
	v_cvt_pk_bf16_f32 v91, v96, v97
	s_waitcnt vmcnt(6)
	v_pk_fma_f32 v[88:89], v[88:89], v[48:49], v[150:151]
	v_cvt_pk_bf16_f32 v92, v92, v93
	v_cvt_pk_bf16_f32 v93, v120, v121
	global_store_dwordx4 v[94:95], v[90:93], off
	v_pk_fma_f32 v[86:87], v[86:87], v[46:47], v[148:149]
	s_waitcnt vmcnt(4)
	v_pk_fma_f32 v[110:111], v[76:77], v[68:69], v[110:111]
	v_pk_fma_f32 v[90:91], v[84:85], v[44:45], v[128:129]
	v_pk_fma_f32 v[84:85], v[82:83], v[42:43], v[126:127]
	v_cvt_pk_bf16_f32 v82, v86, v87
	v_cvt_pk_bf16_f32 v83, v88, v89
	v_add_u32_e32 v88, 0x90, v178
	v_cvt_pk_bf16_f32 v84, v84, v85
	v_cvt_pk_bf16_f32 v85, v90, v91
	global_store_dwordx4 v[94:95], v[82:85], off offset:256
	v_cmp_gt_i32_e32 vcc, s21, v88
	v_ashrrev_i32_e32 v89, 31, v88
	v_add_u32_e32 v82, 0xffffc090, v178
	v_cndmask_b32_e32 v83, 0, v89, vcc
	v_cndmask_b32_e32 v82, v82, v88, vcc
	v_cndmask_b32_e32 v85, v188, v189, vcc
	v_cndmask_b32_e32 v84, v190, v191, vcc
	v_lshlrev_b64 v[82:83], 13, v[82:83]
	v_lshl_add_u64 v[82:83], v[84:85], 0, v[82:83]
	v_lshl_add_u64 v[86:87], v[82:83], 0, v[176:177]
	global_load_dwordx4 v[82:85], v[86:87], off offset:16
	global_load_dwordx4 v[90:93], v[86:87], off
	global_load_dwordx4 v[94:97], v[86:87], off offset:528
	global_load_dwordx4 v[118:121], v[86:87], off offset:512
	v_lshlrev_b64 v[86:87], 12, v[116:117]
	s_waitcnt vmcnt(8)
	v_pk_fma_f32 v[78:79], v[78:79], v[70:71], v[112:113]
	v_pk_fma_f32 v[76:77], v[74:75], v[66:67], v[108:109]
	v_cvt_pk_bf16_f32 v74, v78, v79
	v_lshl_add_u64 v[78:79], s[10:11], 0, v[86:87]
	v_pk_fma_f32 v[80:81], v[80:81], v[72:73], v[114:115]
	v_lshl_add_u64 v[78:79], v[78:79], 0, v[174:175]
	v_cvt_pk_bf16_f32 v75, v80, v81
	v_cvt_pk_bf16_f32 v76, v76, v77
	v_cvt_pk_bf16_f32 v77, v110, v111
	global_store_dwordx4 v[78:79], v[74:77], off
	s_waitcnt vmcnt(7)
	v_pk_fma_f32 v[62:63], v[62:63], v[46:47], v[104:105]
	v_add_u32_e32 v86, 0xa0, v178
	v_pk_fma_f32 v[74:75], v[60:61], v[44:45], v[102:103]
	v_pk_fma_f32 v[60:61], v[58:59], v[42:43], v[100:101]
	v_cvt_pk_bf16_f32 v58, v62, v63
	v_pk_fma_f32 v[64:65], v[64:65], v[48:49], v[106:107]
	v_cmp_gt_i32_e32 vcc, s21, v86
	v_cvt_pk_bf16_f32 v59, v64, v65
	v_cvt_pk_bf16_f32 v60, v60, v61
	v_cvt_pk_bf16_f32 v61, v74, v75
	global_store_dwordx4 v[78:79], v[58:61], off offset:256
	v_ashrrev_i32_e32 v87, 31, v86
	v_lshlrev_b64 v[88:89], 12, v[88:89]
	v_add_u32_e32 v58, 0xffffc0a0, v178
	v_cndmask_b32_e32 v59, 0, v87, vcc
	v_cndmask_b32_e32 v58, v58, v86, vcc
	v_cndmask_b32_e32 v61, v188, v189, vcc
	v_cndmask_b32_e32 v60, v190, v191, vcc
	v_lshlrev_b64 v[58:59], 13, v[58:59]
	v_lshl_add_u64 v[58:59], v[60:61], 0, v[58:59]
	v_lshl_add_u64 v[62:63], v[58:59], 0, v[176:177]
	global_load_dwordx4 v[74:77], v[62:63], off offset:16
	global_load_dwordx4 v[78:81], v[62:63], off
	global_load_dwordx4 v[58:61], v[62:63], off offset:528
	s_nop 0
	global_load_dwordx4 v[62:65], v[62:63], off offset:512
	s_waitcnt vmcnt(9)
	v_pk_fma_f32 v[84:85], v[52:53], v[68:69], v[84:85]
	s_waitcnt vmcnt(8)
	v_pk_fma_f32 v[54:55], v[54:55], v[70:71], v[90:91]
	v_pk_fma_f32 v[52:53], v[50:51], v[66:67], v[82:83]
	v_cvt_pk_bf16_f32 v50, v54, v55
	v_lshl_add_u64 v[54:55], s[10:11], 0, v[88:89]
	v_pk_fma_f32 v[56:57], v[56:57], v[72:73], v[92:93]
	v_lshl_add_u64 v[54:55], v[54:55], 0, v[174:175]
	v_cvt_pk_bf16_f32 v51, v56, v57
	v_cvt_pk_bf16_f32 v52, v52, v53
	v_cvt_pk_bf16_f32 v53, v84, v85
	global_store_dwordx4 v[54:55], v[50:53], off
	s_waitcnt vmcnt(7)
	v_pk_fma_f32 v[40:41], v[40:41], v[48:49], v[120:121]
	v_pk_fma_f32 v[38:39], v[38:39], v[46:47], v[118:119]
	v_pk_fma_f32 v[50:51], v[36:37], v[44:45], v[96:97]
	v_pk_fma_f32 v[36:37], v[34:35], v[42:43], v[94:95]
	v_cvt_pk_bf16_f32 v34, v38, v39
	v_cvt_pk_bf16_f32 v35, v40, v41
	v_lshlrev_b64 v[56:57], 12, v[86:87]
	v_cvt_pk_bf16_f32 v36, v36, v37
	v_cvt_pk_bf16_f32 v37, v50, v51
	global_store_dwordx4 v[54:55], v[34:37], off offset:256
	v_add_u32_e32 v54, 0xb0, v178
	v_cmp_gt_i32_e32 vcc, s21, v54
	v_ashrrev_i32_e32 v55, 31, v54
	v_add_u32_e32 v34, 0xffffc0b0, v178
	v_cndmask_b32_e32 v35, 0, v55, vcc
	v_cndmask_b32_e32 v34, v34, v54, vcc
	v_cndmask_b32_e32 v37, v188, v189, vcc
	v_cndmask_b32_e32 v36, v190, v191, vcc
	v_lshlrev_b64 v[34:35], 13, v[34:35]
	v_lshl_add_u64 v[34:35], v[36:37], 0, v[34:35]
	v_lshl_add_u64 v[50:51], v[34:35], 0, v[176:177]
	global_load_dwordx4 v[34:37], v[50:51], off offset:16
	global_load_dwordx4 v[82:85], v[50:51], off
	global_load_dwordx4 v[38:41], v[50:51], off offset:528
	s_nop 0
	global_load_dwordx4 v[50:53], v[50:51], off offset:512
	s_waitcnt vmcnt(9)
	v_pk_fma_f32 v[76:77], v[28:29], v[68:69], v[76:77]
	s_waitcnt vmcnt(8)
	v_pk_fma_f32 v[30:31], v[30:31], v[70:71], v[78:79]
	v_pk_fma_f32 v[28:29], v[26:27], v[66:67], v[74:75]
	v_cvt_pk_bf16_f32 v26, v30, v31
	v_lshl_add_u64 v[30:31], s[10:11], 0, v[56:57]
	v_pk_fma_f32 v[32:33], v[32:33], v[72:73], v[80:81]
	v_lshl_add_u64 v[30:31], v[30:31], 0, v[174:175]
	v_cvt_pk_bf16_f32 v27, v32, v33
	v_cvt_pk_bf16_f32 v28, v28, v29
	v_cvt_pk_bf16_f32 v29, v76, v77
	global_store_dwordx4 v[30:31], v[26:29], off
	s_waitcnt vmcnt(7)
	v_pk_fma_f32 v[24:25], v[24:25], v[48:49], v[64:65]
	v_pk_fma_f32 v[22:23], v[22:23], v[46:47], v[62:63]
	v_pk_fma_f32 v[26:27], v[20:21], v[44:45], v[60:61]
	v_pk_fma_f32 v[20:21], v[18:19], v[42:43], v[58:59]
	v_cvt_pk_bf16_f32 v18, v22, v23
	v_cvt_pk_bf16_f32 v19, v24, v25
	s_andn2_b64 vcc, exec, s[40:41]
	v_cvt_pk_bf16_f32 v20, v20, v21
	v_cvt_pk_bf16_f32 v21, v26, v27
	global_store_dwordx4 v[30:31], v[18:21], off offset:256
	s_waitcnt vmcnt(4)
	v_pk_fma_f32 v[14:15], v[14:15], v[70:71], v[82:83]
	v_lshlrev_b64 v[18:19], 12, v[54:55]
	v_pk_fma_f32 v[20:21], v[12:13], v[68:69], v[36:37]
	v_pk_fma_f32 v[12:13], v[10:11], v[66:67], v[34:35]
	v_cvt_pk_bf16_f32 v10, v14, v15
	v_lshl_add_u64 v[14:15], s[10:11], 0, v[18:19]
	v_pk_fma_f32 v[16:17], v[16:17], v[72:73], v[84:85]
	v_lshl_add_u64 v[14:15], v[14:15], 0, v[174:175]
	v_cvt_pk_bf16_f32 v11, v16, v17
	v_cvt_pk_bf16_f32 v12, v12, v13
	v_cvt_pk_bf16_f32 v13, v20, v21
	global_store_dwordx4 v[14:15], v[10:13], off
	s_waitcnt vmcnt(3)
	v_pk_fma_f32 v[8:9], v[8:9], v[48:49], v[52:53]
	v_pk_fma_f32 v[6:7], v[6:7], v[46:47], v[50:51]
	v_pk_fma_f32 v[10:11], v[4:5], v[44:45], v[40:41]
	v_pk_fma_f32 v[4:5], v[2:3], v[42:43], v[38:39]
	v_cvt_pk_bf16_f32 v2, v6, v7
	v_cvt_pk_bf16_f32 v3, v8, v9
	s_mov_b64 s[10:11], -1
	v_cvt_pk_bf16_f32 v4, v4, v5
	v_cvt_pk_bf16_f32 v5, v10, v11
	global_store_dwordx4 v[14:15], v[2:5], off offset:256
	s_mov_b64 s[100:101], -1
	s_cbranch_vccnz .LBB0_1064
	s_andn2_b64 vcc, exec, s[8:9]
	s_cbranch_vccnz .LBB0_1063
	s_barrier
	s_branch .LBB0_1063

.LBB0_1419:
	s_mov_b64 s[100:101], 0
	s_cmp_le_i32 s92, s2
	s_cselect_b64 s[4:5], -1, 0
	s_cmp_lt_i32 s2, s93
	s_cselect_b64 s[6:7], -1, 0
	s_and_b64 s[6:7], s[4:5], s[6:7]
	s_mov_b64 s[4:5], -1
	s_and_b64 vcc, exec, s[6:7]
	s_cbranch_vccnz .LBB0_1421
	v_readlane_b32 s2, v255, 4
	s_add_i32 s2, s2, 11
	s_mov_b64 s[4:5], 0

.LBB0_1432:
	s_mov_b64 vcc, s[100:101]
	s_cbranch_vccnz .Lepw8
	s_waitcnt vmcnt(8)
.Lepw8:
	s_add_u32 s31, s46, 0x80
	s_waitcnt lgkmcnt(0)
	s_addc_u32 s50, s47, 0
	s_and_b64 s[48:49], s[48:49], exec
	v_mov_b32_e32 v211, v99
	s_cselect_b32 s49, s21, s68
	s_cselect_b32 s48, s41, s43
	s_cselect_b32 s51, s77, s50
	s_cselect_b32 s50, s76, s31
	s_barrier
	s_setprio 1
	s_waitcnt lgkmcnt(0)
	v_mfma_scale_f32_16x16x128_f8f6f4 v[192:195], v[18:25], v[58:65], v[192:195], v224, v224 op_sel_hi:[0,0,0]
	v_mfma_scale_f32_16x16x128_f8f6f4 v[184:187], v[26:33], v[58:65], v[184:187], v224, v224 op_sel_hi:[0,0,0]
	v_mfma_scale_f32_16x16x128_f8f6f4 v[176:179], v[18:25], v[50:57], v[176:179], v224, v224 op_sel_hi:[0,0,0]
	v_mfma_scale_f32_16x16x128_f8f6f4 v[168:171], v[26:33], v[50:57], v[168:171], v224, v224 op_sel_hi:[0,0,0]
	v_mfma_scale_f32_16x16x128_f8f6f4 v[160:163], v[18:25], v[42:49], v[160:163], v224, v224 op_sel_hi:[0,0,0]
	v_mfma_scale_f32_16x16x128_f8f6f4 v[152:155], v[26:33], v[42:49], v[152:155], v224, v224 op_sel_hi:[0,0,0]
	v_mfma_scale_f32_16x16x128_f8f6f4 v[144:147], v[18:25], v[34:41], v[144:147], v224, v224 op_sel_hi:[0,0,0]
	v_mfma_scale_f32_16x16x128_f8f6f4 v[136:139], v[26:33], v[34:41], v[136:139], v224, v224 op_sel_hi:[0,0,0]
	s_setprio 0
	s_setprio 1
	v_mfma_scale_f32_16x16x128_f8f6f4 v[188:191], v[2:9], v[58:65], v[188:191], v224, v224 op_sel_hi:[0,0,0]
	v_mfma_scale_f32_16x16x128_f8f6f4 v[180:183], v[10:17], v[58:65], v[180:183], v224, v224 op_sel_hi:[0,0,0]
	v_mfma_scale_f32_16x16x128_f8f6f4 v[172:175], v[2:9], v[50:57], v[172:175], v224, v224 op_sel_hi:[0,0,0]
	v_mfma_scale_f32_16x16x128_f8f6f4 v[164:167], v[10:17], v[50:57], v[164:167], v224, v224 op_sel_hi:[0,0,0]
	v_mfma_scale_f32_16x16x128_f8f6f4 v[156:159], v[2:9], v[42:49], v[156:159], v224, v224 op_sel_hi:[0,0,0]
	v_mfma_scale_f32_16x16x128_f8f6f4 v[148:151], v[10:17], v[42:49], v[148:151], v224, v224 op_sel_hi:[0,0,0]
	v_mfma_scale_f32_16x16x128_f8f6f4 v[140:143], v[2:9], v[34:41], v[140:143], v224, v224 op_sel_hi:[0,0,0]
	v_mfma_scale_f32_16x16x128_f8f6f4 v[132:135], v[10:17], v[34:41], v[132:135], v224, v224 op_sel_hi:[0,0,0]
	s_setprio 0
	s_barrier
	s_mov_b32 m0, s17
	v_lshl_add_u64 v[196:197], s[48:49], 0, v[204:205]
	s_add_u32 s90, s48, 0x40000
	ds_read_b128 v[34:37], v219 offset:16384
	ds_read_b128 v[38:41], v219 offset:17408
	ds_read_b128 v[42:45], v219 offset:18432
	ds_read_b128 v[46:49], v219 offset:19456
	ds_read_b128 v[50:53], v219 offset:20480
	ds_read_b128 v[54:57], v219 offset:21504
	ds_read_b128 v[58:61], v219 offset:22528
	ds_read_b128 v[62:65], v219 offset:23552
	global_load_lds_dwordx4 v[196:197], off
	v_lshl_add_u64 v[226:227], s[48:49], 0, v[202:203]
	s_mov_b32 m0, s18
	s_addc_u32 s91, s49, 0
	global_load_lds_dwordx4 v[226:227], off
	v_lshl_add_u64 v[228:229], s[90:91], 0, v[204:205]
	s_mov_b32 m0, s19
	v_mov_b32_e32 v207, v99
	global_load_lds_dwordx4 v[228:229], off
	v_lshl_add_u64 v[228:229], s[90:91], 0, v[202:203]
	s_mov_b32 m0, s20
	v_lshl_add_u64 v[238:239], s[50:51], 0, v[206:207]
	global_load_lds_dwordx4 v[228:229], off
	s_mov_b32 m0, s2
	v_lshl_add_u64 v[228:229], s[50:51], 0, v[98:99]
	global_load_lds_dwordx4 v98, s[50:51]
	s_mov_b32 m0, s24
	s_nop 0
	global_load_lds_dwordx4 v206, s[50:51]
	s_mov_b64 vcc, s[100:101]
	s_cbranch_vccnz .Lepw7
	s_waitcnt vmcnt(8)
.Lepw7:
	s_waitcnt lgkmcnt(0)
	s_barrier
	s_setprio 1
	s_waitcnt lgkmcnt(0)
	v_mfma_scale_f32_16x16x128_f8f6f4 v[128:131], v[18:25], v[34:41], v[128:131], v224, v224 op_sel_hi:[0,0,0]
	v_mfma_scale_f32_16x16x128_f8f6f4 v[120:123], v[26:33], v[34:41], v[120:123], v224, v224 op_sel_hi:[0,0,0]
	v_mfma_scale_f32_16x16x128_f8f6f4 v[112:115], v[18:25], v[42:49], v[112:115], v224, v224 op_sel_hi:[0,0,0]
	v_mfma_scale_f32_16x16x128_f8f6f4 v[104:107], v[26:33], v[42:49], v[104:107], v224, v224 op_sel_hi:[0,0,0]
	v_mfma_scale_f32_16x16x128_f8f6f4 v[94:97], v[18:25], v[50:57], v[94:97], v224, v224 op_sel_hi:[0,0,0]
	v_mfma_scale_f32_16x16x128_f8f6f4 v[86:89], v[26:33], v[50:57], v[86:89], v224, v224 op_sel_hi:[0,0,0]
	v_mfma_scale_f32_16x16x128_f8f6f4 v[78:81], v[18:25], v[58:65], v[78:81], v224, v224 op_sel_hi:[0,0,0]
	v_mfma_scale_f32_16x16x128_f8f6f4 v[70:73], v[26:33], v[58:65], v[70:73], v224, v224 op_sel_hi:[0,0,0]
	s_setprio 0
	s_setprio 1
	v_mfma_scale_f32_16x16x128_f8f6f4 v[124:127], v[2:9], v[34:41], v[124:127], v224, v224 op_sel_hi:[0,0,0]
	v_mfma_scale_f32_16x16x128_f8f6f4 v[116:119], v[10:17], v[34:41], v[116:119], v224, v224 op_sel_hi:[0,0,0]
	v_mfma_scale_f32_16x16x128_f8f6f4 v[108:111], v[2:9], v[42:49], v[108:111], v224, v224 op_sel_hi:[0,0,0]
	v_mfma_scale_f32_16x16x128_f8f6f4 v[100:103], v[10:17], v[42:49], v[100:103], v224, v224 op_sel_hi:[0,0,0]
	v_mfma_scale_f32_16x16x128_f8f6f4 v[90:93], v[2:9], v[50:57], v[90:93], v224, v224 op_sel_hi:[0,0,0]
	v_mfma_scale_f32_16x16x128_f8f6f4 v[82:85], v[10:17], v[50:57], v[82:85], v224, v224 op_sel_hi:[0,0,0]
	v_mfma_scale_f32_16x16x128_f8f6f4 v[74:77], v[2:9], v[58:65], v[74:77], v224, v224 op_sel_hi:[0,0,0]
	v_mfma_scale_f32_16x16x128_f8f6f4 v[66:69], v[10:17], v[58:65], v[66:69], v224, v224 op_sel_hi:[0,0,0]
	s_setprio 0
	s_barrier
	ds_read_b128 v[2:5], v218 offset:32768
	ds_read_b128 v[6:9], v218 offset:33792
	ds_read_b128 v[10:13], v218 offset:34816
	ds_read_b128 v[14:17], v218 offset:35840
	ds_read_b128 v[18:21], v218 offset:49152
	ds_read_b128 v[22:25], v218 offset:50176
	ds_read_b128 v[26:29], v218 offset:51200
	ds_read_b128 v[30:33], v218 offset:52224
	s_mov_b32 m0, s27
	v_lshl_add_u64 v[240:241], s[50:51], 0, v[208:209]
	ds_read_b128 v[34:37], v219 offset:32768
	ds_read_b128 v[38:41], v219 offset:33792
	ds_read_b128 v[42:45], v219 offset:34816
	ds_read_b128 v[46:49], v219 offset:35840
	ds_read_b128 v[50:53], v219 offset:36864
	ds_read_b128 v[54:57], v219 offset:37888
	ds_read_b128 v[58:61], v219 offset:38912
	ds_read_b128 v[62:65], v219 offset:39936
	global_load_lds_dwordx4 v[240:241], off
	v_lshl_add_u64 v[240:241], s[50:51], 0, v[210:211]
	s_mov_b32 m0, s28
	s_nop 0
	global_load_lds_dwordx4 v[240:241], off
	s_waitcnt vmcnt(8)
	s_mov_b64 s[100:101], 0
	s_waitcnt lgkmcnt(0)
	s_barrier
	s_setprio 1
	s_waitcnt lgkmcnt(0)
	v_mfma_scale_f32_16x16x128_f8f6f4 v[192:195], v[2:9], v[34:41], v[192:195], v224, v224 op_sel_hi:[0,0,0]
	v_mfma_scale_f32_16x16x128_f8f6f4 v[184:187], v[10:17], v[34:41], v[184:187], v224, v224 op_sel_hi:[0,0,0]
	v_mfma_scale_f32_16x16x128_f8f6f4 v[176:179], v[2:9], v[42:49], v[176:179], v224, v224 op_sel_hi:[0,0,0]
	v_mfma_scale_f32_16x16x128_f8f6f4 v[168:171], v[10:17], v[42:49], v[168:171], v224, v224 op_sel_hi:[0,0,0]
	v_mfma_scale_f32_16x16x128_f8f6f4 v[160:163], v[2:9], v[50:57], v[160:163], v224, v224 op_sel_hi:[0,0,0]
	v_mfma_scale_f32_16x16x128_f8f6f4 v[152:155], v[10:17], v[50:57], v[152:155], v224, v224 op_sel_hi:[0,0,0]
	v_mfma_scale_f32_16x16x128_f8f6f4 v[144:147], v[2:9], v[58:65], v[144:147], v224, v224 op_sel_hi:[0,0,0]
	v_mfma_scale_f32_16x16x128_f8f6f4 v[136:139], v[10:17], v[58:65], v[136:139], v224, v224 op_sel_hi:[0,0,0]
	s_setprio 0
	s_setprio 1
	v_mfma_scale_f32_16x16x128_f8f6f4 v[188:191], v[18:25], v[34:41], v[188:191], v224, v224 op_sel_hi:[0,0,0]
	v_mfma_scale_f32_16x16x128_f8f6f4 v[180:183], v[26:33], v[34:41], v[180:183], v224, v224 op_sel_hi:[0,0,0]
	v_mfma_scale_f32_16x16x128_f8f6f4 v[172:175], v[18:25], v[42:49], v[172:175], v224, v224 op_sel_hi:[0,0,0]
	v_mfma_scale_f32_16x16x128_f8f6f4 v[164:167], v[26:33], v[42:49], v[164:167], v224, v224 op_sel_hi:[0,0,0]
	v_mfma_scale_f32_16x16x128_f8f6f4 v[156:159], v[18:25], v[50:57], v[156:159], v224, v224 op_sel_hi:[0,0,0]
	v_mfma_scale_f32_16x16x128_f8f6f4 v[148:151], v[26:33], v[50:57], v[148:151], v224, v224 op_sel_hi:[0,0,0]
	v_mfma_scale_f32_16x16x128_f8f6f4 v[140:143], v[18:25], v[58:65], v[140:143], v224, v224 op_sel_hi:[0,0,0]
	v_mfma_scale_f32_16x16x128_f8f6f4 v[132:135], v[26:33], v[58:65], v[132:135], v224, v224 op_sel_hi:[0,0,0]
	s_setprio 0
	s_barrier
	s_mov_b32 m0, s57
	v_lshl_add_u64 v[196:197], v[196:197], 0, s[62:63]
	s_add_u32 s48, s48, 0x40080
	ds_read_b128 v[34:37], v219 offset:49152
	ds_read_b128 v[38:41], v219 offset:50176
	ds_read_b128 v[42:45], v219 offset:51200
	ds_read_b128 v[46:49], v219 offset:52224
	ds_read_b128 v[50:53], v219 offset:53248
	ds_read_b128 v[54:57], v219 offset:54272
	ds_read_b128 v[58:61], v219 offset:55296
	ds_read_b128 v[62:65], v219 offset:56320
	global_load_lds_dwordx4 v[196:197], off
	v_lshl_add_u64 v[196:197], v[226:227], 0, s[62:63]
	s_mov_b32 m0, s58
	s_addc_u32 s49, s49, 0
	global_load_lds_dwordx4 v[196:197], off
	v_lshl_add_u64 v[196:197], s[48:49], 0, v[204:205]
	s_mov_b32 m0, s61
	s_nop 0
	global_load_lds_dwordx4 v[196:197], off
	v_lshl_add_u64 v[196:197], s[48:49], 0, v[202:203]
	s_mov_b32 m0, s65
	s_nop 0
	global_load_lds_dwordx4 v[196:197], off
	v_lshl_add_u64 v[196:197], v[228:229], 0, s[62:63]
	s_mov_b32 m0, s59
	s_nop 0
	global_load_lds_dwordx4 v[196:197], off
	v_lshl_add_u64 v[196:197], v[238:239], 0, s[62:63]
	s_mov_b32 m0, s60
	s_nop 0
	global_load_lds_dwordx4 v[196:197], off
	s_waitcnt vmcnt(8)
	s_waitcnt lgkmcnt(0)
	s_barrier
	s_setprio 1
	s_waitcnt lgkmcnt(0)
	v_mfma_scale_f32_16x16x128_f8f6f4 v[128:131], v[2:9], v[34:41], v[128:131], v224, v224 op_sel_hi:[0,0,0]
	v_mfma_scale_f32_16x16x128_f8f6f4 v[120:123], v[10:17], v[34:41], v[120:123], v224, v224 op_sel_hi:[0,0,0]
	v_mfma_scale_f32_16x16x128_f8f6f4 v[112:115], v[2:9], v[42:49], v[112:115], v224, v224 op_sel_hi:[0,0,0]
	v_mfma_scale_f32_16x16x128_f8f6f4 v[104:107], v[10:17], v[42:49], v[104:107], v224, v224 op_sel_hi:[0,0,0]
	v_mfma_scale_f32_16x16x128_f8f6f4 v[94:97], v[2:9], v[50:57], v[94:97], v224, v224 op_sel_hi:[0,0,0]
	v_mfma_scale_f32_16x16x128_f8f6f4 v[86:89], v[10:17], v[50:57], v[86:89], v224, v224 op_sel_hi:[0,0,0]
	v_mfma_scale_f32_16x16x128_f8f6f4 v[78:81], v[2:9], v[58:65], v[78:81], v224, v224 op_sel_hi:[0,0,0]
	v_mfma_scale_f32_16x16x128_f8f6f4 v[70:73], v[10:17], v[58:65], v[70:73], v224, v224 op_sel_hi:[0,0,0]
	s_setprio 0
	s_setprio 1
	v_mfma_scale_f32_16x16x128_f8f6f4 v[124:127], v[18:25], v[34:41], v[124:127], v224, v224 op_sel_hi:[0,0,0]
	v_mfma_scale_f32_16x16x128_f8f6f4 v[116:119], v[26:33], v[34:41], v[116:119], v224, v224 op_sel_hi:[0,0,0]
	v_mfma_scale_f32_16x16x128_f8f6f4 v[108:111], v[18:25], v[42:49], v[108:111], v224, v224 op_sel_hi:[0,0,0]
	v_mfma_scale_f32_16x16x128_f8f6f4 v[100:103], v[26:33], v[42:49], v[100:103], v224, v224 op_sel_hi:[0,0,0]
	v_mfma_scale_f32_16x16x128_f8f6f4 v[90:93], v[18:25], v[50:57], v[90:93], v224, v224 op_sel_hi:[0,0,0]
	v_mfma_scale_f32_16x16x128_f8f6f4 v[82:85], v[26:33], v[50:57], v[82:85], v224, v224 op_sel_hi:[0,0,0]
	v_mfma_scale_f32_16x16x128_f8f6f4 v[74:77], v[18:25], v[58:65], v[74:77], v224, v224 op_sel_hi:[0,0,0]
	v_mfma_scale_f32_16x16x128_f8f6f4 v[66:69], v[26:33], v[58:65], v[66:69], v224, v224 op_sel_hi:[0,0,0]
	s_setprio 0
	s_barrier
	s_add_i32 s83, s83, 2
	s_add_u32 s46, s46, 0x100
	s_addc_u32 s47, s47, 0
	s_add_u32 s43, s43, 0x100
	s_addc_u32 s68, s68, 0
	s_cmp_gt_u32 s83, 13
	s_cbranch_scc1 .LBB0_1435

.LBB0_1437:
	s_lshl_b32 s21, s11, 8
	s_ashr_i32 s11, s10, 31
	s_lshl_b64 s[10:11], s[10:11], 13
	s_add_u32 s31, s29, s10
	s_addc_u32 s41, s55, s11
	v_readlane_b32 s10, v253, 36
	v_readlane_b32 s11, v253, 37
	s_lshl_b32 s10, s10, 7
	s_ashr_i32 s11, s10, 31
	v_mov_b32_e32 v2, v216
	v_mov_b32_e32 v20, v201
	s_lshl_b64 s[46:47], s[10:11], 2
	s_add_u32 s46, s31, s46
	v_lshl_add_u32 v18, v2, 3, s13
	s_addc_u32 s47, s41, s47
	v_ashrrev_i32_e32 v19, 31, v18
	v_lshl_add_u64 v[6:7], v[18:19], 2, s[46:47]
	s_mov_b64 s[46:47], 0x1000
	v_lshl_add_u64 v[8:9], v[6:7], 0, s[46:47]
	global_load_dwordx4 v[2:5], v[6:7], off offset:16
	global_load_dwordx4 v[10:13], v[6:7], off
	v_add_co_u32_e32 v6, vcc, s88, v6
	s_add_i32 s21, s21, s56
	s_nop 0
	v_addc_co_u32_e32 v7, vcc, 0, v7, vcc
	global_load_dwordx4 v[14:17], v[6:7], off
	s_nop 0
	global_load_dwordx4 v[6:9], v[8:9], off offset:16
	v_add_u32_e32 v20, s21, v20
	v_ashrrev_i32_e32 v21, 31, v20
	v_lshlrev_b64 v[20:21], 10, v[20:21]
	v_lshl_add_u64 v[20:21], s[80:81], 0, v[20:21]
	v_lshl_add_u64 v[20:21], v[20:21], 0, s[10:11]
	v_lshl_add_u64 v[18:19], v[20:21], 0, v[18:19]
	v_mov_b32_e32 v20, v99
	v_mov_b32_e32 v21, v99
	s_movk_i32 s10, 0x4000
	v_readlane_b32 s83, v255, 2
	s_waitcnt vmcnt(0)
	v_add_f32_e32 v22, v192, v10
	v_min_f32_e32 v22, 0x40e00000, v22
	v_add_f32_e32 v23, v188, v14
	v_med3_f32 v23, v23, s26, v236
	v_add_f32_e32 v23, 1.0, v23
	v_mul_f32_e32 v23, v22, v23
	v_mul_f32_e32 v22, 0xc01d265f, v22
	v_exp_f32_e32 v22, v22
	v_add_f32_e32 v24, v189, v15
	v_med3_f32 v24, v24, s26, v236
	v_add_f32_e32 v24, 1.0, v24
	v_add_f32_e32 v22, 1.0, v22
	v_rcp_f32_e32 v22, v22
	v_add_f32_e32 v25, v190, v16
	v_med3_f32 v25, v25, s26, v236
	v_add_f32_e32 v25, 1.0, v25
	v_mul_f32_e32 v22, v23, v22
	v_add_f32_e32 v23, v193, v11
	v_min_f32_e32 v23, 0x40e00000, v23
	v_mul_f32_e32 v24, v23, v24
	v_mul_f32_e32 v23, 0xc01d265f, v23
	v_exp_f32_e32 v23, v23
	v_add_f32_e32 v26, v191, v17
	v_med3_f32 v26, v26, s26, v236
	v_add_f32_e32 v26, 1.0, v26
	v_add_f32_e32 v23, 1.0, v23
	v_rcp_f32_e32 v23, v23
	v_add_f32_e32 v27, v180, v6
	v_med3_f32 v27, v27, s26, v236
	v_add_f32_e32 v27, 1.0, v27
	v_mul_f32_e32 v23, v24, v23
	v_add_f32_e32 v24, v194, v12
	v_min_f32_e32 v24, 0x40e00000, v24
	v_mul_f32_e32 v25, v24, v25
	v_mul_f32_e32 v24, 0xc01d265f, v24
	v_exp_f32_e32 v24, v24
	v_add_f32_e32 v28, v181, v7
	v_med3_f32 v28, v28, s26, v236
	v_add_f32_e32 v28, 1.0, v28
	v_add_f32_e32 v24, 1.0, v24
	v_rcp_f32_e32 v24, v24
	v_add_f32_e32 v29, v182, v8
	v_med3_f32 v29, v29, s26, v236
	v_add_f32_e32 v29, 1.0, v29
	v_mul_f32_e32 v24, v25, v24
	v_add_f32_e32 v25, v195, v13
	v_min_f32_e32 v25, 0x40e00000, v25
	v_mul_f32_e32 v26, v25, v26
	v_mul_f32_e32 v25, 0xc01d265f, v25
	v_exp_f32_e32 v25, v25
	v_add_f32_e32 v30, v183, v9
	v_med3_f32 v30, v30, s26, v236
	v_add_f32_e32 v30, 1.0, v30
	v_add_f32_e32 v25, 1.0, v25
	v_rcp_f32_e32 v25, v25
	v_cvt_pk_fp8_f32 v20, v22, v23
	v_add_f32_e32 v22, v173, v15
	v_med3_f32 v22, v22, s26, v236
	v_mul_f32_e32 v25, v26, v25
	v_add_f32_e32 v26, v184, v2
	v_min_f32_e32 v26, 0x40e00000, v26
	v_mul_f32_e32 v27, v26, v27
	v_mul_f32_e32 v26, 0xc01d265f, v26
	v_exp_f32_e32 v26, v26
	v_cvt_pk_fp8_f32 v20, v24, v25 op_sel:[0,0,1]
	v_add_f32_e32 v22, 1.0, v22
	v_add_f32_e32 v23, v174, v16
	v_add_f32_e32 v26, 1.0, v26
	v_rcp_f32_e32 v26, v26
	v_med3_f32 v23, v23, s26, v236
	v_add_f32_e32 v23, 1.0, v23
	v_add_f32_e32 v24, v175, v17
	v_mul_f32_e32 v26, v27, v26
	v_add_f32_e32 v27, v185, v3
	v_min_f32_e32 v27, 0x40e00000, v27
	v_mul_f32_e32 v28, v27, v28
	v_mul_f32_e32 v27, 0xc01d265f, v27
	v_exp_f32_e32 v27, v27
	v_med3_f32 v24, v24, s26, v236
	v_add_f32_e32 v24, 1.0, v24
	v_add_f32_e32 v25, v164, v6
	v_add_f32_e32 v27, 1.0, v27
	v_rcp_f32_e32 v27, v27
	v_med3_f32 v25, v25, s26, v236
	v_add_f32_e32 v25, 1.0, v25
	v_mul_f32_e32 v27, v28, v27
	v_add_f32_e32 v28, v186, v4
	v_min_f32_e32 v28, 0x40e00000, v28
	v_mul_f32_e32 v29, v28, v29
	v_mul_f32_e32 v28, 0xc01d265f, v28
	v_exp_f32_e32 v28, v28
	v_cvt_pk_fp8_f32 v21, v26, v27
	v_add_f32_e32 v26, v165, v7
	v_med3_f32 v26, v26, s26, v236
	v_add_f32_e32 v28, 1.0, v28
	v_rcp_f32_e32 v28, v28
	v_add_f32_e32 v26, 1.0, v26
	v_add_f32_e32 v27, v166, v8
	v_med3_f32 v27, v27, s26, v236
	v_mul_f32_e32 v28, v29, v28
	v_add_f32_e32 v29, v187, v5
	v_min_f32_e32 v29, 0x40e00000, v29
	v_mul_f32_e32 v30, v29, v30
	v_mul_f32_e32 v29, 0xc01d265f, v29
	v_exp_f32_e32 v29, v29
	v_add_f32_e32 v27, 1.0, v27
	v_add_f32_e32 v29, 1.0, v29
	v_rcp_f32_e32 v29, v29
	s_nop 0
	v_mul_f32_e32 v29, v30, v29
	v_cvt_pk_fp8_f32 v21, v28, v29 op_sel:[0,0,1]
	v_add_f32_e32 v28, v167, v9
	v_med3_f32 v28, v28, s26, v236
	v_add_f32_e32 v28, 1.0, v28
	global_store_dwordx2 v[18:19], v[20:21], off
	v_add_f32_e32 v21, v172, v14
	v_add_f32_e32 v20, v176, v10
	v_med3_f32 v21, v21, s26, v236
	v_min_f32_e32 v20, 0x40e00000, v20
	v_add_f32_e32 v21, 1.0, v21
	v_mul_f32_e32 v21, v20, v21
	v_mul_f32_e32 v20, 0xc01d265f, v20
	v_exp_f32_e32 v20, v20
	s_nop 0
	v_add_f32_e32 v20, 1.0, v20
	v_rcp_f32_e32 v20, v20
	s_nop 0
	v_mul_f32_e32 v21, v21, v20
	v_add_f32_e32 v20, v177, v11
	v_min_f32_e32 v20, 0x40e00000, v20
	v_mul_f32_e32 v22, v20, v22
	v_mul_f32_e32 v20, 0xc01d265f, v20
	v_exp_f32_e32 v20, v20
	s_nop 0
	v_add_f32_e32 v20, 1.0, v20
	v_rcp_f32_e32 v20, v20
	s_nop 0
	v_mul_f32_e32 v22, v22, v20
	v_add_f32_e32 v20, v178, v12
	v_min_f32_e32 v20, 0x40e00000, v20
	v_mul_f32_e32 v23, v20, v23
	v_mul_f32_e32 v20, 0xc01d265f, v20
	v_exp_f32_e32 v20, v20
	s_nop 0
	v_add_f32_e32 v20, 1.0, v20
	v_rcp_f32_e32 v20, v20
	s_nop 0
	v_mul_f32_e32 v23, v23, v20
	v_add_f32_e32 v20, v179, v13
	v_min_f32_e32 v20, 0x40e00000, v20
	v_mul_f32_e32 v24, v20, v24
	v_mul_f32_e32 v20, 0xc01d265f, v20
	v_exp_f32_e32 v20, v20
	s_nop 0
	v_add_f32_e32 v20, 1.0, v20
	v_rcp_f32_e32 v20, v20
	s_nop 0
	v_mul_f32_e32 v24, v24, v20
	v_add_f32_e32 v20, v168, v2
	v_min_f32_e32 v20, 0x40e00000, v20
	v_mul_f32_e32 v25, v20, v25
	v_mul_f32_e32 v20, 0xc01d265f, v20
	v_exp_f32_e32 v20, v20
	s_nop 0
	v_add_f32_e32 v20, 1.0, v20
	v_rcp_f32_e32 v20, v20
	s_nop 0
	v_mul_f32_e32 v25, v25, v20
	v_add_f32_e32 v20, v169, v3
	v_min_f32_e32 v20, 0x40e00000, v20
	v_mul_f32_e32 v26, v20, v26
	v_mul_f32_e32 v20, 0xc01d265f, v20
	v_exp_f32_e32 v20, v20
	s_nop 0
	v_add_f32_e32 v20, 1.0, v20
	v_rcp_f32_e32 v20, v20
	s_nop 0
	v_mul_f32_e32 v26, v26, v20
	v_add_f32_e32 v20, v170, v4
	v_min_f32_e32 v20, 0x40e00000, v20
	v_mul_f32_e32 v27, v20, v27
	v_mul_f32_e32 v20, 0xc01d265f, v20
	v_exp_f32_e32 v20, v20
	s_nop 0
	v_add_f32_e32 v20, 1.0, v20
	v_rcp_f32_e32 v20, v20
	s_nop 0
	v_mul_f32_e32 v27, v27, v20
	v_add_f32_e32 v20, v171, v5
	v_min_f32_e32 v20, 0x40e00000, v20
	v_mul_f32_e32 v28, v20, v28
	v_mul_f32_e32 v20, 0xc01d265f, v20
	v_exp_f32_e32 v20, v20
	s_nop 0
	v_add_f32_e32 v20, 1.0, v20
	v_rcp_f32_e32 v20, v20
	s_nop 0
	v_mul_f32_e32 v28, v28, v20
	v_mov_b32_e32 v20, v99
	v_cvt_pk_fp8_f32 v20, v21, v22
	v_mov_b32_e32 v21, v99
	v_cvt_pk_fp8_f32 v21, v25, v26
	v_add_co_u32_e32 v22, vcc, s10, v18
	v_cvt_pk_fp8_f32 v20, v23, v24 op_sel:[0,0,1]
	v_cvt_pk_fp8_f32 v21, v27, v28 op_sel:[0,0,1]
	v_addc_co_u32_e32 v23, vcc, 0, v19, vcc
	v_add_f32_e32 v24, v159, v17
	global_store_dwordx2 v[22:23], v[20:21], off
	v_add_f32_e32 v21, v156, v14
	v_add_f32_e32 v20, v160, v10
	v_med3_f32 v21, v21, s26, v236
	v_min_f32_e32 v20, 0x40e00000, v20
	v_add_f32_e32 v21, 1.0, v21
	v_mul_f32_e32 v21, v20, v21
	v_mul_f32_e32 v20, 0xc01d265f, v20
	v_exp_f32_e32 v20, v20
	v_add_f32_e32 v22, v157, v15
	v_med3_f32 v22, v22, s26, v236
	v_add_f32_e32 v22, 1.0, v22
	v_add_f32_e32 v20, 1.0, v20
	v_rcp_f32_e32 v20, v20
	v_add_f32_e32 v23, v158, v16
	v_med3_f32 v23, v23, s26, v236
	v_add_f32_e32 v23, 1.0, v23
	v_mul_f32_e32 v21, v21, v20
	v_add_f32_e32 v20, v161, v11
	v_min_f32_e32 v20, 0x40e00000, v20
	v_mul_f32_e32 v22, v20, v22
	v_mul_f32_e32 v20, 0xc01d265f, v20
	v_exp_f32_e32 v20, v20
	v_med3_f32 v24, v24, s26, v236
	v_add_f32_e32 v24, 1.0, v24
	v_add_f32_e32 v25, v148, v6
	v_add_f32_e32 v20, 1.0, v20
	v_rcp_f32_e32 v20, v20
	v_med3_f32 v25, v25, s26, v236
	v_add_f32_e32 v25, 1.0, v25
	v_add_f32_e32 v26, v149, v7
	v_mul_f32_e32 v22, v22, v20
	v_add_f32_e32 v20, v162, v12
	v_min_f32_e32 v20, 0x40e00000, v20
	v_mul_f32_e32 v23, v20, v23
	v_mul_f32_e32 v20, 0xc01d265f, v20
	v_exp_f32_e32 v20, v20
	v_med3_f32 v26, v26, s26, v236
	v_add_f32_e32 v26, 1.0, v26
	v_add_f32_e32 v27, v150, v8
	v_add_f32_e32 v20, 1.0, v20
	v_rcp_f32_e32 v20, v20
	v_med3_f32 v27, v27, s26, v236
	v_add_f32_e32 v27, 1.0, v27
	v_add_f32_e32 v28, v151, v9
	v_mul_f32_e32 v23, v23, v20
	v_add_f32_e32 v20, v163, v13
	v_min_f32_e32 v20, 0x40e00000, v20
	v_mul_f32_e32 v24, v20, v24
	v_mul_f32_e32 v20, 0xc01d265f, v20
	v_exp_f32_e32 v20, v20
	v_med3_f32 v28, v28, s26, v236
	v_add_f32_e32 v28, 1.0, v28
	s_mov_b32 s10, 0x8000
	v_add_f32_e32 v20, 1.0, v20
	v_rcp_f32_e32 v20, v20
	s_nop 0
	v_mul_f32_e32 v24, v24, v20
	v_add_f32_e32 v20, v152, v2
	v_min_f32_e32 v20, 0x40e00000, v20
	v_mul_f32_e32 v25, v20, v25
	v_mul_f32_e32 v20, 0xc01d265f, v20
	v_exp_f32_e32 v20, v20
	s_nop 0
	v_add_f32_e32 v20, 1.0, v20
	v_rcp_f32_e32 v20, v20
	s_nop 0
	v_mul_f32_e32 v25, v25, v20
	v_add_f32_e32 v20, v153, v3
	v_min_f32_e32 v20, 0x40e00000, v20
	v_mul_f32_e32 v26, v20, v26
	v_mul_f32_e32 v20, 0xc01d265f, v20
	v_exp_f32_e32 v20, v20
	s_nop 0
	v_add_f32_e32 v20, 1.0, v20
	v_rcp_f32_e32 v20, v20
	s_nop 0
	v_mul_f32_e32 v26, v26, v20
	v_add_f32_e32 v20, v154, v4
	v_min_f32_e32 v20, 0x40e00000, v20
	v_mul_f32_e32 v27, v20, v27
	v_mul_f32_e32 v20, 0xc01d265f, v20
	v_exp_f32_e32 v20, v20
	s_nop 0
	v_add_f32_e32 v20, 1.0, v20
	v_rcp_f32_e32 v20, v20
	s_nop 0
	v_mul_f32_e32 v27, v27, v20
	v_add_f32_e32 v20, v155, v5
	v_min_f32_e32 v20, 0x40e00000, v20
	v_mul_f32_e32 v28, v20, v28
	v_mul_f32_e32 v20, 0xc01d265f, v20
	v_exp_f32_e32 v20, v20
	s_nop 0
	v_add_f32_e32 v20, 1.0, v20
	v_rcp_f32_e32 v20, v20
	s_nop 0
	v_mul_f32_e32 v28, v28, v20
	v_mov_b32_e32 v20, v99
	v_cvt_pk_fp8_f32 v20, v21, v22
	v_mov_b32_e32 v21, v99
	v_cvt_pk_fp8_f32 v21, v25, v26
	v_add_co_u32_e32 v22, vcc, s10, v18
	v_cvt_pk_fp8_f32 v20, v23, v24 op_sel:[0,0,1]
	v_cvt_pk_fp8_f32 v21, v27, v28 op_sel:[0,0,1]
	v_addc_co_u32_e32 v23, vcc, 0, v19, vcc
	v_add_f32_e32 v24, v143, v17
	global_store_dwordx2 v[22:23], v[20:21], off
	v_add_f32_e32 v21, v140, v14
	v_add_f32_e32 v20, v144, v10
	v_med3_f32 v21, v21, s26, v236
	v_min_f32_e32 v20, 0x40e00000, v20
	v_add_f32_e32 v21, 1.0, v21
	v_mul_f32_e32 v21, v20, v21
	v_mul_f32_e32 v20, 0xc01d265f, v20
	v_exp_f32_e32 v20, v20
	v_add_f32_e32 v22, v141, v15
	v_med3_f32 v22, v22, s26, v236
	v_add_f32_e32 v22, 1.0, v22
	v_add_f32_e32 v20, 1.0, v20
	v_rcp_f32_e32 v20, v20
	v_add_f32_e32 v23, v142, v16
	v_med3_f32 v23, v23, s26, v236
	v_add_f32_e32 v23, 1.0, v23
	v_mul_f32_e32 v21, v21, v20
	v_add_f32_e32 v20, v145, v11
	v_min_f32_e32 v20, 0x40e00000, v20
	v_mul_f32_e32 v22, v20, v22
	v_mul_f32_e32 v20, 0xc01d265f, v20
	v_exp_f32_e32 v20, v20
	v_med3_f32 v24, v24, s26, v236
	v_add_f32_e32 v24, 1.0, v24
	v_add_f32_e32 v25, v132, v6
	v_add_f32_e32 v20, 1.0, v20
	v_rcp_f32_e32 v20, v20
	v_med3_f32 v25, v25, s26, v236
	v_add_f32_e32 v25, 1.0, v25
	v_add_f32_e32 v26, v133, v7
	v_mul_f32_e32 v22, v22, v20
	v_add_f32_e32 v20, v146, v12
	v_min_f32_e32 v20, 0x40e00000, v20
	v_mul_f32_e32 v23, v20, v23
	v_mul_f32_e32 v20, 0xc01d265f, v20
	v_exp_f32_e32 v20, v20
	v_med3_f32 v26, v26, s26, v236
	v_add_f32_e32 v26, 1.0, v26
	v_add_f32_e32 v27, v134, v8
	v_add_f32_e32 v20, 1.0, v20
	v_rcp_f32_e32 v20, v20
	v_med3_f32 v27, v27, s26, v236
	v_add_f32_e32 v27, 1.0, v27
	v_add_f32_e32 v28, v135, v9
	v_mul_f32_e32 v23, v23, v20
	v_add_f32_e32 v20, v147, v13
	v_min_f32_e32 v20, 0x40e00000, v20
	v_mul_f32_e32 v24, v20, v24
	v_mul_f32_e32 v20, 0xc01d265f, v20
	v_exp_f32_e32 v20, v20
	v_med3_f32 v28, v28, s26, v236
	v_add_f32_e32 v28, 1.0, v28
	s_mov_b32 s10, 0xc000
	v_add_f32_e32 v20, 1.0, v20
	v_rcp_f32_e32 v20, v20
	s_nop 0
	v_mul_f32_e32 v24, v24, v20
	v_add_f32_e32 v20, v136, v2
	v_min_f32_e32 v20, 0x40e00000, v20
	v_mul_f32_e32 v25, v20, v25
	v_mul_f32_e32 v20, 0xc01d265f, v20
	v_exp_f32_e32 v20, v20
	s_nop 0
	v_add_f32_e32 v20, 1.0, v20
	v_rcp_f32_e32 v20, v20
	s_nop 0
	v_mul_f32_e32 v25, v25, v20
	v_add_f32_e32 v20, v137, v3
	v_min_f32_e32 v20, 0x40e00000, v20
	v_mul_f32_e32 v26, v20, v26
	v_mul_f32_e32 v20, 0xc01d265f, v20
	v_exp_f32_e32 v20, v20
	s_nop 0
	v_add_f32_e32 v20, 1.0, v20
	v_rcp_f32_e32 v20, v20
	s_nop 0
	v_mul_f32_e32 v26, v26, v20
	v_add_f32_e32 v20, v138, v4
	v_min_f32_e32 v20, 0x40e00000, v20
	v_mul_f32_e32 v27, v20, v27
	v_mul_f32_e32 v20, 0xc01d265f, v20
	v_exp_f32_e32 v20, v20
	s_nop 0
	v_add_f32_e32 v20, 1.0, v20
	v_rcp_f32_e32 v20, v20
	s_nop 0
	v_mul_f32_e32 v27, v27, v20
	v_add_f32_e32 v20, v139, v5
	v_min_f32_e32 v20, 0x40e00000, v20
	v_mul_f32_e32 v28, v20, v28
	v_mul_f32_e32 v20, 0xc01d265f, v20
	v_exp_f32_e32 v20, v20
	s_nop 0
	v_add_f32_e32 v20, 1.0, v20
	v_rcp_f32_e32 v20, v20
	s_nop 0
	v_mul_f32_e32 v28, v28, v20
	v_mov_b32_e32 v20, v99
	v_cvt_pk_fp8_f32 v20, v21, v22
	v_mov_b32_e32 v21, v99
	v_cvt_pk_fp8_f32 v21, v25, v26
	v_add_co_u32_e32 v22, vcc, s10, v18
	v_cvt_pk_fp8_f32 v20, v23, v24 op_sel:[0,0,1]
	v_cvt_pk_fp8_f32 v21, v27, v28 op_sel:[0,0,1]
	v_addc_co_u32_e32 v23, vcc, 0, v19, vcc
	v_add_f32_e32 v24, v127, v17
	global_store_dwordx2 v[22:23], v[20:21], off
	v_add_f32_e32 v21, v124, v14
	v_add_f32_e32 v20, v128, v10
	v_med3_f32 v21, v21, s26, v236
	v_min_f32_e32 v20, 0x40e00000, v20
	v_add_f32_e32 v21, 1.0, v21
	v_mul_f32_e32 v21, v20, v21
	v_mul_f32_e32 v20, 0xc01d265f, v20
	v_exp_f32_e32 v20, v20
	v_add_f32_e32 v22, v125, v15
	v_med3_f32 v22, v22, s26, v236
	v_add_f32_e32 v22, 1.0, v22
	v_add_f32_e32 v20, 1.0, v20
	v_rcp_f32_e32 v20, v20
	v_add_f32_e32 v23, v126, v16
	v_med3_f32 v23, v23, s26, v236
	v_add_f32_e32 v23, 1.0, v23
	v_mul_f32_e32 v21, v21, v20
	v_add_f32_e32 v20, v129, v11
	v_min_f32_e32 v20, 0x40e00000, v20
	v_mul_f32_e32 v22, v20, v22
	v_mul_f32_e32 v20, 0xc01d265f, v20
	v_exp_f32_e32 v20, v20
	v_med3_f32 v24, v24, s26, v236
	v_add_f32_e32 v24, 1.0, v24
	v_add_f32_e32 v25, v116, v6
	v_add_f32_e32 v20, 1.0, v20
	v_rcp_f32_e32 v20, v20
	v_med3_f32 v25, v25, s26, v236
	v_add_f32_e32 v25, 1.0, v25
	v_add_f32_e32 v26, v117, v7
	v_mul_f32_e32 v22, v22, v20
	v_add_f32_e32 v20, v130, v12
	v_min_f32_e32 v20, 0x40e00000, v20
	v_mul_f32_e32 v23, v20, v23
	v_mul_f32_e32 v20, 0xc01d265f, v20
	v_exp_f32_e32 v20, v20
	v_med3_f32 v26, v26, s26, v236
	v_add_f32_e32 v26, 1.0, v26
	v_add_f32_e32 v27, v118, v8
	v_add_f32_e32 v20, 1.0, v20
	v_rcp_f32_e32 v20, v20
	v_med3_f32 v27, v27, s26, v236
	v_add_f32_e32 v27, 1.0, v27
	v_add_f32_e32 v28, v119, v9
	v_mul_f32_e32 v23, v23, v20
	v_add_f32_e32 v20, v131, v13
	v_min_f32_e32 v20, 0x40e00000, v20
	v_mul_f32_e32 v24, v20, v24
	v_mul_f32_e32 v20, 0xc01d265f, v20
	v_exp_f32_e32 v20, v20
	v_med3_f32 v28, v28, s26, v236
	v_add_f32_e32 v28, 1.0, v28
	s_mov_b32 s10, 0x20000
	v_add_f32_e32 v20, 1.0, v20
	v_rcp_f32_e32 v20, v20
	s_nop 0
	v_mul_f32_e32 v24, v24, v20
	v_add_f32_e32 v20, v120, v2
	v_min_f32_e32 v20, 0x40e00000, v20
	v_mul_f32_e32 v25, v20, v25
	v_mul_f32_e32 v20, 0xc01d265f, v20
	v_exp_f32_e32 v20, v20
	s_nop 0
	v_add_f32_e32 v20, 1.0, v20
	v_rcp_f32_e32 v20, v20
	s_nop 0
	v_mul_f32_e32 v25, v25, v20
	v_add_f32_e32 v20, v121, v3
	v_min_f32_e32 v20, 0x40e00000, v20
	v_mul_f32_e32 v26, v20, v26
	v_mul_f32_e32 v20, 0xc01d265f, v20
	v_exp_f32_e32 v20, v20
	s_nop 0
	v_add_f32_e32 v20, 1.0, v20
	v_rcp_f32_e32 v20, v20
	s_nop 0
	v_mul_f32_e32 v26, v26, v20
	v_add_f32_e32 v20, v122, v4
	v_min_f32_e32 v20, 0x40e00000, v20
	v_mul_f32_e32 v27, v20, v27
	v_mul_f32_e32 v20, 0xc01d265f, v20
	v_exp_f32_e32 v20, v20
	s_nop 0
	v_add_f32_e32 v20, 1.0, v20
	v_rcp_f32_e32 v20, v20
	s_nop 0
	v_mul_f32_e32 v27, v27, v20
	v_add_f32_e32 v20, v123, v5
	v_min_f32_e32 v20, 0x40e00000, v20
	v_mul_f32_e32 v28, v20, v28
	v_mul_f32_e32 v20, 0xc01d265f, v20
	v_exp_f32_e32 v20, v20
	s_nop 0
	v_add_f32_e32 v20, 1.0, v20
	v_rcp_f32_e32 v20, v20
	s_nop 0
	v_mul_f32_e32 v28, v28, v20
	v_mov_b32_e32 v20, v99
	v_cvt_pk_fp8_f32 v20, v21, v22
	v_mov_b32_e32 v21, v99
	v_cvt_pk_fp8_f32 v21, v25, v26
	v_add_co_u32_e32 v22, vcc, s10, v18
	v_cvt_pk_fp8_f32 v20, v23, v24 op_sel:[0,0,1]
	v_cvt_pk_fp8_f32 v21, v27, v28 op_sel:[0,0,1]
	v_addc_co_u32_e32 v23, vcc, 0, v19, vcc
	v_add_f32_e32 v24, v111, v17
	global_store_dwordx2 v[22:23], v[20:21], off
	v_add_f32_e32 v21, v108, v14
	v_add_f32_e32 v20, v112, v10
	v_med3_f32 v21, v21, s26, v236
	v_min_f32_e32 v20, 0x40e00000, v20
	v_add_f32_e32 v21, 1.0, v21
	v_mul_f32_e32 v21, v20, v21
	v_mul_f32_e32 v20, 0xc01d265f, v20
	v_exp_f32_e32 v20, v20
	v_add_f32_e32 v22, v109, v15
	v_med3_f32 v22, v22, s26, v236
	v_add_f32_e32 v22, 1.0, v22
	v_add_f32_e32 v20, 1.0, v20
	v_rcp_f32_e32 v20, v20
	v_add_f32_e32 v23, v110, v16
	v_med3_f32 v23, v23, s26, v236
	v_add_f32_e32 v23, 1.0, v23
	v_mul_f32_e32 v21, v21, v20
	v_add_f32_e32 v20, v113, v11
	v_min_f32_e32 v20, 0x40e00000, v20
	v_mul_f32_e32 v22, v20, v22
	v_mul_f32_e32 v20, 0xc01d265f, v20
	v_exp_f32_e32 v20, v20
	v_med3_f32 v24, v24, s26, v236
	v_add_f32_e32 v24, 1.0, v24
	v_add_f32_e32 v25, v100, v6
	v_add_f32_e32 v20, 1.0, v20
	v_rcp_f32_e32 v20, v20
	v_med3_f32 v25, v25, s26, v236
	v_add_f32_e32 v25, 1.0, v25
	v_add_f32_e32 v26, v101, v7
	v_mul_f32_e32 v22, v22, v20
	v_add_f32_e32 v20, v114, v12
	v_min_f32_e32 v20, 0x40e00000, v20
	v_mul_f32_e32 v23, v20, v23
	v_mul_f32_e32 v20, 0xc01d265f, v20
	v_exp_f32_e32 v20, v20
	v_med3_f32 v26, v26, s26, v236
	v_add_f32_e32 v26, 1.0, v26
	v_add_f32_e32 v27, v102, v8
	v_add_f32_e32 v20, 1.0, v20
	v_rcp_f32_e32 v20, v20
	v_med3_f32 v27, v27, s26, v236
	v_add_f32_e32 v27, 1.0, v27
	v_add_f32_e32 v28, v103, v9
	v_mul_f32_e32 v23, v23, v20
	v_add_f32_e32 v20, v115, v13
	v_min_f32_e32 v20, 0x40e00000, v20
	v_mul_f32_e32 v24, v20, v24
	v_mul_f32_e32 v20, 0xc01d265f, v20
	v_exp_f32_e32 v20, v20
	v_med3_f32 v28, v28, s26, v236
	v_add_f32_e32 v28, 1.0, v28
	s_mov_b32 s10, 0x24000
	v_add_f32_e32 v20, 1.0, v20
	v_rcp_f32_e32 v20, v20
	s_nop 0
	v_mul_f32_e32 v24, v24, v20
	v_add_f32_e32 v20, v104, v2
	v_min_f32_e32 v20, 0x40e00000, v20
	v_mul_f32_e32 v25, v20, v25
	v_mul_f32_e32 v20, 0xc01d265f, v20
	v_exp_f32_e32 v20, v20
	s_nop 0
	v_add_f32_e32 v20, 1.0, v20
	v_rcp_f32_e32 v20, v20
	s_nop 0
	v_mul_f32_e32 v25, v25, v20
	v_add_f32_e32 v20, v105, v3
	v_min_f32_e32 v20, 0x40e00000, v20
	v_mul_f32_e32 v26, v20, v26
	v_mul_f32_e32 v20, 0xc01d265f, v20
	v_exp_f32_e32 v20, v20
	s_nop 0
	v_add_f32_e32 v20, 1.0, v20
	v_rcp_f32_e32 v20, v20
	s_nop 0
	v_mul_f32_e32 v26, v26, v20
	v_add_f32_e32 v20, v106, v4
	v_min_f32_e32 v20, 0x40e00000, v20
	v_mul_f32_e32 v27, v20, v27
	v_mul_f32_e32 v20, 0xc01d265f, v20
	v_exp_f32_e32 v20, v20
	s_nop 0
	v_add_f32_e32 v20, 1.0, v20
	v_rcp_f32_e32 v20, v20
	s_nop 0
	v_mul_f32_e32 v27, v27, v20
	v_add_f32_e32 v20, v107, v5
	v_min_f32_e32 v20, 0x40e00000, v20
	v_mul_f32_e32 v28, v20, v28
	v_mul_f32_e32 v20, 0xc01d265f, v20
	v_exp_f32_e32 v20, v20
	s_nop 0
	v_add_f32_e32 v20, 1.0, v20
	v_rcp_f32_e32 v20, v20
	s_nop 0
	v_mul_f32_e32 v28, v28, v20
	v_mov_b32_e32 v20, v99
	v_cvt_pk_fp8_f32 v20, v21, v22
	v_mov_b32_e32 v21, v99
	v_cvt_pk_fp8_f32 v21, v25, v26
	v_add_co_u32_e32 v22, vcc, s10, v18
	v_cvt_pk_fp8_f32 v20, v23, v24 op_sel:[0,0,1]
	v_cvt_pk_fp8_f32 v21, v27, v28 op_sel:[0,0,1]
	v_addc_co_u32_e32 v23, vcc, 0, v19, vcc
	v_add_f32_e32 v24, v93, v17
	global_store_dwordx2 v[22:23], v[20:21], off
	v_add_f32_e32 v21, v90, v14
	v_add_f32_e32 v20, v94, v10
	v_med3_f32 v21, v21, s26, v236
	v_min_f32_e32 v20, 0x40e00000, v20
	v_add_f32_e32 v21, 1.0, v21
	v_mul_f32_e32 v21, v20, v21
	v_mul_f32_e32 v20, 0xc01d265f, v20
	v_exp_f32_e32 v20, v20
	v_add_f32_e32 v22, v91, v15
	v_med3_f32 v22, v22, s26, v236
	v_add_f32_e32 v22, 1.0, v22
	v_add_f32_e32 v20, 1.0, v20
	v_rcp_f32_e32 v20, v20
	v_add_f32_e32 v23, v92, v16
	v_med3_f32 v23, v23, s26, v236
	v_add_f32_e32 v23, 1.0, v23
	v_mul_f32_e32 v21, v21, v20
	v_add_f32_e32 v20, v95, v11
	v_min_f32_e32 v20, 0x40e00000, v20
	v_mul_f32_e32 v22, v20, v22
	v_mul_f32_e32 v20, 0xc01d265f, v20
	v_exp_f32_e32 v20, v20
	v_med3_f32 v24, v24, s26, v236
	v_add_f32_e32 v24, 1.0, v24
	v_add_f32_e32 v25, v82, v6
	v_add_f32_e32 v20, 1.0, v20
	v_rcp_f32_e32 v20, v20
	v_add_f32_e32 v6, v66, v6
	v_med3_f32 v25, v25, s26, v236
	v_med3_f32 v6, v6, s26, v236
	v_mul_f32_e32 v22, v22, v20
	v_add_f32_e32 v20, v96, v12
	v_min_f32_e32 v20, 0x40e00000, v20
	v_mul_f32_e32 v23, v20, v23
	v_mul_f32_e32 v20, 0xc01d265f, v20
	v_exp_f32_e32 v20, v20
	v_add_f32_e32 v25, 1.0, v25
	v_add_f32_e32 v6, 1.0, v6
	v_add_f32_e32 v14, v74, v14
	v_add_f32_e32 v20, 1.0, v20
	v_rcp_f32_e32 v20, v20
	v_add_f32_e32 v10, v78, v10
	v_med3_f32 v14, v14, s26, v236
	v_min_f32_e32 v10, 0x40e00000, v10
	v_mul_f32_e32 v23, v23, v20
	v_add_f32_e32 v20, v97, v13
	v_min_f32_e32 v20, 0x40e00000, v20
	v_mul_f32_e32 v24, v20, v24
	v_mul_f32_e32 v20, 0xc01d265f, v20
	v_exp_f32_e32 v20, v20
	v_add_f32_e32 v14, 1.0, v14
	v_mul_f32_e32 v14, v10, v14
	v_mul_f32_e32 v10, 0xc01d265f, v10
	v_add_f32_e32 v20, 1.0, v20
	v_rcp_f32_e32 v20, v20
	v_exp_f32_e32 v10, v10
	v_add_f32_e32 v26, v83, v7
	v_med3_f32 v26, v26, s26, v236
	v_mul_f32_e32 v24, v24, v20
	v_add_f32_e32 v20, v86, v2
	v_add_f32_e32 v2, v70, v2
	v_min_f32_e32 v20, 0x40e00000, v20
	v_min_f32_e32 v2, 0x40e00000, v2
	v_mul_f32_e32 v25, v20, v25
	v_mul_f32_e32 v20, 0xc01d265f, v20
	v_mul_f32_e32 v6, v2, v6
	v_mul_f32_e32 v2, 0xc01d265f, v2
	v_exp_f32_e32 v20, v20
	v_exp_f32_e32 v2, v2
	v_add_f32_e32 v10, 1.0, v10
	v_rcp_f32_e32 v10, v10
	v_add_f32_e32 v20, 1.0, v20
	v_add_f32_e32 v2, 1.0, v2
	v_rcp_f32_e32 v20, v20
	v_rcp_f32_e32 v2, v2
	v_add_f32_e32 v26, 1.0, v26
	v_mul_f32_e32 v10, v14, v10
	v_mul_f32_e32 v25, v25, v20
	v_add_f32_e32 v20, v87, v3
	v_mul_f32_e32 v6, v6, v2
	v_add_f32_e32 v2, v71, v3
	v_add_f32_e32 v3, v67, v7
	v_med3_f32 v3, v3, s26, v236
	v_min_f32_e32 v2, 0x40e00000, v2
	v_add_f32_e32 v3, 1.0, v3
	v_min_f32_e32 v20, 0x40e00000, v20
	v_mul_f32_e32 v3, v2, v3
	v_mul_f32_e32 v2, 0xc01d265f, v2
	v_mul_f32_e32 v26, v20, v26
	v_mul_f32_e32 v20, 0xc01d265f, v20
	v_add_f32_e32 v14, v75, v15
	v_exp_f32_e32 v2, v2
	v_exp_f32_e32 v20, v20
	v_add_f32_e32 v11, v79, v11
	v_med3_f32 v14, v14, s26, v236
	v_min_f32_e32 v11, 0x40e00000, v11
	v_add_f32_e32 v14, 1.0, v14
	v_mul_f32_e32 v14, v11, v14
	v_mul_f32_e32 v11, 0xc01d265f, v11
	v_exp_f32_e32 v11, v11
	v_add_f32_e32 v2, 1.0, v2
	v_add_f32_e32 v20, 1.0, v20
	v_rcp_f32_e32 v2, v2
	v_rcp_f32_e32 v20, v20
	v_add_f32_e32 v11, 1.0, v11
	v_add_f32_e32 v27, v84, v8
	v_rcp_f32_e32 v11, v11
	v_mul_f32_e32 v7, v3, v2
	v_add_f32_e32 v3, v68, v8
	v_mul_f32_e32 v26, v26, v20
	v_add_f32_e32 v20, v88, v4
	v_med3_f32 v27, v27, s26, v236
	v_add_f32_e32 v2, v72, v4
	v_med3_f32 v3, v3, s26, v236
	v_min_f32_e32 v20, 0x40e00000, v20
	v_add_f32_e32 v27, 1.0, v27
	v_min_f32_e32 v2, 0x40e00000, v2
	v_add_f32_e32 v3, 1.0, v3
	v_mul_f32_e32 v27, v20, v27
	v_mul_f32_e32 v20, 0xc01d265f, v20
	v_mul_f32_e32 v3, v2, v3
	v_mul_f32_e32 v2, 0xc01d265f, v2
	v_exp_f32_e32 v20, v20
	v_mul_f32_e32 v11, v14, v11
	v_add_f32_e32 v14, v76, v16
	v_exp_f32_e32 v2, v2
	v_add_f32_e32 v12, v80, v12
	v_med3_f32 v14, v14, s26, v236
	v_min_f32_e32 v12, 0x40e00000, v12
	v_add_f32_e32 v14, 1.0, v14
	v_mul_f32_e32 v14, v12, v14
	v_mul_f32_e32 v12, 0xc01d265f, v12
	v_add_f32_e32 v20, 1.0, v20
	v_exp_f32_e32 v12, v12
	v_add_f32_e32 v2, 1.0, v2
	v_rcp_f32_e32 v20, v20
	v_rcp_f32_e32 v2, v2
	v_add_f32_e32 v28, v85, v9
	v_add_f32_e32 v12, 1.0, v12
	v_mul_f32_e32 v27, v27, v20
	v_add_f32_e32 v20, v89, v5
	v_med3_f32 v28, v28, s26, v236
	v_rcp_f32_e32 v12, v12
	v_mul_f32_e32 v4, v3, v2
	v_add_f32_e32 v3, v69, v9
	v_min_f32_e32 v20, 0x40e00000, v20
	v_add_f32_e32 v28, 1.0, v28
	v_add_f32_e32 v2, v73, v5
	v_med3_f32 v3, v3, s26, v236
	v_mul_f32_e32 v28, v20, v28
	v_mul_f32_e32 v20, 0xc01d265f, v20
	v_min_f32_e32 v2, 0x40e00000, v2
	v_add_f32_e32 v3, 1.0, v3
	v_exp_f32_e32 v20, v20
	v_mul_f32_e32 v3, v2, v3
	v_mul_f32_e32 v2, 0xc01d265f, v2
	v_mul_f32_e32 v12, v14, v12
	v_add_f32_e32 v14, v77, v17
	v_exp_f32_e32 v2, v2
	v_add_f32_e32 v13, v81, v13
	v_med3_f32 v14, v14, s26, v236
	v_min_f32_e32 v13, 0x40e00000, v13
	v_add_f32_e32 v14, 1.0, v14
	v_add_f32_e32 v20, 1.0, v20
	v_mul_f32_e32 v14, v13, v14
	v_mul_f32_e32 v13, 0xc01d265f, v13
	v_rcp_f32_e32 v20, v20
	v_exp_f32_e32 v13, v13
	v_add_f32_e32 v2, 1.0, v2
	v_rcp_f32_e32 v2, v2
	v_mul_f32_e32 v28, v28, v20
	v_mov_b32_e32 v20, v99
	v_add_f32_e32 v13, 1.0, v13
	v_cvt_pk_fp8_f32 v20, v21, v22
	v_mov_b32_e32 v21, v99
	v_rcp_f32_e32 v13, v13
	v_mul_f32_e32 v5, v3, v2
	v_mov_b32_e32 v2, v99
	v_mov_b32_e32 v3, v99
	v_cvt_pk_fp8_f32 v21, v25, v26
	v_cvt_pk_fp8_f32 v2, v10, v11
	v_cvt_pk_fp8_f32 v3, v6, v7
	s_mov_b32 s10, 0x28000
	v_add_co_u32_e32 v22, vcc, s10, v18
	v_mul_f32_e32 v13, v14, v13
	v_cvt_pk_fp8_f32 v20, v23, v24 op_sel:[0,0,1]
	v_cvt_pk_fp8_f32 v21, v27, v28 op_sel:[0,0,1]
	v_addc_co_u32_e32 v23, vcc, 0, v19, vcc
	v_cvt_pk_fp8_f32 v2, v12, v13 op_sel:[0,0,1]
	v_cvt_pk_fp8_f32 v3, v4, v5 op_sel:[0,0,1]
	v_add_co_u32_e32 v4, vcc, 0x2c000, v18
	s_mov_b64 s[10:11], -1
	s_nop 0
	v_addc_co_u32_e32 v5, vcc, 0, v19, vcc
	s_andn2_b64 vcc, exec, s[8:9]
	global_store_dwordx2 v[22:23], v[20:21], off
	global_store_dwordx2 v[4:5], v[2:3], off
	s_mov_b64 s[100:101], -1
	s_cbranch_vccnz .LBB0_1427
	s_andn2_b64 vcc, exec, s[4:5]
	s_cbranch_vccnz .LBB0_1426
	s_barrier
	s_branch .LBB0_1426

.LBB0_1495:
	s_mov_b64 s[100:101], 0
	s_cmp_le_i32 s92, s2
	s_cselect_b64 s[4:5], -1, 0
	s_cmp_lt_i32 s2, s93
	s_cselect_b64 s[6:7], -1, 0
	s_and_b64 s[4:5], s[4:5], s[6:7]
	s_andn2_b64 vcc, exec, s[4:5]
	s_cbranch_vccz .LBB0_1496
	s_getpc_b64 s[98:99]

.LBB0_1504:
	s_ashr_i32 s41, s40, 31
	s_lshl_b64 s[10:11], s[40:41], 21
	s_add_u32 s31, s13, s10
	s_addc_u32 s41, s17, s11
	v_readlane_b32 s10, v253, 36
	v_readlane_b32 s11, v253, 37
	s_mov_b32 s46, s10
	s_ashr_i32 s47, s10, 31
	v_writelane_b32 v253, s10, 36
	v_lshl_add_u32 v2, s61, 18, v239
	v_mov_b32_e32 v66, 0
	v_writelane_b32 v253, s11, 37
	s_lshl_b64 s[10:11], s[46:47], 18
	s_add_u32 s10, s31, s10
	s_addc_u32 s11, s41, s11
	s_and_b64 s[46:47], s[8:9], exec
	s_cselect_b32 s41, s11, s45
	s_cselect_b32 s65, s10, s44
	s_add_u32 s66, s44, 0x100
	s_addc_u32 s68, s45, 0
	v_readlane_b32 s44, v253, 42
	v_add_u32_e32 v245, v2, v238
	v_add_u32_e32 v246, v240, v2
	v_add_u32_e32 v212, v241, v2
	v_add_u32_e32 v214, v242, v2
	v_mov_b32_e32 v213, v99
	v_mov_b32_e32 v215, v99
	s_mov_b32 s83, -2
	v_readlane_b32 s45, v253, 43
	v_mov_b32_e32 v67, v66
	v_mov_b32_e32 v68, v66
	v_mov_b32_e32 v69, v66
	v_mov_b32_e32 v70, v66
	v_mov_b32_e32 v71, v66
	v_mov_b32_e32 v72, v66
	v_mov_b32_e32 v73, v66
	v_mov_b32_e32 v74, v66
	v_mov_b32_e32 v75, v66
	v_mov_b32_e32 v76, v66
	v_mov_b32_e32 v77, v66
	v_mov_b32_e32 v78, v66
	v_mov_b32_e32 v79, v66
	v_mov_b32_e32 v80, v66
	v_mov_b32_e32 v81, v66
	v_mov_b32_e32 v82, v66
	v_mov_b32_e32 v83, v66
	v_mov_b32_e32 v84, v66
	v_mov_b32_e32 v85, v66
	v_mov_b32_e32 v86, v66
	v_mov_b32_e32 v87, v66
	v_mov_b32_e32 v88, v66
	v_mov_b32_e32 v89, v66
	v_mov_b32_e32 v90, v66
	v_mov_b32_e32 v91, v66
	v_mov_b32_e32 v92, v66
	v_mov_b32_e32 v93, v66
	v_mov_b32_e32 v94, v66
	v_mov_b32_e32 v95, v66
	v_mov_b32_e32 v96, v66
	v_mov_b32_e32 v97, v66
	v_mov_b32_e32 v124, v66
	v_mov_b32_e32 v125, v66
	v_mov_b32_e32 v126, v66
	v_mov_b32_e32 v127, v66
	v_mov_b32_e32 v132, v66
	v_mov_b32_e32 v133, v66
	v_mov_b32_e32 v134, v66
	v_mov_b32_e32 v135, v66
	v_mov_b32_e32 v140, v66
	v_mov_b32_e32 v141, v66
	v_mov_b32_e32 v142, v66
	v_mov_b32_e32 v143, v66
	v_mov_b32_e32 v144, v66
	v_mov_b32_e32 v145, v66
	v_mov_b32_e32 v146, v66
	v_mov_b32_e32 v147, v66
	v_mov_b32_e32 v148, v66
	v_mov_b32_e32 v149, v66
	v_mov_b32_e32 v150, v66
	v_mov_b32_e32 v151, v66
	v_mov_b32_e32 v152, v66
	v_mov_b32_e32 v153, v66
	v_mov_b32_e32 v154, v66
	v_mov_b32_e32 v155, v66
	v_mov_b32_e32 v156, v66
	v_mov_b32_e32 v157, v66
	v_mov_b32_e32 v158, v66
	v_mov_b32_e32 v159, v66
	v_mov_b32_e32 v160, v66
	v_mov_b32_e32 v161, v66
	v_mov_b32_e32 v162, v66
	v_mov_b32_e32 v163, v66
	v_mov_b32_e32 v100, v66
	v_mov_b32_e32 v101, v66
	v_mov_b32_e32 v102, v66
	v_mov_b32_e32 v103, v66
	v_mov_b32_e32 v104, v66
	v_mov_b32_e32 v105, v66
	v_mov_b32_e32 v106, v66
	v_mov_b32_e32 v107, v66
	v_mov_b32_e32 v108, v66
	v_mov_b32_e32 v109, v66
	v_mov_b32_e32 v110, v66
	v_mov_b32_e32 v111, v66
	v_mov_b32_e32 v112, v66
	v_mov_b32_e32 v113, v66
	v_mov_b32_e32 v114, v66
	v_mov_b32_e32 v115, v66
	v_mov_b32_e32 v116, v66
	v_mov_b32_e32 v117, v66
	v_mov_b32_e32 v118, v66
	v_mov_b32_e32 v119, v66
	v_mov_b32_e32 v120, v66
	v_mov_b32_e32 v121, v66
	v_mov_b32_e32 v122, v66
	v_mov_b32_e32 v123, v66
	v_mov_b32_e32 v128, v66
	v_mov_b32_e32 v129, v66
	v_mov_b32_e32 v130, v66
	v_mov_b32_e32 v131, v66
	v_mov_b32_e32 v136, v66
	v_mov_b32_e32 v137, v66
	v_mov_b32_e32 v138, v66
	v_mov_b32_e32 v139, v66
	v_mov_b32_e32 v164, v66
	v_mov_b32_e32 v165, v66
	v_mov_b32_e32 v166, v66
	v_mov_b32_e32 v167, v66
	v_mov_b32_e32 v168, v66
	v_mov_b32_e32 v169, v66
	v_mov_b32_e32 v170, v66
	v_mov_b32_e32 v171, v66
	v_mov_b32_e32 v172, v66
	v_mov_b32_e32 v173, v66
	v_mov_b32_e32 v174, v66
	v_mov_b32_e32 v175, v66
	v_mov_b32_e32 v176, v66
	v_mov_b32_e32 v177, v66
	v_mov_b32_e32 v178, v66
	v_mov_b32_e32 v179, v66
	v_mov_b32_e32 v180, v66
	v_mov_b32_e32 v181, v66
	v_mov_b32_e32 v182, v66
	v_mov_b32_e32 v183, v66
	v_mov_b32_e32 v184, v66
	v_mov_b32_e32 v185, v66
	v_mov_b32_e32 v186, v66
	v_mov_b32_e32 v187, v66
	v_mov_b32_e32 v188, v66
	v_mov_b32_e32 v189, v66
	v_mov_b32_e32 v190, v66
	v_mov_b32_e32 v191, v66
	v_mov_b32_e32 v192, v66
	v_mov_b32_e32 v193, v66
	v_mov_b32_e32 v194, v66
	v_mov_b32_e32 v195, v66
	s_branch .LBB0_1507

.Lepw10:
	s_add_u32 s31, s44, 0x80
	s_waitcnt lgkmcnt(0)
	s_addc_u32 s48, s45, 0
	s_and_b64 s[46:47], s[46:47], exec
	s_cselect_b32 s47, s41, s68
	s_cselect_b32 s46, s65, s66
	s_cselect_b32 s49, s81, s48
	s_cselect_b32 s48, s80, s31
	s_barrier
	s_setprio 1
	s_waitcnt lgkmcnt(0)
	v_mfma_scale_f32_16x16x128_f8f6f4 v[192:195], v[18:25], v[58:65], v[192:195], v224, v224 op_sel_hi:[0,0,0]
	v_mfma_scale_f32_16x16x128_f8f6f4 v[188:191], v[26:33], v[58:65], v[188:191], v224, v224 op_sel_hi:[0,0,0]
	v_mfma_scale_f32_16x16x128_f8f6f4 v[184:187], v[18:25], v[50:57], v[184:187], v224, v224 op_sel_hi:[0,0,0]
	v_mfma_scale_f32_16x16x128_f8f6f4 v[180:183], v[26:33], v[50:57], v[180:183], v224, v224 op_sel_hi:[0,0,0]
	v_mfma_scale_f32_16x16x128_f8f6f4 v[176:179], v[18:25], v[42:49], v[176:179], v224, v224 op_sel_hi:[0,0,0]
	v_mfma_scale_f32_16x16x128_f8f6f4 v[172:175], v[26:33], v[42:49], v[172:175], v224, v224 op_sel_hi:[0,0,0]
	v_mfma_scale_f32_16x16x128_f8f6f4 v[168:171], v[18:25], v[34:41], v[168:171], v224, v224 op_sel_hi:[0,0,0]
	v_mfma_scale_f32_16x16x128_f8f6f4 v[164:167], v[26:33], v[34:41], v[164:167], v224, v224 op_sel_hi:[0,0,0]
	s_setprio 0
	s_setprio 1
	v_mfma_scale_f32_16x16x128_f8f6f4 v[136:139], v[2:9], v[58:65], v[136:139], v224, v224 op_sel_hi:[0,0,0]
	v_mfma_scale_f32_16x16x128_f8f6f4 v[128:131], v[10:17], v[58:65], v[128:131], v224, v224 op_sel_hi:[0,0,0]
	v_mfma_scale_f32_16x16x128_f8f6f4 v[120:123], v[2:9], v[50:57], v[120:123], v224, v224 op_sel_hi:[0,0,0]
	v_mfma_scale_f32_16x16x128_f8f6f4 v[116:119], v[10:17], v[50:57], v[116:119], v224, v224 op_sel_hi:[0,0,0]
	v_mfma_scale_f32_16x16x128_f8f6f4 v[112:115], v[2:9], v[42:49], v[112:115], v224, v224 op_sel_hi:[0,0,0]
	v_mfma_scale_f32_16x16x128_f8f6f4 v[108:111], v[10:17], v[42:49], v[108:111], v224, v224 op_sel_hi:[0,0,0]
	v_mfma_scale_f32_16x16x128_f8f6f4 v[104:107], v[2:9], v[34:41], v[104:107], v224, v224 op_sel_hi:[0,0,0]
	v_mfma_scale_f32_16x16x128_f8f6f4 v[100:103], v[10:17], v[34:41], v[100:103], v224, v224 op_sel_hi:[0,0,0]
	s_setprio 0
	s_barrier
	s_mov_b32 m0, s20
	v_lshl_add_u64 v[196:197], s[46:47], 0, v[204:205]
	s_add_u32 s90, s46, 0x20000
	ds_read_b128 v[34:37], v244 offset:16384
	ds_read_b128 v[38:41], v244 offset:17408
	ds_read_b128 v[42:45], v244 offset:18432
	ds_read_b128 v[46:49], v244 offset:19456
	ds_read_b128 v[50:53], v244 offset:20480
	ds_read_b128 v[54:57], v244 offset:21504
	ds_read_b128 v[58:61], v244 offset:22528
	ds_read_b128 v[62:65], v244 offset:23552
	global_load_lds_dwordx4 v[196:197], off
	v_lshl_add_u64 v[226:227], s[46:47], 0, v[202:203]
	s_mov_b32 m0, s21
	s_addc_u32 s91, s47, 0
	global_load_lds_dwordx4 v[226:227], off
	v_lshl_add_u64 v[228:229], s[90:91], 0, v[204:205]
	s_mov_b32 m0, s24
	v_mov_b32_e32 v207, v99
	global_load_lds_dwordx4 v[228:229], off
	v_lshl_add_u64 v[228:229], s[90:91], 0, v[202:203]
	s_mov_b32 m0, s27
	v_lshl_add_u64 v[248:249], s[48:49], 0, v[206:207]
	global_load_lds_dwordx4 v[228:229], off
	s_mov_b32 m0, s19
	v_lshl_add_u64 v[228:229], s[48:49], 0, v[98:99]
	global_load_lds_dwordx4 v98, s[48:49]
	s_mov_b32 m0, s28
	s_nop 0
	global_load_lds_dwordx4 v206, s[48:49]
	s_mov_b64 vcc, s[100:101]
	s_cbranch_vccnz .Lepw9
	s_waitcnt vmcnt(8)
.Lepw9:
	s_waitcnt lgkmcnt(0)
	s_barrier
	s_setprio 1
	s_waitcnt lgkmcnt(0)
	v_mfma_scale_f32_16x16x128_f8f6f4 v[160:163], v[18:25], v[34:41], v[160:163], v224, v224 op_sel_hi:[0,0,0]
	v_mfma_scale_f32_16x16x128_f8f6f4 v[156:159], v[26:33], v[34:41], v[156:159], v224, v224 op_sel_hi:[0,0,0]
	v_mfma_scale_f32_16x16x128_f8f6f4 v[152:155], v[18:25], v[42:49], v[152:155], v224, v224 op_sel_hi:[0,0,0]
	v_mfma_scale_f32_16x16x128_f8f6f4 v[148:151], v[26:33], v[42:49], v[148:151], v224, v224 op_sel_hi:[0,0,0]
	v_mfma_scale_f32_16x16x128_f8f6f4 v[144:147], v[18:25], v[50:57], v[144:147], v224, v224 op_sel_hi:[0,0,0]
	v_mfma_scale_f32_16x16x128_f8f6f4 v[140:143], v[26:33], v[50:57], v[140:143], v224, v224 op_sel_hi:[0,0,0]
	v_mfma_scale_f32_16x16x128_f8f6f4 v[132:135], v[18:25], v[58:65], v[132:135], v224, v224 op_sel_hi:[0,0,0]
	v_mfma_scale_f32_16x16x128_f8f6f4 v[124:127], v[26:33], v[58:65], v[124:127], v224, v224 op_sel_hi:[0,0,0]
	s_setprio 0
	s_setprio 1
	v_mfma_scale_f32_16x16x128_f8f6f4 v[94:97], v[2:9], v[34:41], v[94:97], v224, v224 op_sel_hi:[0,0,0]
	v_mfma_scale_f32_16x16x128_f8f6f4 v[90:93], v[10:17], v[34:41], v[90:93], v224, v224 op_sel_hi:[0,0,0]
	v_mfma_scale_f32_16x16x128_f8f6f4 v[86:89], v[2:9], v[42:49], v[86:89], v224, v224 op_sel_hi:[0,0,0]
	v_mfma_scale_f32_16x16x128_f8f6f4 v[82:85], v[10:17], v[42:49], v[82:85], v224, v224 op_sel_hi:[0,0,0]
	v_mfma_scale_f32_16x16x128_f8f6f4 v[78:81], v[2:9], v[50:57], v[78:81], v224, v224 op_sel_hi:[0,0,0]
	v_mfma_scale_f32_16x16x128_f8f6f4 v[74:77], v[10:17], v[50:57], v[74:77], v224, v224 op_sel_hi:[0,0,0]
	v_mfma_scale_f32_16x16x128_f8f6f4 v[70:73], v[2:9], v[58:65], v[70:73], v224, v224 op_sel_hi:[0,0,0]
	v_mfma_scale_f32_16x16x128_f8f6f4 v[66:69], v[10:17], v[58:65], v[66:69], v224, v224 op_sel_hi:[0,0,0]
	s_setprio 0
	s_barrier
	ds_read_b128 v[2:5], v243 offset:32768
	ds_read_b128 v[6:9], v243 offset:33792
	ds_read_b128 v[10:13], v243 offset:34816
	ds_read_b128 v[14:17], v243 offset:35840
	ds_read_b128 v[18:21], v243 offset:49152
	ds_read_b128 v[22:25], v243 offset:50176
	ds_read_b128 v[26:29], v243 offset:51200
	ds_read_b128 v[30:33], v243 offset:52224
	s_mov_b32 m0, s29
	v_lshl_add_u64 v[218:219], s[48:49], 0, v[218:219]
	ds_read_b128 v[34:37], v244 offset:32768
	ds_read_b128 v[38:41], v244 offset:33792
	ds_read_b128 v[42:45], v244 offset:34816
	ds_read_b128 v[46:49], v244 offset:35840
	ds_read_b128 v[50:53], v244 offset:36864
	ds_read_b128 v[54:57], v244 offset:37888
	ds_read_b128 v[58:61], v244 offset:38912
	ds_read_b128 v[62:65], v244 offset:39936
	global_load_lds_dwordx4 v[218:219], off
	v_lshl_add_u64 v[216:217], s[48:49], 0, v[216:217]
	s_mov_b32 m0, s50
	s_nop 0
	global_load_lds_dwordx4 v[216:217], off
	s_waitcnt vmcnt(8)
	s_mov_b64 s[100:101], 0
	s_waitcnt lgkmcnt(0)
	s_barrier
	s_setprio 1
	s_waitcnt lgkmcnt(0)
	v_mfma_scale_f32_16x16x128_f8f6f4 v[192:195], v[2:9], v[34:41], v[192:195], v224, v224 op_sel_hi:[0,0,0]
	v_mfma_scale_f32_16x16x128_f8f6f4 v[188:191], v[10:17], v[34:41], v[188:191], v224, v224 op_sel_hi:[0,0,0]
	v_mfma_scale_f32_16x16x128_f8f6f4 v[184:187], v[2:9], v[42:49], v[184:187], v224, v224 op_sel_hi:[0,0,0]
	v_mfma_scale_f32_16x16x128_f8f6f4 v[180:183], v[10:17], v[42:49], v[180:183], v224, v224 op_sel_hi:[0,0,0]
	v_mfma_scale_f32_16x16x128_f8f6f4 v[176:179], v[2:9], v[50:57], v[176:179], v224, v224 op_sel_hi:[0,0,0]
	v_mfma_scale_f32_16x16x128_f8f6f4 v[172:175], v[10:17], v[50:57], v[172:175], v224, v224 op_sel_hi:[0,0,0]
	v_mfma_scale_f32_16x16x128_f8f6f4 v[168:171], v[2:9], v[58:65], v[168:171], v224, v224 op_sel_hi:[0,0,0]
	v_mfma_scale_f32_16x16x128_f8f6f4 v[164:167], v[10:17], v[58:65], v[164:167], v224, v224 op_sel_hi:[0,0,0]
	s_setprio 0
	s_setprio 1
	v_mfma_scale_f32_16x16x128_f8f6f4 v[136:139], v[18:25], v[34:41], v[136:139], v224, v224 op_sel_hi:[0,0,0]
	v_mfma_scale_f32_16x16x128_f8f6f4 v[128:131], v[26:33], v[34:41], v[128:131], v224, v224 op_sel_hi:[0,0,0]
	v_mfma_scale_f32_16x16x128_f8f6f4 v[120:123], v[18:25], v[42:49], v[120:123], v224, v224 op_sel_hi:[0,0,0]
	v_mfma_scale_f32_16x16x128_f8f6f4 v[116:119], v[26:33], v[42:49], v[116:119], v224, v224 op_sel_hi:[0,0,0]
	v_mfma_scale_f32_16x16x128_f8f6f4 v[112:115], v[18:25], v[50:57], v[112:115], v224, v224 op_sel_hi:[0,0,0]
	v_mfma_scale_f32_16x16x128_f8f6f4 v[108:111], v[26:33], v[50:57], v[108:111], v224, v224 op_sel_hi:[0,0,0]
	v_mfma_scale_f32_16x16x128_f8f6f4 v[104:107], v[18:25], v[58:65], v[104:107], v224, v224 op_sel_hi:[0,0,0]
	v_mfma_scale_f32_16x16x128_f8f6f4 v[100:103], v[26:33], v[58:65], v[100:103], v224, v224 op_sel_hi:[0,0,0]
	s_setprio 0
	s_barrier
	s_mov_b32 m0, s54
	v_lshl_add_u64 v[196:197], v[196:197], 0, s[62:63]
	s_add_u32 s46, s46, 0x20080
	ds_read_b128 v[34:37], v244 offset:49152
	ds_read_b128 v[38:41], v244 offset:50176
	ds_read_b128 v[42:45], v244 offset:51200
	ds_read_b128 v[46:49], v244 offset:52224
	ds_read_b128 v[50:53], v244 offset:53248
	ds_read_b128 v[54:57], v244 offset:54272
	ds_read_b128 v[58:61], v244 offset:55296
	ds_read_b128 v[62:65], v244 offset:56320
	global_load_lds_dwordx4 v[196:197], off
	v_lshl_add_u64 v[196:197], v[226:227], 0, s[62:63]
	s_mov_b32 m0, s55
	s_addc_u32 s47, s47, 0
	global_load_lds_dwordx4 v[196:197], off
	v_lshl_add_u64 v[196:197], s[46:47], 0, v[204:205]
	s_mov_b32 m0, s58
	s_nop 0
	global_load_lds_dwordx4 v[196:197], off
	v_lshl_add_u64 v[196:197], s[46:47], 0, v[202:203]
	s_mov_b32 m0, s59
	s_nop 0
	global_load_lds_dwordx4 v[196:197], off
	v_lshl_add_u64 v[196:197], v[228:229], 0, s[62:63]
	s_mov_b32 m0, s56
	s_nop 0
	global_load_lds_dwordx4 v[196:197], off
	v_lshl_add_u64 v[196:197], v[248:249], 0, s[62:63]
	s_mov_b32 m0, s57
	s_nop 0
	global_load_lds_dwordx4 v[196:197], off
	s_waitcnt vmcnt(8)
	s_waitcnt lgkmcnt(0)
	s_barrier
	s_setprio 1
	s_waitcnt lgkmcnt(0)
	v_mfma_scale_f32_16x16x128_f8f6f4 v[160:163], v[2:9], v[34:41], v[160:163], v224, v224 op_sel_hi:[0,0,0]
	v_mfma_scale_f32_16x16x128_f8f6f4 v[156:159], v[10:17], v[34:41], v[156:159], v224, v224 op_sel_hi:[0,0,0]
	v_mfma_scale_f32_16x16x128_f8f6f4 v[152:155], v[2:9], v[42:49], v[152:155], v224, v224 op_sel_hi:[0,0,0]
	v_mfma_scale_f32_16x16x128_f8f6f4 v[148:151], v[10:17], v[42:49], v[148:151], v224, v224 op_sel_hi:[0,0,0]
	v_mfma_scale_f32_16x16x128_f8f6f4 v[144:147], v[2:9], v[50:57], v[144:147], v224, v224 op_sel_hi:[0,0,0]
	v_mfma_scale_f32_16x16x128_f8f6f4 v[140:143], v[10:17], v[50:57], v[140:143], v224, v224 op_sel_hi:[0,0,0]
	v_mfma_scale_f32_16x16x128_f8f6f4 v[132:135], v[2:9], v[58:65], v[132:135], v224, v224 op_sel_hi:[0,0,0]
	v_mfma_scale_f32_16x16x128_f8f6f4 v[124:127], v[10:17], v[58:65], v[124:127], v224, v224 op_sel_hi:[0,0,0]
	s_setprio 0
	s_setprio 1
	v_mfma_scale_f32_16x16x128_f8f6f4 v[94:97], v[18:25], v[34:41], v[94:97], v224, v224 op_sel_hi:[0,0,0]
	v_mfma_scale_f32_16x16x128_f8f6f4 v[90:93], v[26:33], v[34:41], v[90:93], v224, v224 op_sel_hi:[0,0,0]
	v_mfma_scale_f32_16x16x128_f8f6f4 v[86:89], v[18:25], v[42:49], v[86:89], v224, v224 op_sel_hi:[0,0,0]
	v_mfma_scale_f32_16x16x128_f8f6f4 v[82:85], v[26:33], v[42:49], v[82:85], v224, v224 op_sel_hi:[0,0,0]
	v_mfma_scale_f32_16x16x128_f8f6f4 v[78:81], v[18:25], v[50:57], v[78:81], v224, v224 op_sel_hi:[0,0,0]
	v_mfma_scale_f32_16x16x128_f8f6f4 v[74:77], v[26:33], v[50:57], v[74:77], v224, v224 op_sel_hi:[0,0,0]
	v_mfma_scale_f32_16x16x128_f8f6f4 v[70:73], v[18:25], v[58:65], v[70:73], v224, v224 op_sel_hi:[0,0,0]
	v_mfma_scale_f32_16x16x128_f8f6f4 v[66:69], v[26:33], v[58:65], v[66:69], v224, v224 op_sel_hi:[0,0,0]
	s_setprio 0
	s_barrier
	s_add_i32 s83, s83, 2
	s_add_u32 s44, s44, 0x100
	s_addc_u32 s45, s45, 0
	s_add_u32 s66, s66, 0x100
	s_addc_u32 s68, s68, 0
	s_cmp_gt_u32 s83, 5
	s_cbranch_scc1 .LBB0_1509

.LBB0_1511:
	s_lshl_b32 s31, s43, 8
	v_mov_b32_e32 v2, v237
	v_mov_b32_e32 v3, v201
	s_add_i32 s31, s31, s53
	v_readlane_b32 s44, v253, 36
	s_ashr_i32 s43, s42, 31
	v_add_u32_e32 v34, s31, v3
	s_lshl_b32 s31, s44, 8
	s_or_b32 s31, s31, s12
	s_lshl_b64 s[42:43], s[42:43], 13
	v_lshl_add_u32 v36, v2, 3, s31
	s_add_u32 s42, s51, s42
	v_ashrrev_i32_e32 v37, 31, v36
	v_ashrrev_i32_e32 v35, 31, v34
	s_addc_u32 s43, s52, s43
	v_lshl_add_u64 v[18:19], v[34:35], 2, s[70:71]
	v_lshl_add_u64 v[6:7], v[36:37], 2, s[42:43]
	global_load_dwordx4 v[10:13], v[6:7], off offset:16
	global_load_dwordx4 v[14:17], v[6:7], off
	global_load_dwordx4 v[2:5], v[6:7], off offset:528
	s_nop 0
	global_load_dwordx4 v[6:9], v[6:7], off offset:512
	s_nop 0
	global_load_dword v21, v[18:19], off offset:704
	global_load_dword v20, v[18:19], off offset:640
	global_load_dword v22, v[18:19], off offset:576
	global_load_dword v23, v[18:19], off offset:512
	global_load_dword v24, v[18:19], off offset:192
	global_load_dword v25, v[18:19], off offset:128
	global_load_dword v26, v[18:19], off offset:64
	s_nop 0
	global_load_dword v18, v[18:19], off
	v_mov_b32_e32 v46, v99
	v_mov_b32_e32 v47, v99
	v_readlane_b32 s42, v251, 14
	v_lshlrev_b64 v[34:35], 11, v[34:35]
	v_readlane_b32 s43, v251, 15
	s_mov_b32 s31, 0x8000
	v_mov_b32_e32 v48, v99
	v_lshl_add_u64 v[34:35], s[42:43], 0, v[34:35]
	v_lshl_add_u64 v[34:35], v[34:35], 0, v[36:37]
	v_mov_b32_e32 v49, v99
	v_mov_b32_e32 v50, v99
	v_mov_b32_e32 v51, v99
	v_mov_b32_e32 v52, v99
	v_mov_b32_e32 v53, v99
	v_mov_b32_e32 v54, v99
	v_mov_b32_e32 v55, v99
	s_mov_b64 s[42:43], 0x8000
	s_mov_b64 s[46:47], s[36:37]
	v_readlane_b32 s83, v255, 2
	v_readlane_b32 s65, v255, 3
	s_movk_i32 s66, 0x5ff
	v_readlane_b32 s45, v253, 37
	s_waitcnt vmcnt(0)
	s_nop 0
	v_mul_f32_e32 v32, 0x41800000, v18
	v_pk_add_f32 v[40:41], v[192:193], v[14:15]
	v_pk_add_f32 v[44:45], v[188:189], v[10:11]
	v_pk_mul_f32 v[40:41], v[40:41], v[32:33] op_sel_hi:[1,0]
	v_pk_mul_f32 v[44:45], v[44:45], v[32:33] op_sel_hi:[1,0]
	v_cvt_pk_fp8_f32 v46, v40, v41
	v_cvt_pk_fp8_f32 v47, v44, v45
	v_pk_add_f32 v[38:39], v[194:195], v[16:17]
	v_pk_add_f32 v[42:43], v[190:191], v[12:13]
	v_pk_mul_f32 v[38:39], v[38:39], v[32:33] op_sel_hi:[1,0]
	v_pk_mul_f32 v[42:43], v[42:43], v[32:33] op_sel_hi:[1,0]
	v_mul_f32_e32 v30, 0x41800000, v26
	v_cvt_pk_fp8_f32 v46, v38, v39 op_sel:[0,0,1]
	v_cvt_pk_fp8_f32 v47, v42, v43 op_sel:[0,0,1]
	v_pk_add_f32 v[38:39], v[184:185], v[14:15]
	v_pk_add_f32 v[42:43], v[180:181], v[10:11]
	v_pk_mul_f32 v[38:39], v[38:39], v[30:31] op_sel_hi:[1,0]
	v_pk_mul_f32 v[42:43], v[42:43], v[30:31] op_sel_hi:[1,0]
	v_mov_b32_e32 v44, v99
	v_mov_b32_e32 v45, v99
	v_cvt_pk_fp8_f32 v44, v38, v39
	v_cvt_pk_fp8_f32 v45, v42, v43
	v_pk_add_f32 v[36:37], v[186:187], v[16:17]
	v_pk_add_f32 v[40:41], v[182:183], v[12:13]
	v_pk_mul_f32 v[36:37], v[36:37], v[30:31] op_sel_hi:[1,0]
	v_pk_mul_f32 v[40:41], v[40:41], v[30:31] op_sel_hi:[1,0]
	v_cvt_pk_fp8_f32 v44, v36, v37 op_sel:[0,0,1]
	v_cvt_pk_fp8_f32 v45, v40, v41 op_sel:[0,0,1]
	v_add_co_u32_e32 v38, vcc, s31, v34
	v_mul_f32_e32 v28, 0x41800000, v25
	s_nop 0
	v_addc_co_u32_e32 v39, vcc, 0, v35, vcc
	global_store_dwordx2 v[38:39], v[44:45], off
	v_pk_add_f32 v[40:41], v[176:177], v[14:15]
	v_pk_add_f32 v[44:45], v[172:173], v[10:11]
	global_store_dwordx2 v[34:35], v[46:47], off
	v_pk_mul_f32 v[40:41], v[40:41], v[28:29] op_sel_hi:[1,0]
	v_pk_mul_f32 v[44:45], v[44:45], v[28:29] op_sel_hi:[1,0]
	v_mov_b32_e32 v46, v99
	v_mov_b32_e32 v47, v99
	v_cvt_pk_fp8_f32 v46, v40, v41
	v_cvt_pk_fp8_f32 v47, v44, v45
	v_pk_add_f32 v[38:39], v[178:179], v[16:17]
	v_pk_add_f32 v[42:43], v[174:175], v[12:13]
	v_pk_mul_f32 v[38:39], v[38:39], v[28:29] op_sel_hi:[1,0]
	v_pk_mul_f32 v[42:43], v[42:43], v[28:29] op_sel_hi:[1,0]
	v_cvt_pk_fp8_f32 v46, v38, v39 op_sel:[0,0,1]
	v_cvt_pk_fp8_f32 v47, v42, v43 op_sel:[0,0,1]
	s_mov_b32 s31, 0x10000
	v_add_co_u32_e32 v40, vcc, s31, v34
	v_mul_f32_e32 v26, 0x41800000, v24
	s_nop 0
	v_addc_co_u32_e32 v41, vcc, 0, v35, vcc
	global_store_dwordx2 v[40:41], v[46:47], off
	v_pk_add_f32 v[42:43], v[168:169], v[14:15]
	v_pk_add_f32 v[46:47], v[164:165], v[10:11]
	v_pk_mul_f32 v[42:43], v[42:43], v[26:27] op_sel_hi:[1,0]
	v_pk_mul_f32 v[46:47], v[46:47], v[26:27] op_sel_hi:[1,0]
	v_cvt_pk_fp8_f32 v48, v42, v43
	v_cvt_pk_fp8_f32 v49, v46, v47
	v_pk_add_f32 v[40:41], v[170:171], v[16:17]
	v_pk_add_f32 v[44:45], v[166:167], v[12:13]
	v_pk_mul_f32 v[40:41], v[40:41], v[26:27] op_sel_hi:[1,0]
	v_pk_mul_f32 v[44:45], v[44:45], v[26:27] op_sel_hi:[1,0]
	v_cvt_pk_fp8_f32 v48, v40, v41 op_sel:[0,0,1]
	v_cvt_pk_fp8_f32 v49, v44, v45 op_sel:[0,0,1]
	s_mov_b32 s31, 0x18000
	v_add_co_u32_e32 v42, vcc, s31, v34
	v_mul_f32_e32 v24, 0x41800000, v23
	s_nop 0
	v_addc_co_u32_e32 v43, vcc, 0, v35, vcc
	global_store_dwordx2 v[42:43], v[48:49], off
	v_pk_add_f32 v[44:45], v[160:161], v[14:15]
	v_pk_add_f32 v[48:49], v[156:157], v[10:11]
	v_pk_mul_f32 v[44:45], v[44:45], v[24:25] op_sel_hi:[1,0]
	v_pk_mul_f32 v[48:49], v[48:49], v[24:25] op_sel_hi:[1,0]
	v_cvt_pk_fp8_f32 v50, v44, v45
	v_cvt_pk_fp8_f32 v51, v48, v49
	v_pk_add_f32 v[42:43], v[162:163], v[16:17]
	v_pk_add_f32 v[46:47], v[158:159], v[12:13]
	v_pk_mul_f32 v[42:43], v[42:43], v[24:25] op_sel_hi:[1,0]
	v_pk_mul_f32 v[46:47], v[46:47], v[24:25] op_sel_hi:[1,0]
	v_cvt_pk_fp8_f32 v50, v42, v43 op_sel:[0,0,1]
	v_cvt_pk_fp8_f32 v51, v46, v47 op_sel:[0,0,1]
	s_mov_b32 s31, 0x40000
	v_add_co_u32_e32 v44, vcc, s31, v34
	v_mul_f32_e32 v22, 0x41800000, v22
	s_nop 0
	v_addc_co_u32_e32 v45, vcc, 0, v35, vcc
	global_store_dwordx2 v[44:45], v[50:51], off
	v_pk_add_f32 v[46:47], v[152:153], v[14:15]
	v_pk_add_f32 v[50:51], v[148:149], v[10:11]
	v_pk_mul_f32 v[46:47], v[46:47], v[22:23] op_sel_hi:[1,0]
	v_pk_mul_f32 v[50:51], v[50:51], v[22:23] op_sel_hi:[1,0]
	v_cvt_pk_fp8_f32 v52, v46, v47
	v_cvt_pk_fp8_f32 v53, v50, v51
	v_pk_add_f32 v[44:45], v[154:155], v[16:17]
	v_pk_add_f32 v[48:49], v[150:151], v[12:13]
	v_pk_mul_f32 v[44:45], v[44:45], v[22:23] op_sel_hi:[1,0]
	v_pk_mul_f32 v[48:49], v[48:49], v[22:23] op_sel_hi:[1,0]
	v_cvt_pk_fp8_f32 v52, v44, v45 op_sel:[0,0,1]
	v_cvt_pk_fp8_f32 v53, v48, v49 op_sel:[0,0,1]
	s_mov_b32 s31, 0x48000
	v_add_co_u32_e32 v46, vcc, s31, v34
	v_mul_f32_e32 v20, 0x41800000, v20
	s_nop 0
	v_addc_co_u32_e32 v47, vcc, 0, v35, vcc
	global_store_dwordx2 v[46:47], v[52:53], off
	v_pk_add_f32 v[48:49], v[144:145], v[14:15]
	v_pk_add_f32 v[52:53], v[140:141], v[10:11]
	v_pk_mul_f32 v[48:49], v[48:49], v[20:21] op_sel_hi:[1,0]
	v_pk_mul_f32 v[52:53], v[52:53], v[20:21] op_sel_hi:[1,0]
	v_cvt_pk_fp8_f32 v54, v48, v49
	v_cvt_pk_fp8_f32 v55, v52, v53
	v_pk_add_f32 v[46:47], v[146:147], v[16:17]
	v_pk_add_f32 v[50:51], v[142:143], v[12:13]
	v_pk_mul_f32 v[46:47], v[46:47], v[20:21] op_sel_hi:[1,0]
	v_pk_mul_f32 v[50:51], v[50:51], v[20:21] op_sel_hi:[1,0]
	v_cvt_pk_fp8_f32 v54, v46, v47 op_sel:[0,0,1]
	v_cvt_pk_fp8_f32 v55, v50, v51 op_sel:[0,0,1]
	s_mov_b32 s31, 0x50000
	v_add_co_u32_e32 v48, vcc, s31, v34
	v_mul_f32_e32 v18, 0x41800000, v21
	s_nop 0
	v_addc_co_u32_e32 v49, vcc, 0, v35, vcc
	v_pk_add_f32 v[14:15], v[132:133], v[14:15]
	v_pk_add_f32 v[10:11], v[124:125], v[10:11]
	global_store_dwordx2 v[48:49], v[54:55], off
	v_pk_mul_f32 v[14:15], v[14:15], v[18:19] op_sel_hi:[1,0]
	v_pk_mul_f32 v[10:11], v[10:11], v[18:19] op_sel_hi:[1,0]
	v_mov_b32_e32 v48, v99
	v_mov_b32_e32 v49, v99
	v_cvt_pk_fp8_f32 v48, v14, v15
	v_cvt_pk_fp8_f32 v49, v10, v11
	v_pk_add_f32 v[16:17], v[134:135], v[16:17]
	v_pk_add_f32 v[12:13], v[126:127], v[12:13]
	v_pk_mul_f32 v[16:17], v[16:17], v[18:19] op_sel_hi:[1,0]
	v_pk_mul_f32 v[12:13], v[12:13], v[18:19] op_sel_hi:[1,0]
	v_cvt_pk_fp8_f32 v48, v16, v17 op_sel:[0,0,1]
	v_cvt_pk_fp8_f32 v49, v12, v13 op_sel:[0,0,1]
	s_mov_b32 s31, 0x58000
	v_add_co_u32_e32 v12, vcc, s31, v34
	v_pk_add_f32 v[14:15], v[136:137], v[6:7]
	s_nop 0
	v_addc_co_u32_e32 v13, vcc, 0, v35, vcc
	global_store_dwordx2 v[12:13], v[48:49], off
	v_pk_add_f32 v[12:13], v[138:139], v[8:9]
	v_pk_add_f32 v[16:17], v[130:131], v[4:5]
	v_pk_add_f32 v[48:49], v[128:129], v[2:3]
	v_pk_mul_f32 v[12:13], v[12:13], v[32:33] op_sel_hi:[1,0]
	v_pk_mul_f32 v[14:15], v[14:15], v[32:33] op_sel_hi:[1,0]
	v_pk_mul_f32 v[16:17], v[16:17], v[32:33] op_sel_hi:[1,0]
	v_pk_mul_f32 v[32:33], v[48:49], v[32:33] op_sel_hi:[1,0]
	v_mov_b32_e32 v48, v99
	v_mov_b32_e32 v49, v99
	v_cvt_pk_fp8_f32 v48, v14, v15
	v_cvt_pk_fp8_f32 v49, v32, v33
	v_pk_add_f32 v[14:15], v[120:121], v[6:7]
	v_pk_add_f32 v[32:33], v[116:117], v[2:3]
	v_cvt_pk_fp8_f32 v48, v12, v13 op_sel:[0,0,1]
	v_cvt_pk_fp8_f32 v49, v16, v17 op_sel:[0,0,1]
	v_pk_add_f32 v[12:13], v[122:123], v[8:9]
	v_pk_add_f32 v[16:17], v[118:119], v[4:5]
	v_pk_mul_f32 v[12:13], v[12:13], v[30:31] op_sel_hi:[1,0]
	v_pk_mul_f32 v[14:15], v[14:15], v[30:31] op_sel_hi:[1,0]
	v_pk_mul_f32 v[16:17], v[16:17], v[30:31] op_sel_hi:[1,0]
	v_pk_mul_f32 v[30:31], v[32:33], v[30:31] op_sel_hi:[1,0]
	v_mov_b32_e32 v32, v99
	v_mov_b32_e32 v33, v99
	v_cvt_pk_fp8_f32 v32, v14, v15
	v_cvt_pk_fp8_f32 v33, v30, v31
	v_pk_add_f32 v[14:15], v[112:113], v[6:7]
	v_pk_add_f32 v[30:31], v[108:109], v[2:3]
	v_cvt_pk_fp8_f32 v32, v12, v13 op_sel:[0,0,1]
	v_cvt_pk_fp8_f32 v33, v16, v17 op_sel:[0,0,1]
	v_pk_add_f32 v[12:13], v[114:115], v[8:9]
	v_pk_add_f32 v[16:17], v[110:111], v[4:5]
	v_pk_mul_f32 v[12:13], v[12:13], v[28:29] op_sel_hi:[1,0]
	v_pk_mul_f32 v[14:15], v[14:15], v[28:29] op_sel_hi:[1,0]
	v_pk_mul_f32 v[16:17], v[16:17], v[28:29] op_sel_hi:[1,0]
	v_pk_mul_f32 v[28:29], v[30:31], v[28:29] op_sel_hi:[1,0]
	v_mov_b32_e32 v30, v99
	v_mov_b32_e32 v31, v99
	v_cvt_pk_fp8_f32 v30, v14, v15
	v_cvt_pk_fp8_f32 v31, v28, v29
	v_pk_add_f32 v[14:15], v[104:105], v[6:7]
	v_pk_add_f32 v[28:29], v[100:101], v[2:3]
	v_cvt_pk_fp8_f32 v30, v12, v13 op_sel:[0,0,1]
	v_cvt_pk_fp8_f32 v31, v16, v17 op_sel:[0,0,1]
	v_pk_add_f32 v[12:13], v[106:107], v[8:9]
	v_pk_add_f32 v[16:17], v[102:103], v[4:5]
	v_pk_mul_f32 v[12:13], v[12:13], v[26:27] op_sel_hi:[1,0]
	v_pk_mul_f32 v[14:15], v[14:15], v[26:27] op_sel_hi:[1,0]
	v_pk_mul_f32 v[16:17], v[16:17], v[26:27] op_sel_hi:[1,0]
	v_pk_mul_f32 v[26:27], v[28:29], v[26:27] op_sel_hi:[1,0]
	v_mov_b32_e32 v28, v99
	v_mov_b32_e32 v29, v99
	v_cvt_pk_fp8_f32 v28, v14, v15
	v_cvt_pk_fp8_f32 v29, v26, v27
	v_pk_add_f32 v[14:15], v[94:95], v[6:7]
	v_pk_add_f32 v[26:27], v[90:91], v[2:3]
	v_cvt_pk_fp8_f32 v28, v12, v13 op_sel:[0,0,1]
	v_cvt_pk_fp8_f32 v29, v16, v17 op_sel:[0,0,1]
	v_pk_add_f32 v[12:13], v[96:97], v[8:9]
	v_pk_add_f32 v[16:17], v[92:93], v[4:5]
	v_pk_mul_f32 v[12:13], v[12:13], v[24:25] op_sel_hi:[1,0]
	v_pk_mul_f32 v[14:15], v[14:15], v[24:25] op_sel_hi:[1,0]
	v_pk_mul_f32 v[16:17], v[16:17], v[24:25] op_sel_hi:[1,0]
	v_pk_mul_f32 v[24:25], v[26:27], v[24:25] op_sel_hi:[1,0]
	v_mov_b32_e32 v26, v99
	v_mov_b32_e32 v27, v99
	v_cvt_pk_fp8_f32 v26, v14, v15
	v_cvt_pk_fp8_f32 v27, v24, v25
	v_pk_add_f32 v[14:15], v[86:87], v[6:7]
	v_pk_add_f32 v[24:25], v[82:83], v[2:3]
	v_cvt_pk_fp8_f32 v26, v12, v13 op_sel:[0,0,1]
	v_cvt_pk_fp8_f32 v27, v16, v17 op_sel:[0,0,1]
	v_pk_add_f32 v[12:13], v[88:89], v[8:9]
	v_pk_add_f32 v[16:17], v[84:85], v[4:5]
	v_pk_mul_f32 v[12:13], v[12:13], v[22:23] op_sel_hi:[1,0]
	v_pk_mul_f32 v[14:15], v[14:15], v[22:23] op_sel_hi:[1,0]
	v_pk_mul_f32 v[16:17], v[16:17], v[22:23] op_sel_hi:[1,0]
	v_pk_mul_f32 v[22:23], v[24:25], v[22:23] op_sel_hi:[1,0]
	v_mov_b32_e32 v24, v99
	v_mov_b32_e32 v25, v99
	v_cvt_pk_fp8_f32 v24, v14, v15
	v_cvt_pk_fp8_f32 v25, v22, v23
	v_pk_add_f32 v[14:15], v[78:79], v[6:7]
	v_pk_add_f32 v[22:23], v[74:75], v[2:3]
	v_cvt_pk_fp8_f32 v24, v12, v13 op_sel:[0,0,1]
	v_cvt_pk_fp8_f32 v25, v16, v17 op_sel:[0,0,1]
	v_pk_add_f32 v[12:13], v[80:81], v[8:9]
	v_pk_add_f32 v[16:17], v[76:77], v[4:5]
	v_pk_mul_f32 v[12:13], v[12:13], v[20:21] op_sel_hi:[1,0]
	v_pk_mul_f32 v[14:15], v[14:15], v[20:21] op_sel_hi:[1,0]
	v_pk_mul_f32 v[16:17], v[16:17], v[20:21] op_sel_hi:[1,0]
	v_pk_mul_f32 v[20:21], v[22:23], v[20:21] op_sel_hi:[1,0]
	v_mov_b32_e32 v22, v99
	v_cvt_pk_fp8_f32 v22, v14, v15
	v_pk_add_f32 v[6:7], v[70:71], v[6:7]
	v_pk_add_f32 v[2:3], v[66:67], v[2:3]
	v_mov_b32_e32 v23, v99
	v_cvt_pk_fp8_f32 v22, v12, v13 op_sel:[0,0,1]
	v_pk_mul_f32 v[6:7], v[6:7], v[18:19] op_sel_hi:[1,0]
	v_pk_mul_f32 v[2:3], v[2:3], v[18:19] op_sel_hi:[1,0]
	v_mov_b32_e32 v12, v99
	v_mov_b32_e32 v13, v99
	v_cvt_pk_fp8_f32 v23, v20, v21
	v_cvt_pk_fp8_f32 v12, v6, v7
	v_cvt_pk_fp8_f32 v13, v2, v3
	v_lshl_add_u64 v[36:37], v[34:35], 0, s[42:43]
	s_mov_b64 s[42:43], 0x10000
	v_lshl_add_u64 v[38:39], v[34:35], 0, s[42:43]
	s_mov_b64 s[42:43], 0x18000
	v_pk_add_f32 v[8:9], v[72:73], v[8:9]
	v_pk_add_f32 v[4:5], v[68:69], v[4:5]
	v_lshl_add_u64 v[40:41], v[34:35], 0, s[42:43]
	s_mov_b64 s[42:43], 0x40000
	v_pk_mul_f32 v[8:9], v[8:9], v[18:19] op_sel_hi:[1,0]
	v_pk_mul_f32 v[4:5], v[4:5], v[18:19] op_sel_hi:[1,0]
	v_lshl_add_u64 v[42:43], v[34:35], 0, s[42:43]
	s_mov_b64 s[42:43], 0x48000
	v_cvt_pk_fp8_f32 v23, v16, v17 op_sel:[0,0,1]
	v_cvt_pk_fp8_f32 v12, v8, v9 op_sel:[0,0,1]
	v_cvt_pk_fp8_f32 v13, v4, v5 op_sel:[0,0,1]
	v_lshl_add_u64 v[44:45], v[34:35], 0, s[42:43]
	s_mov_b64 s[42:43], 0x50000
	v_lshl_add_u64 v[46:47], v[34:35], 0, s[42:43]
	s_mov_b64 s[42:43], 0x58000
	v_lshl_add_u64 v[10:11], v[34:35], 0, s[42:43]
	s_mov_b64 s[42:43], -1
	s_andn2_b64 vcc, exec, s[8:9]
	global_store_dwordx2 v[34:35], v[48:49], off offset:128
	global_store_dwordx2 v[36:37], v[32:33], off offset:128
	global_store_dwordx2 v[38:39], v[30:31], off offset:128
	global_store_dwordx2 v[40:41], v[28:29], off offset:128
	global_store_dwordx2 v[42:43], v[26:27], off offset:128
	global_store_dwordx2 v[44:45], v[24:25], off offset:128
	global_store_dwordx2 v[46:47], v[22:23], off offset:128
	global_store_dwordx2 v[10:11], v[12:13], off offset:128
	s_mov_b64 s[100:101], -1
	s_cbranch_vccnz .LBB0_1501
	s_andn2_b64 vcc, exec, s[4:5]
	s_cbranch_vccnz .LBB0_1500
	s_barrier
	s_branch .LBB0_1500
